# removed dead v_mov 0 before fp8 pack pairs (104 sites), on top of v27
# speedup vs baseline: 1.0068x; 1.0005x over previous
; __device__ __forceinline__ unsigned cvt_pk_bf16(float lo, float hi) { unsigned r; asm volatile("v_cvt_pk_bf16_f32 %0, %1, %2" : "=v"(r) : "v"(lo), "v"(hi)); return r; }
; __device__ __forceinline__ unsigned pk4_fp8(float a, float b, float c, float d) {
;     a = fminf(fmaxf(a, -448.f), 448.f); b = fminf(fmaxf(b, -448.f), 448.f); c = fminf(fmaxf(c, -448.f), 448.f); d = fminf(fmaxf(d, -448.f), 448.f);
;     int p = __builtin_amdgcn_cvt_pk_fp8_f32(a, b, 0, false); p = __builtin_amdgcn_cvt_pk_fp8_f32(c, d, p, true); return (unsigned)p; }
; __device__ __forceinline__ void p0_prologue(const Ctx& C) {
;     ...
; #pragma unroll
;         for (int c = 0; c < 8; ++c) { const f32x4 g4 = *(const f32x4*)(gv + c * 256 + lane * 4); const float h0 = v[c][0] * rs * g4[0], h1 = v[c][1] * rs * g4[1], h2 = v[c][2] * rs * g4[2], h3 = v[c][3] * rs * g4[3];
;             if (!ismem) { u32x2 w; w.x = cvt_pk_bf16(h0, h1); w.y = cvt_pk_bf16(h2, h3); *(u32x2*)(dst + c * 256 + lane * 4) = w; }
;             *(unsigned*)(d8 + c * 256 + lane * 4) = pk4_fp8(h0, h1, h2, h3); }
.LBB0_77:
	v_max_f32_e32 v5, v5, v5
	v_max_f32_e32 v4, v4, v4
	v_med3_f32 v5, v5, s30, v44
	v_med3_f32 v4, v4, s30, v44
	v_cvt_pk_fp8_f32 v6, v5, v4
	v_max_f32_e32 v3, v3, v3
	v_max_f32_e32 v2, v2, v2
	v_med3_f32 v3, v3, s30, v44
	v_med3_f32 v2, v2, s30, v44
	s_add_u32 s2, s2, s10
	v_cvt_pk_fp8_f32 v6, v3, v2 op_sel:[0,0,1]
	s_addc_u32 s3, s3, s11
	s_add_u32 s12, s12, s14
	s_addc_u32 s13, s13, s15
	s_cmp_gt_i32 s2, 0x81ff
	global_store_dword v[42:43], v6, off offset:1792
	s_cbranch_scc1 .LBB0_98

; __device__ __forceinline__ unsigned cvt_pk_bf16(float lo, float hi) { unsigned r; asm volatile("v_cvt_pk_bf16_f32 %0, %1, %2" : "=v"(r) : "v"(lo), "v"(hi)); return r; }
; __device__ __forceinline__ unsigned pk4_fp8(float a, float b, float c, float d) {
;     a = fminf(fmaxf(a, -448.f), 448.f); b = fminf(fmaxf(b, -448.f), 448.f); c = fminf(fmaxf(c, -448.f), 448.f); d = fminf(fmaxf(d, -448.f), 448.f);
;     int p = __builtin_amdgcn_cvt_pk_fp8_f32(a, b, 0, false); p = __builtin_amdgcn_cvt_pk_fp8_f32(c, d, p, true); return (unsigned)p; }
; __device__ __forceinline__ void p0_prologue(const Ctx& C) {
;     ...
; #pragma unroll
;         for (int c = 0; c < 8; ++c) { const f32x4 g4 = *(const f32x4*)(gv + c * 256 + lane * 4); const float h0 = v[c][0] * rs * g4[0], h1 = v[c][1] * rs * g4[1], h2 = v[c][2] * rs * g4[2], h3 = v[c][3] * rs * g4[3];
;             if (!ismem) { u32x2 w; w.x = cvt_pk_bf16(h0, h1); w.y = cvt_pk_bf16(h2, h3); *(u32x2*)(dst + c * 256 + lane * 4) = w; }
;             *(unsigned*)(d8 + c * 256 + lane * 4) = pk4_fp8(h0, h1, h2, h3); }
.LBB0_84:
	v_max_f32_e32 v47, v47, v47
	v_max_f32_e32 v46, v46, v46
	v_med3_f32 v47, v47, s30, v44
	v_med3_f32 v46, v46, s30, v44
	s_lshl_b64 s[0:1], s[20:21], 11
	s_lshl_b64 s[8:9], s[16:17], 11
	v_cvt_pk_fp8_f32 v48, v47, v46
	s_add_u32 s8, s26, s8
	s_addc_u32 s9, s27, s9
	v_max_f32_e32 v43, v43, v43
	v_max_f32_e32 v42, v42, v42
	s_add_u32 s16, s24, s0
	v_med3_f32 v43, v43, s30, v44
	v_med3_f32 v42, v42, s30, v44
	s_addc_u32 s20, s25, s1
	v_cvt_pk_fp8_f32 v48, v43, v42 op_sel:[0,0,1]
	s_and_b64 s[0:1], s[18:19], exec
	s_cselect_b32 s1, s9, s20
	s_cselect_b32 s0, s8, s16
	v_lshl_add_u64 v[42:43], s[0:1], 0, v[32:33]
	global_store_dword v[42:43], v48, off
	flat_load_dwordx4 v[46:49], v[38:39] offset:1024
	v_mul_f32_e32 v26, v26, v45
	v_mul_f32_e32 v27, v27, v45
	v_mul_f32_e32 v50, v28, v45
	v_mul_f32_e32 v51, v29, v45
	s_and_b64 vcc, exec, s[6:7]
	s_waitcnt vmcnt(0) lgkmcnt(0)
	v_mul_f32_e32 v29, v26, v46
	v_mul_f32_e32 v28, v27, v47
	v_mul_f32_e32 v27, v50, v48
	v_mul_f32_e32 v26, v51, v49
	s_cbranch_vccnz .LBB0_86
	v_cvt_pk_bf16_f32 v46, v29, v28
	v_cvt_pk_bf16_f32 v47, v27, v26
	global_store_dwordx2 v[40:41], v[46:47], off offset:512
.LBB0_86:
	v_max_f32_e32 v29, v29, v29
	v_max_f32_e32 v28, v28, v28
	v_med3_f32 v29, v29, s30, v44
	v_med3_f32 v28, v28, s30, v44
	v_cvt_pk_fp8_f32 v46, v29, v28
	v_max_f32_e32 v27, v27, v27
	v_max_f32_e32 v26, v26, v26
	v_med3_f32 v27, v27, s30, v44
	v_med3_f32 v26, v26, s30, v44
	v_cvt_pk_fp8_f32 v46, v27, v26 op_sel:[0,0,1]
	v_mul_f32_e32 v22, v22, v45
	v_mul_f32_e32 v23, v23, v45
	v_mul_f32_e32 v47, v25, v45
	global_store_dword v[42:43], v46, off offset:256
	flat_load_dwordx4 v[26:29], v[38:39] offset:2048
	v_mul_f32_e32 v46, v24, v45
	s_and_b64 vcc, exec, s[6:7]
	s_waitcnt vmcnt(0) lgkmcnt(0)
	v_mul_f32_e32 v25, v22, v26
	v_mul_f32_e32 v24, v23, v27
	v_mul_f32_e32 v23, v46, v28
	v_mul_f32_e32 v22, v47, v29
	s_cbranch_vccnz .LBB0_88
	v_cvt_pk_bf16_f32 v26, v25, v24
	v_cvt_pk_bf16_f32 v27, v23, v22
	global_store_dwordx2 v[40:41], v[26:27], off offset:1024
.LBB0_88:
	v_max_f32_e32 v25, v25, v25
	v_max_f32_e32 v24, v24, v24
	v_med3_f32 v25, v25, s30, v44
	v_med3_f32 v24, v24, s30, v44
	v_cvt_pk_fp8_f32 v26, v25, v24
	v_max_f32_e32 v23, v23, v23
	v_max_f32_e32 v22, v22, v22
	v_med3_f32 v23, v23, s30, v44
	v_med3_f32 v22, v22, s30, v44
	v_cvt_pk_fp8_f32 v26, v23, v22 op_sel:[0,0,1]
	v_mul_f32_e32 v18, v18, v45
	v_mul_f32_e32 v19, v19, v45
	v_mul_f32_e32 v27, v21, v45
	global_store_dword v[42:43], v26, off offset:512
	flat_load_dwordx4 v[22:25], v[38:39] offset:3072
	v_mul_f32_e32 v26, v20, v45
	s_and_b64 vcc, exec, s[6:7]
	s_waitcnt vmcnt(0) lgkmcnt(0)
	v_mul_f32_e32 v21, v18, v22
	v_mul_f32_e32 v20, v19, v23
	v_mul_f32_e32 v19, v26, v24
	v_mul_f32_e32 v18, v27, v25
	s_cbranch_vccnz .LBB0_90
	v_cvt_pk_bf16_f32 v22, v21, v20
	v_cvt_pk_bf16_f32 v23, v19, v18
	global_store_dwordx2 v[40:41], v[22:23], off offset:1536
.LBB0_90:
	v_max_f32_e32 v21, v21, v21
	v_max_f32_e32 v20, v20, v20
	v_med3_f32 v21, v21, s30, v44
	v_med3_f32 v20, v20, s30, v44
	v_cvt_pk_fp8_f32 v22, v21, v20
	v_max_f32_e32 v19, v19, v19
	v_max_f32_e32 v18, v18, v18
	v_med3_f32 v19, v19, s30, v44
	v_med3_f32 v18, v18, s30, v44
	v_cvt_pk_fp8_f32 v22, v19, v18 op_sel:[0,0,1]
	v_add_co_u32_e32 v18, vcc, 0x1000, v38
	v_mul_f32_e32 v14, v14, v45
	global_store_dword v[42:43], v22, off offset:768
	v_addc_co_u32_e32 v19, vcc, 0, v39, vcc
	flat_load_dwordx4 v[18:21], v[18:19]
	v_mul_f32_e32 v15, v15, v45
	v_mul_f32_e32 v22, v16, v45
	v_mul_f32_e32 v23, v17, v45
	s_and_b64 vcc, exec, s[6:7]
	s_waitcnt vmcnt(0) lgkmcnt(0)
	v_mul_f32_e32 v17, v14, v18
	v_mul_f32_e32 v16, v15, v19
	v_mul_f32_e32 v15, v22, v20
	v_mul_f32_e32 v14, v23, v21
	s_cbranch_vccnz .LBB0_92
	v_cvt_pk_bf16_f32 v18, v17, v16
	v_cvt_pk_bf16_f32 v19, v15, v14
	global_store_dwordx2 v[40:41], v[18:19], off offset:2048
.LBB0_92:
	v_max_f32_e32 v17, v17, v17
	v_max_f32_e32 v16, v16, v16
	v_med3_f32 v17, v17, s30, v44
	v_med3_f32 v16, v16, s30, v44
	v_cvt_pk_fp8_f32 v18, v17, v16
	v_max_f32_e32 v15, v15, v15
	v_max_f32_e32 v14, v14, v14
	v_med3_f32 v15, v15, s30, v44
	v_med3_f32 v14, v14, s30, v44
	v_cvt_pk_fp8_f32 v18, v15, v14 op_sel:[0,0,1]
	v_add_co_u32_e32 v14, vcc, s28, v38
	v_mul_f32_e32 v10, v10, v45
	global_store_dword v[42:43], v18, off offset:1024
	v_addc_co_u32_e32 v15, vcc, 0, v39, vcc
	flat_load_dwordx4 v[16:19], v[14:15] offset:1024
	v_mul_f32_e32 v11, v11, v45
	v_mul_f32_e32 v20, v12, v45
	v_mul_f32_e32 v21, v13, v45
	s_and_b64 vcc, exec, s[6:7]
	s_waitcnt vmcnt(0) lgkmcnt(0)
	v_mul_f32_e32 v13, v10, v16
	v_mul_f32_e32 v12, v11, v17
	v_mul_f32_e32 v11, v20, v18
	v_mul_f32_e32 v10, v21, v19
	s_cbranch_vccnz .LBB0_94
	v_cvt_pk_bf16_f32 v16, v13, v12
	v_cvt_pk_bf16_f32 v17, v11, v10
	global_store_dwordx2 v[40:41], v[16:17], off offset:2560
.LBB0_94:
	v_max_f32_e32 v13, v13, v13
	v_max_f32_e32 v12, v12, v12
	v_med3_f32 v13, v13, s30, v44
	v_med3_f32 v12, v12, s30, v44
	v_cvt_pk_fp8_f32 v16, v13, v12
	v_max_f32_e32 v11, v11, v11
	v_max_f32_e32 v10, v10, v10
	v_med3_f32 v11, v11, s30, v44
	v_med3_f32 v10, v10, s30, v44
	v_cvt_pk_fp8_f32 v16, v11, v10 op_sel:[0,0,1]
	v_mul_f32_e32 v6, v6, v45
	v_mul_f32_e32 v7, v7, v45
	s_and_b64 vcc, exec, s[6:7]
	global_store_dword v[42:43], v16, off offset:1280
	flat_load_dwordx4 v[10:13], v[14:15] offset:2048
	v_mul_f32_e32 v14, v8, v45
	v_mul_f32_e32 v15, v9, v45
	s_waitcnt vmcnt(0) lgkmcnt(0)
	v_mul_f32_e32 v9, v6, v10
	v_mul_f32_e32 v8, v7, v11
	v_mul_f32_e32 v7, v14, v12
	v_mul_f32_e32 v6, v15, v13
	s_cbranch_vccnz .LBB0_96
	v_cvt_pk_bf16_f32 v10, v9, v8
	v_cvt_pk_bf16_f32 v11, v7, v6
	global_store_dwordx2 v[40:41], v[10:11], off offset:3072
.LBB0_96:
	v_max_f32_e32 v9, v9, v9
	v_max_f32_e32 v8, v8, v8
	v_med3_f32 v9, v9, s30, v44
	v_med3_f32 v8, v8, s30, v44
	v_cvt_pk_fp8_f32 v10, v9, v8
	v_max_f32_e32 v7, v7, v7
	v_max_f32_e32 v6, v6, v6
	v_med3_f32 v7, v7, s30, v44
	v_med3_f32 v6, v6, s30, v44
	v_cvt_pk_fp8_f32 v10, v7, v6 op_sel:[0,0,1]
	v_add_co_u32_e32 v6, vcc, 0x1000, v38
	v_mul_f32_e32 v2, v2, v45
	global_store_dword v[42:43], v10, off offset:1536
	v_addc_co_u32_e32 v7, vcc, 0, v39, vcc
	flat_load_dwordx4 v[6:9], v[6:7] offset:3072
	v_mul_f32_e32 v3, v3, v45
	v_mul_f32_e32 v10, v4, v45
	v_mul_f32_e32 v11, v5, v45
	s_and_b64 vcc, exec, s[6:7]
	s_waitcnt vmcnt(0) lgkmcnt(0)
	v_mul_f32_e32 v5, v2, v6
	v_mul_f32_e32 v4, v3, v7
	v_mul_f32_e32 v3, v10, v8
	v_mul_f32_e32 v2, v11, v9
	s_cbranch_vccnz .LBB0_77
	v_cvt_pk_bf16_f32 v6, v5, v4
	v_cvt_pk_bf16_f32 v7, v3, v2
	global_store_dwordx2 v[40:41], v[6:7], off offset:3584
	s_branch .LBB0_77

; #define LAS __attribute__((address_space(3)))
; #define TB_LOAD(R_, t_) do { const int _t = (t_); if (_t < tot) { const int _b = _t / per, _r = _t % per; ttb_load(R_, src + (size_t)_b * K_ * N_, N_, (_r % kt) * 128, (_r / kt) * 64, C.tid); } } while (0)
; __device__ __forceinline__ void ttb_load(TReg& R, const float* src, int ld, int k0, int n0, int tid) {
;     const int kr = tid >> 4, nq = tid & 15;
; #pragma unroll
;     for (int rep = 0; rep < 4; ++rep) R.v[rep] = __builtin_nontemporal_load((const f32x4*)(src + (size_t)(k0 + 4 * kr + rep) * ld + n0 + 4 * nq)); }
; __device__ __forceinline__ void ttb_put(const TReg& R, LAS unsigned* tile, int tid) {
;     const int kr = tid >> 4, nq = tid & 15;
; #pragma unroll
;     for (int c = 0; c < 4; ++c) { const int n = 4 * nq + c;
;         tile[n * 32 + (kr ^ (n & 31))] = pk4_fp8(R.v[0][c] * W_FP8_SCALE, R.v[1][c] * W_FP8_SCALE, R.v[2][c] * W_FP8_SCALE, R.v[3][c] * W_FP8_SCALE); } }
; __device__ __forceinline__ void ttb_finish(LAS const unsigned* tile, unsigned char* dst, int ldd, int k0, int n0, int map, int tid) {
;     const int n = tid >> 3, kq = tid & 7, m = n & 31, ns = n0 + n; int r = ns;
;     if (map == 2) { const int j = ns >> 1, par = ns & 1; r = 256 * (j >> 7) + 128 * par + (j & 127); }
;     const u32x4 g = *(LAS const u32x4*)(tile + n * 32 + 4 * (kq ^ (m >> 2)));
;     const unsigned a0 = (m & 1) ? g.y : g.x, a1 = (m & 1) ? g.x : g.y, a2 = (m & 1) ? g.w : g.z, a3 = (m & 1) ? g.z : g.w;
;     u32x4 w; w.x = (m & 2) ? a2 : a0; w.y = (m & 2) ? a3 : a1; w.z = (m & 2) ? a0 : a2; w.w = (m & 2) ? a1 : a3;
;     __builtin_nontemporal_store(w, (u32x4*)(dst + (size_t)r * ldd + k0 + 16 * kq));
; }
; template <int K_, int N_, int MAP_> __device__ __forceinline__ void tjob_b(const Ctx& C, int bid, int G, const float* src, unsigned char* dstb, int nbatch) {
;     constexpr int kt = K_ / 128, ntile = N_ / 64, per = kt * ntile; const int tot = per * nbatch;
;     TReg R0, R1, R2, R3; int kbuf = 0;
;     ...
;     TB_LOAD(R0, bid); TB_LOAD(R1, bid + G); TB_LOAD(R2, bid + 2 * G); TB_LOAD(R3, bid + 3 * G);
;     for (int t = bid; t < tot; t += 4 * G) { TB_STEP(R0, t); TB_STEP(R1, t + G); TB_STEP(R2, t + 2 * G); TB_STEP(R3, t + 3 * G); }
.LBB0_189:
	s_waitcnt vmcnt(0) lgkmcnt(0)
	v_mul_f32_e32 v72, 0x43800000, v2
	v_mul_f32_e32 v93, 0x43800000, v6
	v_med3_f32 v72, v72, s31, v87
	v_med3_f32 v93, v93, s31, v87
	v_cvt_pk_fp8_f32 v95, v72, v93
	v_mul_f32_e32 v94, 0x43800000, v10
	v_mul_f32_e32 v72, 0x43800000, v14
	v_med3_f32 v93, v94, s31, v87
	v_med3_f32 v72, v72, s31, v87
	v_cvt_pk_fp8_f32 v95, v93, v72 op_sel:[0,0,1]
	v_mul_f32_e32 v72, 0x43800000, v3
	v_mul_f32_e32 v93, 0x43800000, v7
	v_med3_f32 v72, v72, s31, v87
	v_med3_f32 v93, v93, s31, v87
	v_cvt_pk_fp8_f32 v96, v72, v93
	v_mul_f32_e32 v94, 0x43800000, v11
	v_mul_f32_e32 v72, 0x43800000, v15
	v_med3_f32 v93, v94, s31, v87
	v_med3_f32 v72, v72, s31, v87
	s_lshl_b32 s12, s27, 13
	v_cvt_pk_fp8_f32 v96, v93, v72 op_sel:[0,0,1]
	s_add_i32 s35, s12, 0
	v_add3_u32 v72, s35, v80, v88
	ds_write_b32 v72, v95
	v_add3_u32 v72, s35, v81, v89
	ds_write_b32 v72, v96
	v_mul_f32_e32 v72, 0x43800000, v4
	v_mul_f32_e32 v93, 0x43800000, v8
	v_med3_f32 v72, v72, s31, v87
	v_med3_f32 v93, v93, s31, v87
	v_cvt_pk_fp8_f32 v95, v72, v93
	v_mul_f32_e32 v94, 0x43800000, v12
	v_mul_f32_e32 v72, 0x43800000, v16
	v_med3_f32 v93, v94, s31, v87
	v_med3_f32 v72, v72, s31, v87
	v_cvt_pk_fp8_f32 v95, v93, v72 op_sel:[0,0,1]
	v_mul_f32_e32 v72, 0x43800000, v5
	v_mul_f32_e32 v93, 0x43800000, v9
	v_med3_f32 v72, v72, s31, v87
	v_med3_f32 v93, v93, s31, v87
	v_cvt_pk_fp8_f32 v96, v72, v93
	v_mul_f32_e32 v94, 0x43800000, v13
	v_mul_f32_e32 v72, 0x43800000, v17
	v_med3_f32 v93, v94, s31, v87
	v_med3_f32 v72, v72, s31, v87
	v_cvt_pk_fp8_f32 v96, v93, v72 op_sel:[0,0,1]
	s_add_i32 s33, s34, s16
	s_cmpk_gt_i32 s33, 0x7fff
	v_add3_u32 v72, s35, v82, v90
	s_cselect_b64 s[12:13], -1, 0
	ds_write_b32 v72, v95
	v_add3_u32 v72, s35, v83, v91
	s_and_b64 vcc, exec, s[12:13]
	ds_write_b32 v72, v96
	s_cbranch_vccnz .LBB0_191
	s_ashr_i32 s36, s33, 31
	s_lshr_b32 s36, s36, 22
	s_add_i32 s37, s33, s36
	s_ashr_i32 s36, s37, 10
	s_and_b32 s37, s37, 0xfc00
	s_sub_i32 s38, s33, s37
	s_ashr_i32 s37, s36, 31
	s_lshl_b64 s[36:37], s[36:37], 25
	v_lshl_add_u64 v[2:3], v[66:67], 0, s[36:37]
	s_sext_i32_i16 s36, s38
	s_bfe_u32 s36, s36, 0x4001b
	s_add_i32 s36, s38, s36
	s_sext_i32_i16 s37, s36
	s_and_b32 s36, s36, 0xfff0
	s_sub_i32 s36, s38, s36
	s_sext_i32_i16 s38, s36
	s_lshl_b32 s36, s37, 2
	s_andn2_b32 s36, s36, 63
	v_lshl_add_u32 v10, s38, 7, v86
	s_ashr_i32 s37, s36, 31
	v_lshl_add_u64 v[2:3], s[36:37], 2, v[2:3]
	v_lshlrev_b32_e32 v72, 2, v68
	v_ashrrev_i32_e32 v11, 31, v10
	v_lshl_add_u64 v[12:13], v[2:3], 0, v[72:73]
	v_lshlrev_b64 v[2:3], 14, v[10:11]
	v_or_b32_e32 v4, 1, v10
	v_or_b32_e32 v14, 2, v10
	v_or_b32_e32 v10, 3, v10
	v_ashrrev_i32_e32 v5, 31, v4
	v_ashrrev_i32_e32 v15, 31, v14
	v_ashrrev_i32_e32 v11, 31, v10
	v_lshlrev_b64 v[4:5], 14, v[4:5]
	v_lshlrev_b64 v[14:15], 14, v[14:15]
	v_lshlrev_b64 v[10:11], 14, v[10:11]
	v_lshl_add_u64 v[2:3], v[12:13], 0, v[2:3]
	v_lshl_add_u64 v[6:7], v[12:13], 0, v[4:5]
	v_lshl_add_u64 v[14:15], v[12:13], 0, v[14:15]
	v_lshl_add_u64 v[16:17], v[12:13], 0, v[10:11]
	flat_load_dwordx4 v[2:5], v[2:3] nt
	s_nop 0
	flat_load_dwordx4 v[6:9], v[6:7] nt
	s_nop 0
	flat_load_dwordx4 v[10:13], v[14:15] nt
	s_nop 0
	flat_load_dwordx4 v[14:17], v[16:17] nt
; #define LAS __attribute__((address_space(3)))
; #define TB_LOAD(R_, t_) do { const int _t = (t_); if (_t < tot) { const int _b = _t / per, _r = _t % per; ttb_load(R_, src + (size_t)_b * K_ * N_, N_, (_r % kt) * 128, (_r / kt) * 64, C.tid); } } while (0)
; __device__ __forceinline__ void ttb_load(TReg& R, const float* src, int ld, int k0, int n0, int tid) {
;     const int kr = tid >> 4, nq = tid & 15;
; #pragma unroll
;     for (int rep = 0; rep < 4; ++rep) R.v[rep] = __builtin_nontemporal_load((const f32x4*)(src + (size_t)(k0 + 4 * kr + rep) * ld + n0 + 4 * nq)); }
; __device__ __forceinline__ void ttb_put(const TReg& R, LAS unsigned* tile, int tid) {
;     const int kr = tid >> 4, nq = tid & 15;
; #pragma unroll
;     for (int c = 0; c < 4; ++c) { const int n = 4 * nq + c;
;         tile[n * 32 + (kr ^ (n & 31))] = pk4_fp8(R.v[0][c] * W_FP8_SCALE, R.v[1][c] * W_FP8_SCALE, R.v[2][c] * W_FP8_SCALE, R.v[3][c] * W_FP8_SCALE); } }
; __device__ __forceinline__ void ttb_finish(LAS const unsigned* tile, unsigned char* dst, int ldd, int k0, int n0, int map, int tid) {
;     const int n = tid >> 3, kq = tid & 7, m = n & 31, ns = n0 + n; int r = ns;
;     if (map == 2) { const int j = ns >> 1, par = ns & 1; r = 256 * (j >> 7) + 128 * par + (j & 127); }
;     const u32x4 g = *(LAS const u32x4*)(tile + n * 32 + 4 * (kq ^ (m >> 2)));
;     const unsigned a0 = (m & 1) ? g.y : g.x, a1 = (m & 1) ? g.x : g.y, a2 = (m & 1) ? g.w : g.z, a3 = (m & 1) ? g.z : g.w;
;     u32x4 w; w.x = (m & 2) ? a2 : a0; w.y = (m & 2) ? a3 : a1; w.z = (m & 2) ? a0 : a2; w.w = (m & 2) ? a1 : a3;
;     __builtin_nontemporal_store(w, (u32x4*)(dst + (size_t)r * ldd + k0 + 16 * kq));
; }
; template <int K_, int N_, int MAP_> __device__ __forceinline__ void tjob_b(const Ctx& C, int bid, int G, const float* src, unsigned char* dstb, int nbatch) {
;     constexpr int kt = K_ / 128, ntile = N_ / 64, per = kt * ntile; const int tot = per * nbatch;
;     TReg R0, R1, R2, R3; int kbuf = 0;
;     ...
;     TB_LOAD(R0, bid); TB_LOAD(R1, bid + G); TB_LOAD(R2, bid + 2 * G); TB_LOAD(R3, bid + 3 * G);
;     for (int t = bid; t < tot; t += 4 * G) { TB_STEP(R0, t); TB_STEP(R1, t + G); TB_STEP(R2, t + 2 * G); TB_STEP(R3, t + 3 * G); }
.LBB0_191:
	s_ashr_i32 s36, s34, 31
	s_lshr_b32 s36, s36, 22
	s_add_i32 s37, s34, s36
	s_ashr_i32 s36, s37, 10
	s_and_b32 s37, s37, 0xfc00
	s_sub_i32 s38, s34, s37
	s_ashr_i32 s37, s36, 31
	s_lshl_b64 s[36:37], s[36:37], 23
	s_add_u32 s36, s25, s36
	s_sext_i32_i16 s39, s38
	s_addc_u32 s37, s26, s37
	s_bfe_u32 s39, s39, 0x4001b
	s_add_i32 s39, s38, s39
	v_add3_u32 v72, s35, v84, v92
	s_waitcnt lgkmcnt(0)
	s_barrier
	s_sext_i32_i16 s40, s39
	s_and_b32 s39, s39, 0xfff0
	ds_read_b128 v[94:97], v72
	s_sub_i32 s38, s38, s39
	s_lshl_b32 s39, s40, 2
	s_andn2_b32 s39, s39, 63
	v_add_u32_e32 v72, s39, v1
	v_and_b32_e32 v93, 0xffffff00, v72
	v_bfe_u32 v72, v72, 1, 7
	v_or3_b32 v98, v93, v72, v85
	s_waitcnt lgkmcnt(0)
	v_cndmask_b32_e64 v72, v95, v94, s[6:7]
	v_cndmask_b32_e64 v99, v97, v96, s[6:7]
	s_sext_i32_i16 s38, s38
	v_cndmask_b32_e64 v93, v94, v95, s[6:7]
	v_cndmask_b32_e64 v97, v96, v97, s[6:7]
	v_cndmask_b32_e64 v94, v99, v72, s[8:9]
	v_cndmask_b32_e64 v96, v72, v99, s[8:9]
	v_ashrrev_i32_e32 v99, 31, v98
	s_lshl_b32 s38, s38, 7
	v_lshlrev_b64 v[98:99], 11, v[98:99]
	v_lshl_add_u64 v[98:99], s[36:37], 0, v[98:99]
	s_ashr_i32 s39, s38, 31
	v_lshl_add_u64 v[98:99], v[98:99], 0, s[38:39]
	s_xor_b32 s36, s27, 1
	s_add_i32 s35, s0, s34
	v_cndmask_b32_e64 v95, v97, v93, s[8:9]
	v_cndmask_b32_e64 v97, v93, v97, s[8:9]
	v_lshl_add_u64 v[98:99], v[98:99], 0, v[70:71]
	s_cmpk_gt_i32 s35, 0x7fff
	global_store_dwordx4 v[98:99], v[94:97], off nt
	s_cbranch_scc1 .LBB0_195
	v_mul_f32_e32 v72, 0x43800000, v18
	v_mul_f32_e32 v93, 0x43800000, v22
	v_med3_f32 v72, v72, s31, v87
	v_med3_f32 v93, v93, s31, v87
	v_cvt_pk_fp8_f32 v95, v72, v93
	v_mul_f32_e32 v94, 0x43800000, v26
	v_mul_f32_e32 v72, 0x43800000, v30
	v_med3_f32 v93, v94, s31, v87
	v_med3_f32 v72, v72, s31, v87
	v_cvt_pk_fp8_f32 v95, v93, v72 op_sel:[0,0,1]
	s_lshl_b32 s36, s36, 13
	s_add_i32 s36, s36, 0
	v_add3_u32 v72, s36, v80, v88
	ds_write_b32 v72, v95
	v_mul_f32_e32 v72, 0x43800000, v19
	v_mul_f32_e32 v93, 0x43800000, v23
	v_med3_f32 v72, v72, s31, v87
	v_med3_f32 v93, v93, s31, v87
	v_cvt_pk_fp8_f32 v95, v72, v93
	v_mul_f32_e32 v94, 0x43800000, v27
	v_mul_f32_e32 v72, 0x43800000, v31
	v_med3_f32 v93, v94, s31, v87
	v_med3_f32 v72, v72, s31, v87
	v_cvt_pk_fp8_f32 v95, v93, v72 op_sel:[0,0,1]
	v_mul_f32_e32 v72, 0x43800000, v20
	v_mul_f32_e32 v93, 0x43800000, v24
	v_med3_f32 v72, v72, s31, v87
	v_med3_f32 v93, v93, s31, v87
	v_cvt_pk_fp8_f32 v96, v72, v93
	v_mul_f32_e32 v94, 0x43800000, v28
	v_mul_f32_e32 v72, 0x43800000, v32
	v_med3_f32 v93, v94, s31, v87
	v_med3_f32 v72, v72, s31, v87
	v_cvt_pk_fp8_f32 v96, v93, v72 op_sel:[0,0,1]
	v_add3_u32 v72, s36, v81, v89
	ds_write_b32 v72, v95
	v_add3_u32 v72, s36, v82, v90
	ds_write_b32 v72, v96
	v_mul_f32_e32 v72, 0x43800000, v21
	v_mul_f32_e32 v93, 0x43800000, v25
	v_med3_f32 v72, v72, s31, v87
	v_med3_f32 v93, v93, s31, v87
	v_cvt_pk_fp8_f32 v95, v72, v93
	v_mul_f32_e32 v94, 0x43800000, v29
	v_mul_f32_e32 v72, 0x43800000, v33
	v_med3_f32 v93, v94, s31, v87
	v_med3_f32 v72, v72, s31, v87
	v_cvt_pk_fp8_f32 v95, v93, v72 op_sel:[0,0,1]
	s_add_i32 s37, s19, s34
	v_add3_u32 v72, s36, v83, v91
	s_cmpk_gt_i32 s37, 0x7fff
	ds_write_b32 v72, v95
	s_cbranch_scc1 .LBB0_194
	s_ashr_i32 s38, s37, 31
	s_lshr_b32 s38, s38, 22
	s_add_i32 s39, s37, s38
	s_ashr_i32 s38, s39, 10
	s_and_b32 s39, s39, 0xfc00
	s_sub_i32 s37, s37, s39
	s_ashr_i32 s39, s38, 31
	s_lshl_b64 s[38:39], s[38:39], 25
	v_lshl_add_u64 v[18:19], v[66:67], 0, s[38:39]
	s_sext_i32_i16 s38, s37
	s_bfe_u32 s38, s38, 0x4001b
	s_add_i32 s38, s37, s38
	s_sext_i32_i16 s39, s38
	s_and_b32 s38, s38, 0xfff0
	s_sub_i32 s37, s37, s38
	s_lshl_b32 s38, s39, 2
	s_sext_i32_i16 s37, s37
	s_andn2_b32 s38, s38, 63
	v_lshl_add_u32 v26, s37, 7, v86
	s_ashr_i32 s39, s38, 31
	v_lshl_add_u64 v[18:19], s[38:39], 2, v[18:19]
	v_lshlrev_b32_e32 v72, 2, v68
	v_ashrrev_i32_e32 v27, 31, v26
	v_lshl_add_u64 v[28:29], v[18:19], 0, v[72:73]
	v_lshlrev_b64 v[18:19], 14, v[26:27]
	v_or_b32_e32 v20, 1, v26
	v_or_b32_e32 v30, 2, v26
	v_or_b32_e32 v26, 3, v26
	v_ashrrev_i32_e32 v21, 31, v20
	v_ashrrev_i32_e32 v31, 31, v30
	v_ashrrev_i32_e32 v27, 31, v26
	v_lshlrev_b64 v[20:21], 14, v[20:21]
	v_lshlrev_b64 v[30:31], 14, v[30:31]
	v_lshlrev_b64 v[26:27], 14, v[26:27]
	v_lshl_add_u64 v[18:19], v[28:29], 0, v[18:19]
	v_lshl_add_u64 v[22:23], v[28:29], 0, v[20:21]
	v_lshl_add_u64 v[30:31], v[28:29], 0, v[30:31]
	v_lshl_add_u64 v[32:33], v[28:29], 0, v[26:27]
	flat_load_dwordx4 v[18:21], v[18:19] nt
	s_nop 0
	flat_load_dwordx4 v[22:25], v[22:23] nt
	s_nop 0
	flat_load_dwordx4 v[26:29], v[30:31] nt
	s_nop 0
	flat_load_dwordx4 v[30:33], v[32:33] nt

; #define LAS __attribute__((address_space(3)))
; #define TB_LOAD(R_, t_) do { const int _t = (t_); if (_t < tot) { const int _b = _t / per, _r = _t % per; ttb_load(R_, src + (size_t)_b * K_ * N_, N_, (_r % kt) * 128, (_r / kt) * 64, C.tid); } } while (0)
; __device__ __forceinline__ void ttb_load(TReg& R, const float* src, int ld, int k0, int n0, int tid) {
;     const int kr = tid >> 4, nq = tid & 15;
; #pragma unroll
;     for (int rep = 0; rep < 4; ++rep) R.v[rep] = __builtin_nontemporal_load((const f32x4*)(src + (size_t)(k0 + 4 * kr + rep) * ld + n0 + 4 * nq)); }
; __device__ __forceinline__ void ttb_put(const TReg& R, LAS unsigned* tile, int tid) {
;     const int kr = tid >> 4, nq = tid & 15;
; #pragma unroll
;     for (int c = 0; c < 4; ++c) { const int n = 4 * nq + c;
;         tile[n * 32 + (kr ^ (n & 31))] = pk4_fp8(R.v[0][c] * W_FP8_SCALE, R.v[1][c] * W_FP8_SCALE, R.v[2][c] * W_FP8_SCALE, R.v[3][c] * W_FP8_SCALE); } }
; __device__ __forceinline__ void ttb_finish(LAS const unsigned* tile, unsigned char* dst, int ldd, int k0, int n0, int map, int tid) {
;     const int n = tid >> 3, kq = tid & 7, m = n & 31, ns = n0 + n; int r = ns;
;     if (map == 2) { const int j = ns >> 1, par = ns & 1; r = 256 * (j >> 7) + 128 * par + (j & 127); }
;     const u32x4 g = *(LAS const u32x4*)(tile + n * 32 + 4 * (kq ^ (m >> 2)));
;     const unsigned a0 = (m & 1) ? g.y : g.x, a1 = (m & 1) ? g.x : g.y, a2 = (m & 1) ? g.w : g.z, a3 = (m & 1) ? g.z : g.w;
;     u32x4 w; w.x = (m & 2) ? a2 : a0; w.y = (m & 2) ? a3 : a1; w.z = (m & 2) ? a0 : a2; w.w = (m & 2) ? a1 : a3;
;     __builtin_nontemporal_store(w, (u32x4*)(dst + (size_t)r * ldd + k0 + 16 * kq));
; }
; template <int K_, int N_, int MAP_> __device__ __forceinline__ void tjob_b(const Ctx& C, int bid, int G, const float* src, unsigned char* dstb, int nbatch) {
;     constexpr int kt = K_ / 128, ntile = N_ / 64, per = kt * ntile; const int tot = per * nbatch;
;     TReg R0, R1, R2, R3; int kbuf = 0;
;     ...
;     TB_LOAD(R0, bid); TB_LOAD(R1, bid + G); TB_LOAD(R2, bid + 2 * G); TB_LOAD(R3, bid + 3 * G);
;     for (int t = bid; t < tot; t += 4 * G) { TB_STEP(R0, t); TB_STEP(R1, t + G); TB_STEP(R2, t + 2 * G); TB_STEP(R3, t + 3 * G); }
.LBB0_196:
	v_mul_f32_e32 v72, 0x43800000, v34
	v_mul_f32_e32 v93, 0x43800000, v38
	v_med3_f32 v72, v72, s31, v87
	v_med3_f32 v93, v93, s31, v87
	v_cvt_pk_fp8_f32 v95, v72, v93
	v_mul_f32_e32 v94, 0x43800000, v42
	v_mul_f32_e32 v72, 0x43800000, v46
	v_med3_f32 v93, v94, s31, v87
	v_med3_f32 v72, v72, s31, v87
	v_cvt_pk_fp8_f32 v95, v93, v72 op_sel:[0,0,1]
	s_lshl_b32 s35, s27, 13
	s_add_i32 s35, s35, 0
	v_add3_u32 v72, s35, v80, v88
	ds_write_b32 v72, v95
	v_mul_f32_e32 v72, 0x43800000, v35
	v_mul_f32_e32 v93, 0x43800000, v39
	v_med3_f32 v72, v72, s31, v87
	v_med3_f32 v93, v93, s31, v87
	v_cvt_pk_fp8_f32 v95, v72, v93
	v_mul_f32_e32 v94, 0x43800000, v43
	v_mul_f32_e32 v72, 0x43800000, v47
	v_med3_f32 v93, v94, s31, v87
	v_med3_f32 v72, v72, s31, v87
	v_cvt_pk_fp8_f32 v95, v93, v72 op_sel:[0,0,1]
	v_mul_f32_e32 v72, 0x43800000, v36
	v_mul_f32_e32 v93, 0x43800000, v40
	v_med3_f32 v72, v72, s31, v87
	v_med3_f32 v93, v93, s31, v87
	v_cvt_pk_fp8_f32 v96, v72, v93
	v_mul_f32_e32 v94, 0x43800000, v44
	v_mul_f32_e32 v72, 0x43800000, v48
	v_med3_f32 v93, v94, s31, v87
	v_med3_f32 v72, v72, s31, v87
	v_cvt_pk_fp8_f32 v96, v93, v72 op_sel:[0,0,1]
	v_add3_u32 v72, s35, v81, v89
	ds_write_b32 v72, v95
	v_add3_u32 v72, s35, v82, v90
	ds_write_b32 v72, v96
	v_mul_f32_e32 v72, 0x43800000, v37
	v_mul_f32_e32 v93, 0x43800000, v41
	v_med3_f32 v72, v72, s31, v87
	v_med3_f32 v93, v93, s31, v87
	v_cvt_pk_fp8_f32 v95, v72, v93
	v_mul_f32_e32 v94, 0x43800000, v45
	v_mul_f32_e32 v72, 0x43800000, v49
	v_med3_f32 v93, v94, s31, v87
	v_med3_f32 v72, v72, s31, v87
	v_cvt_pk_fp8_f32 v95, v93, v72 op_sel:[0,0,1]
	s_add_i32 s37, s18, s34
	v_add3_u32 v72, s35, v83, v91
	s_cmpk_gt_i32 s37, 0x7fff
	ds_write_b32 v72, v95
	s_cbranch_scc1 .LBB0_198
	s_ashr_i32 s38, s37, 31
	s_lshr_b32 s38, s38, 22
	s_add_i32 s39, s37, s38
	s_ashr_i32 s38, s39, 10
	s_and_b32 s39, s39, 0xfc00
	s_sub_i32 s37, s37, s39
	s_ashr_i32 s39, s38, 31
	s_lshl_b64 s[38:39], s[38:39], 25
	v_lshl_add_u64 v[34:35], v[66:67], 0, s[38:39]
	s_sext_i32_i16 s38, s37
	s_bfe_u32 s38, s38, 0x4001b
	s_add_i32 s38, s37, s38
	s_sext_i32_i16 s39, s38
	s_and_b32 s38, s38, 0xfff0
	s_sub_i32 s37, s37, s38
	s_lshl_b32 s38, s39, 2
	s_sext_i32_i16 s37, s37
	s_andn2_b32 s38, s38, 63
	v_lshl_add_u32 v42, s37, 7, v86
	s_ashr_i32 s39, s38, 31
	v_lshl_add_u64 v[34:35], s[38:39], 2, v[34:35]
	v_lshlrev_b32_e32 v72, 2, v68
	v_ashrrev_i32_e32 v43, 31, v42
	v_lshl_add_u64 v[44:45], v[34:35], 0, v[72:73]
	v_lshlrev_b64 v[34:35], 14, v[42:43]
	v_or_b32_e32 v36, 1, v42
	v_or_b32_e32 v46, 2, v42
	v_or_b32_e32 v42, 3, v42
	v_ashrrev_i32_e32 v37, 31, v36
	v_ashrrev_i32_e32 v47, 31, v46
	v_ashrrev_i32_e32 v43, 31, v42
	v_lshlrev_b64 v[36:37], 14, v[36:37]
	v_lshlrev_b64 v[46:47], 14, v[46:47]
	v_lshlrev_b64 v[42:43], 14, v[42:43]
	v_lshl_add_u64 v[34:35], v[44:45], 0, v[34:35]
	v_lshl_add_u64 v[38:39], v[44:45], 0, v[36:37]
	v_lshl_add_u64 v[46:47], v[44:45], 0, v[46:47]
	v_lshl_add_u64 v[48:49], v[44:45], 0, v[42:43]
	flat_load_dwordx4 v[34:37], v[34:35] nt
	s_nop 0
	flat_load_dwordx4 v[38:41], v[38:39] nt
	s_nop 0
	flat_load_dwordx4 v[42:45], v[46:47] nt
	s_nop 0
	flat_load_dwordx4 v[46:49], v[48:49] nt

; #define LAS __attribute__((address_space(3)))
; #define TB_LOAD(R_, t_) do { const int _t = (t_); if (_t < tot) { const int _b = _t / per, _r = _t % per; ttb_load(R_, src + (size_t)_b * K_ * N_, N_, (_r % kt) * 128, (_r / kt) * 64, C.tid); } } while (0)
; __device__ __forceinline__ void ttb_load(TReg& R, const float* src, int ld, int k0, int n0, int tid) {
;     const int kr = tid >> 4, nq = tid & 15;
; #pragma unroll
;     for (int rep = 0; rep < 4; ++rep) R.v[rep] = __builtin_nontemporal_load((const f32x4*)(src + (size_t)(k0 + 4 * kr + rep) * ld + n0 + 4 * nq)); }
; __device__ __forceinline__ void ttb_put(const TReg& R, LAS unsigned* tile, int tid) {
;     const int kr = tid >> 4, nq = tid & 15;
; #pragma unroll
;     for (int c = 0; c < 4; ++c) { const int n = 4 * nq + c;
;         tile[n * 32 + (kr ^ (n & 31))] = pk4_fp8(R.v[0][c] * W_FP8_SCALE, R.v[1][c] * W_FP8_SCALE, R.v[2][c] * W_FP8_SCALE, R.v[3][c] * W_FP8_SCALE); } }
; __device__ __forceinline__ void ttb_finish(LAS const unsigned* tile, unsigned char* dst, int ldd, int k0, int n0, int map, int tid) {
;     const int n = tid >> 3, kq = tid & 7, m = n & 31, ns = n0 + n; int r = ns;
;     if (map == 2) { const int j = ns >> 1, par = ns & 1; r = 256 * (j >> 7) + 128 * par + (j & 127); }
;     const u32x4 g = *(LAS const u32x4*)(tile + n * 32 + 4 * (kq ^ (m >> 2)));
;     const unsigned a0 = (m & 1) ? g.y : g.x, a1 = (m & 1) ? g.x : g.y, a2 = (m & 1) ? g.w : g.z, a3 = (m & 1) ? g.z : g.w;
;     u32x4 w; w.x = (m & 2) ? a2 : a0; w.y = (m & 2) ? a3 : a1; w.z = (m & 2) ? a0 : a2; w.w = (m & 2) ? a1 : a3;
;     __builtin_nontemporal_store(w, (u32x4*)(dst + (size_t)r * ldd + k0 + 16 * kq));
; }
; template <int K_, int N_, int MAP_> __device__ __forceinline__ void tjob_b(const Ctx& C, int bid, int G, const float* src, unsigned char* dstb, int nbatch) {
;     constexpr int kt = K_ / 128, ntile = N_ / 64, per = kt * ntile; const int tot = per * nbatch;
;     TReg R0, R1, R2, R3; int kbuf = 0;
;     ...
;     TB_LOAD(R0, bid); TB_LOAD(R1, bid + G); TB_LOAD(R2, bid + 2 * G); TB_LOAD(R3, bid + 3 * G);
;     for (int t = bid; t < tot; t += 4 * G) { TB_STEP(R0, t); TB_STEP(R1, t + G); TB_STEP(R2, t + 2 * G); TB_STEP(R3, t + 3 * G); }
.LBB0_199:
	s_add_i32 s36, s15, s34
	s_cmpk_gt_i32 s36, 0x7fff
	s_cbranch_scc1 .LBB0_188
	v_mul_f32_e32 v72, 0x43800000, v50
	v_mul_f32_e32 v93, 0x43800000, v54
	v_med3_f32 v72, v72, s31, v87
	v_med3_f32 v93, v93, s31, v87
	v_cvt_pk_fp8_f32 v95, v72, v93
	v_mul_f32_e32 v94, 0x43800000, v58
	v_mul_f32_e32 v72, 0x43800000, v62
	v_med3_f32 v93, v94, s31, v87
	v_med3_f32 v72, v72, s31, v87
	v_cvt_pk_fp8_f32 v95, v93, v72 op_sel:[0,0,1]
	s_lshl_b32 s35, s27, 13
	s_add_i32 s35, s35, 0
	v_add3_u32 v72, s35, v80, v88
	ds_write_b32 v72, v95
	v_mul_f32_e32 v72, 0x43800000, v51
	v_mul_f32_e32 v93, 0x43800000, v55
	v_med3_f32 v72, v72, s31, v87
	v_med3_f32 v93, v93, s31, v87
	v_cvt_pk_fp8_f32 v95, v72, v93
	v_mul_f32_e32 v94, 0x43800000, v59
	v_mul_f32_e32 v72, 0x43800000, v63
	v_med3_f32 v93, v94, s31, v87
	v_med3_f32 v72, v72, s31, v87
	v_cvt_pk_fp8_f32 v95, v93, v72 op_sel:[0,0,1]
	v_mul_f32_e32 v72, 0x43800000, v52
	v_mul_f32_e32 v93, 0x43800000, v56
	v_med3_f32 v72, v72, s31, v87
	v_med3_f32 v93, v93, s31, v87
	v_cvt_pk_fp8_f32 v96, v72, v93
	v_mul_f32_e32 v94, 0x43800000, v60
	v_mul_f32_e32 v72, 0x43800000, v64
	v_med3_f32 v93, v94, s31, v87
	v_med3_f32 v72, v72, s31, v87
	v_cvt_pk_fp8_f32 v96, v93, v72 op_sel:[0,0,1]
	v_add3_u32 v72, s35, v81, v89
	ds_write_b32 v72, v95
	v_add3_u32 v72, s35, v82, v90
	ds_write_b32 v72, v96
	v_mul_f32_e32 v72, 0x43800000, v53
	v_mul_f32_e32 v93, 0x43800000, v57
	v_med3_f32 v72, v72, s31, v87
	v_med3_f32 v93, v93, s31, v87
	v_cvt_pk_fp8_f32 v95, v72, v93
	v_mul_f32_e32 v94, 0x43800000, v61
	v_mul_f32_e32 v72, 0x43800000, v65
	v_med3_f32 v93, v94, s31, v87
	v_med3_f32 v72, v72, s31, v87
	v_cvt_pk_fp8_f32 v95, v93, v72 op_sel:[0,0,1]
	s_add_i32 s34, s17, s34
	v_add3_u32 v72, s35, v83, v91
	s_cmpk_gt_i32 s34, 0x7fff
	ds_write_b32 v72, v95
	s_cbranch_scc1 .LBB0_187
	s_ashr_i32 s37, s34, 31
	s_lshr_b32 s37, s37, 22
	s_add_i32 s37, s34, s37
	s_ashr_i32 s38, s37, 10
	s_and_b32 s37, s37, 0xfc00
	s_sub_i32 s34, s34, s37
	s_sext_i32_i16 s37, s34
	s_ashr_i32 s39, s38, 31
	s_bfe_u32 s37, s37, 0x4001b
	s_lshl_b64 s[38:39], s[38:39], 25
	s_add_i32 s37, s34, s37
	v_lshl_add_u64 v[50:51], v[66:67], 0, s[38:39]
	s_sext_i32_i16 s38, s37
	s_and_b32 s37, s37, 0xfff0
	s_sub_i32 s34, s34, s37
	s_lshl_b32 s37, s38, 2
	s_sext_i32_i16 s34, s34
	s_and_b32 s38, s37, 0xffffffc0
	v_lshl_add_u32 v58, s34, 7, v86
	s_ashr_i32 s39, s38, 31
	v_lshl_add_u64 v[50:51], s[38:39], 2, v[50:51]
	v_lshlrev_b32_e32 v72, 2, v68
	v_ashrrev_i32_e32 v59, 31, v58
	v_lshl_add_u64 v[60:61], v[50:51], 0, v[72:73]
	v_lshlrev_b64 v[50:51], 14, v[58:59]
	v_or_b32_e32 v52, 1, v58
	v_or_b32_e32 v62, 2, v58
	v_or_b32_e32 v58, 3, v58
	v_ashrrev_i32_e32 v53, 31, v52
	v_ashrrev_i32_e32 v63, 31, v62
	v_ashrrev_i32_e32 v59, 31, v58
	v_lshlrev_b64 v[52:53], 14, v[52:53]
	v_lshlrev_b64 v[62:63], 14, v[62:63]
	v_lshlrev_b64 v[58:59], 14, v[58:59]
	v_lshl_add_u64 v[50:51], v[60:61], 0, v[50:51]
	v_lshl_add_u64 v[54:55], v[60:61], 0, v[52:53]
	v_lshl_add_u64 v[62:63], v[60:61], 0, v[62:63]
	v_lshl_add_u64 v[64:65], v[60:61], 0, v[58:59]
	flat_load_dwordx4 v[50:53], v[50:51] nt
	s_nop 0
	flat_load_dwordx4 v[54:57], v[54:55] nt
	s_nop 0
	flat_load_dwordx4 v[58:61], v[62:63] nt
	s_nop 0
	flat_load_dwordx4 v[62:65], v[64:65] nt
	s_branch .LBB0_187

; #define LAS __attribute__((address_space(3)))
; #define TB_LOAD(R_, t_) do { const int _t = (t_); if (_t < tot) { const int _b = _t / per, _r = _t % per; ttb_load(R_, src + (size_t)_b * K_ * N_, N_, (_r % kt) * 128, (_r / kt) * 64, C.tid); } } while (0)
; __device__ __forceinline__ void ttb_load(TReg& R, const float* src, int ld, int k0, int n0, int tid) {
;     const int kr = tid >> 4, nq = tid & 15;
; #pragma unroll
;     for (int rep = 0; rep < 4; ++rep) R.v[rep] = __builtin_nontemporal_load((const f32x4*)(src + (size_t)(k0 + 4 * kr + rep) * ld + n0 + 4 * nq)); }
; __device__ __forceinline__ void ttb_put(const TReg& R, LAS unsigned* tile, int tid) {
;     const int kr = tid >> 4, nq = tid & 15;
; #pragma unroll
;     for (int c = 0; c < 4; ++c) { const int n = 4 * nq + c;
;         tile[n * 32 + (kr ^ (n & 31))] = pk4_fp8(R.v[0][c] * W_FP8_SCALE, R.v[1][c] * W_FP8_SCALE, R.v[2][c] * W_FP8_SCALE, R.v[3][c] * W_FP8_SCALE); } }
; __device__ __forceinline__ void ttb_finish(LAS const unsigned* tile, unsigned char* dst, int ldd, int k0, int n0, int map, int tid) {
;     const int n = tid >> 3, kq = tid & 7, m = n & 31, ns = n0 + n; int r = ns;
;     if (map == 2) { const int j = ns >> 1, par = ns & 1; r = 256 * (j >> 7) + 128 * par + (j & 127); }
;     const u32x4 g = *(LAS const u32x4*)(tile + n * 32 + 4 * (kq ^ (m >> 2)));
;     const unsigned a0 = (m & 1) ? g.y : g.x, a1 = (m & 1) ? g.x : g.y, a2 = (m & 1) ? g.w : g.z, a3 = (m & 1) ? g.z : g.w;
;     u32x4 w; w.x = (m & 2) ? a2 : a0; w.y = (m & 2) ? a3 : a1; w.z = (m & 2) ? a0 : a2; w.w = (m & 2) ? a1 : a3;
;     __builtin_nontemporal_store(w, (u32x4*)(dst + (size_t)r * ldd + k0 + 16 * kq));
; }
; template <int K_, int N_, int MAP_> __device__ __forceinline__ void tjob_b(const Ctx& C, int bid, int G, const float* src, unsigned char* dstb, int nbatch) {
;     constexpr int kt = K_ / 128, ntile = N_ / 64, per = kt * ntile; const int tot = per * nbatch;
;     TReg R0, R1, R2, R3; int kbuf = 0;
;     ...
;     TB_LOAD(R0, bid); TB_LOAD(R1, bid + G); TB_LOAD(R2, bid + 2 * G); TB_LOAD(R3, bid + 3 * G);
;     for (int t = bid; t < tot; t += 4 * G) { TB_STEP(R0, t); TB_STEP(R1, t + G); TB_STEP(R2, t + 2 * G); TB_STEP(R3, t + 3 * G); }
.LBB0_214:
	s_waitcnt vmcnt(0) lgkmcnt(0)
	v_mul_f32_e32 v72, 0x43800000, v2
	v_mul_f32_e32 v85, 0x43800000, v6
	v_med3_f32 v72, v72, s26, v75
	v_med3_f32 v85, v85, s26, v75
	v_cvt_pk_fp8_f32 v87, v72, v85
	v_mul_f32_e32 v86, 0x43800000, v10
	v_mul_f32_e32 v72, 0x43800000, v14
	v_med3_f32 v85, v86, s26, v75
	v_med3_f32 v72, v72, s26, v75
	v_cvt_pk_fp8_f32 v87, v85, v72 op_sel:[0,0,1]
	v_mul_f32_e32 v72, 0x43800000, v3
	v_mul_f32_e32 v85, 0x43800000, v7
	v_med3_f32 v72, v72, s26, v75
	v_med3_f32 v85, v85, s26, v75
	v_cvt_pk_fp8_f32 v88, v72, v85
	v_mul_f32_e32 v86, 0x43800000, v11
	v_mul_f32_e32 v72, 0x43800000, v15
	v_med3_f32 v85, v86, s26, v75
	v_med3_f32 v72, v72, s26, v75
	s_lshl_b32 s12, s24, 13
	v_cvt_pk_fp8_f32 v88, v85, v72 op_sel:[0,0,1]
	s_add_i32 s31, s12, 0
	v_add3_u32 v72, s31, v74, v76
	ds_write_b32 v72, v87
	v_add3_u32 v72, s31, v79, v77
	ds_write_b32 v72, v88
	v_mul_f32_e32 v72, 0x43800000, v4
	v_mul_f32_e32 v85, 0x43800000, v8
	v_med3_f32 v72, v72, s26, v75
	v_med3_f32 v85, v85, s26, v75
	v_cvt_pk_fp8_f32 v87, v72, v85
	v_mul_f32_e32 v86, 0x43800000, v12
	v_mul_f32_e32 v72, 0x43800000, v16
	v_med3_f32 v85, v86, s26, v75
	v_med3_f32 v72, v72, s26, v75
	v_cvt_pk_fp8_f32 v87, v85, v72 op_sel:[0,0,1]
	v_mul_f32_e32 v72, 0x43800000, v5
	v_mul_f32_e32 v85, 0x43800000, v9
	v_med3_f32 v72, v72, s26, v75
	v_med3_f32 v85, v85, s26, v75
	v_cvt_pk_fp8_f32 v88, v72, v85
	v_mul_f32_e32 v86, 0x43800000, v13
	v_mul_f32_e32 v72, 0x43800000, v17
	v_med3_f32 v85, v86, s26, v75
	v_med3_f32 v72, v72, s26, v75
	v_cvt_pk_fp8_f32 v88, v85, v72 op_sel:[0,0,1]
	s_add_i32 s27, s1, s16
	s_cmp_ge_i32 s27, s25
	v_add3_u32 v72, s31, v80, v82
	s_cselect_b64 s[12:13], -1, 0
	ds_write_b32 v72, v87
	v_add3_u32 v72, s31, v78, v83
	s_and_b64 vcc, exec, s[12:13]
	ds_write_b32 v72, v88
	s_cbranch_vccnz .LBB0_216
	s_ashr_i32 s33, s27, 31
	s_lshr_b32 s33, s33, 23
	s_add_i32 s33, s27, s33
	s_ashr_i32 s34, s33, 9
	s_and_b32 s33, s33, 0xfe00
	s_ashr_i32 s35, s34, 31
	s_sub_i32 s33, s27, s33
	s_lshl_b64 s[34:35], s[34:35], 24
	v_lshl_add_u64 v[2:3], v[66:67], 0, s[34:35]
	s_sext_i32_i16 s34, s33
	s_bfe_u32 s34, s34, 0x4001b
	s_add_i32 s34, s33, s34
	s_sext_i32_i16 s35, s34
	s_and_b32 s34, s34, 0xfff0
	s_sub_i32 s33, s33, s34
	s_lshl_b32 s34, s35, 2
	s_sext_i32_i16 s33, s33
	s_andn2_b32 s34, s34, 63
	v_lshl_add_u32 v10, s33, 7, v69
	s_ashr_i32 s35, s34, 31
	v_lshl_add_u64 v[2:3], s[34:35], 2, v[2:3]
	v_lshlrev_b32_e32 v72, 2, v68
	v_ashrrev_i32_e32 v11, 31, v10
	v_lshl_add_u64 v[12:13], v[2:3], 0, v[72:73]
	v_lshlrev_b64 v[2:3], 13, v[10:11]
	v_lshl_add_u64 v[14:15], v[12:13], 0, v[2:3]
	v_or_b32_e32 v2, 1, v10
	v_ashrrev_i32_e32 v3, 31, v2
	v_lshlrev_b64 v[2:3], 13, v[2:3]
	v_lshl_add_u64 v[16:17], v[12:13], 0, v[2:3]
	flat_load_dwordx4 v[2:5], v[14:15] nt
	flat_load_dwordx4 v[6:9], v[16:17] nt
	v_or_b32_e32 v14, 2, v10
	v_ashrrev_i32_e32 v15, 31, v14
	v_or_b32_e32 v10, 3, v10
	v_lshlrev_b64 v[14:15], 13, v[14:15]
	v_ashrrev_i32_e32 v11, 31, v10
	v_lshl_add_u64 v[86:87], v[12:13], 0, v[14:15]
	v_lshlrev_b64 v[10:11], 13, v[10:11]
	v_lshl_add_u64 v[88:89], v[12:13], 0, v[10:11]
	flat_load_dwordx4 v[10:13], v[86:87] nt
	flat_load_dwordx4 v[14:17], v[88:89] nt
; #define LAS __attribute__((address_space(3)))
; #define TB_LOAD(R_, t_) do { const int _t = (t_); if (_t < tot) { const int _b = _t / per, _r = _t % per; ttb_load(R_, src + (size_t)_b * K_ * N_, N_, (_r % kt) * 128, (_r / kt) * 64, C.tid); } } while (0)
; __device__ __forceinline__ void ttb_load(TReg& R, const float* src, int ld, int k0, int n0, int tid) {
;     const int kr = tid >> 4, nq = tid & 15;
; #pragma unroll
;     for (int rep = 0; rep < 4; ++rep) R.v[rep] = __builtin_nontemporal_load((const f32x4*)(src + (size_t)(k0 + 4 * kr + rep) * ld + n0 + 4 * nq)); }
; __device__ __forceinline__ void ttb_put(const TReg& R, LAS unsigned* tile, int tid) {
;     const int kr = tid >> 4, nq = tid & 15;
; #pragma unroll
;     for (int c = 0; c < 4; ++c) { const int n = 4 * nq + c;
;         tile[n * 32 + (kr ^ (n & 31))] = pk4_fp8(R.v[0][c] * W_FP8_SCALE, R.v[1][c] * W_FP8_SCALE, R.v[2][c] * W_FP8_SCALE, R.v[3][c] * W_FP8_SCALE); } }
; __device__ __forceinline__ void ttb_finish(LAS const unsigned* tile, unsigned char* dst, int ldd, int k0, int n0, int map, int tid) {
;     const int n = tid >> 3, kq = tid & 7, m = n & 31, ns = n0 + n; int r = ns;
;     if (map == 2) { const int j = ns >> 1, par = ns & 1; r = 256 * (j >> 7) + 128 * par + (j & 127); }
;     const u32x4 g = *(LAS const u32x4*)(tile + n * 32 + 4 * (kq ^ (m >> 2)));
;     const unsigned a0 = (m & 1) ? g.y : g.x, a1 = (m & 1) ? g.x : g.y, a2 = (m & 1) ? g.w : g.z, a3 = (m & 1) ? g.z : g.w;
;     u32x4 w; w.x = (m & 2) ? a2 : a0; w.y = (m & 2) ? a3 : a1; w.z = (m & 2) ? a0 : a2; w.w = (m & 2) ? a1 : a3;
;     __builtin_nontemporal_store(w, (u32x4*)(dst + (size_t)r * ldd + k0 + 16 * kq));
; }
; template <int K_, int N_, int MAP_> __device__ __forceinline__ void tjob_b(const Ctx& C, int bid, int G, const float* src, unsigned char* dstb, int nbatch) {
;     constexpr int kt = K_ / 128, ntile = N_ / 64, per = kt * ntile; const int tot = per * nbatch;
;     TReg R0, R1, R2, R3; int kbuf = 0;
;     ...
;     TB_LOAD(R0, bid); TB_LOAD(R1, bid + G); TB_LOAD(R2, bid + 2 * G); TB_LOAD(R3, bid + 3 * G);
;     for (int t = bid; t < tot; t += 4 * G) { TB_STEP(R0, t); TB_STEP(R1, t + G); TB_STEP(R2, t + 2 * G); TB_STEP(R3, t + 3 * G); }
.LBB0_216:
	s_ashr_i32 s33, s1, 31
	s_lshr_b32 s33, s33, 23
	s_add_i32 s33, s1, s33
	s_ashr_i32 s34, s33, 9
	s_and_b32 s33, s33, 0xfe00
	s_ashr_i32 s35, s34, 31
	s_sub_i32 s33, s1, s33
	s_lshl_b64 s[34:35], s[34:35], 22
	s_add_u32 s34, s22, s34
	s_sext_i32_i16 s36, s33
	v_add3_u32 v72, s31, v81, v84
	s_waitcnt lgkmcnt(0)
	s_barrier
	s_addc_u32 s35, s23, s35
	s_bfe_u32 s36, s36, 0x4001b
	ds_read_b128 v[86:89], v72
	s_add_i32 s36, s33, s36
	s_sext_i32_i16 s37, s36
	s_lshl_b32 s31, s37, 2
	s_and_b32 s36, s36, 0xfff0
	s_andn2_b32 s31, s31, 63
	s_sub_i32 s33, s33, s36
	v_add_u32_e32 v90, s31, v1
	s_waitcnt lgkmcnt(0)
	v_cndmask_b32_e64 v72, v87, v86, s[6:7]
	v_cndmask_b32_e64 v91, v89, v88, s[6:7]
	s_sext_i32_i16 s33, s33
	v_cndmask_b32_e64 v85, v86, v87, s[6:7]
	v_cndmask_b32_e64 v89, v88, v89, s[6:7]
	v_cndmask_b32_e64 v86, v91, v72, s[8:9]
	v_cndmask_b32_e64 v88, v72, v91, s[8:9]
	v_ashrrev_i32_e32 v91, 31, v90
	s_lshl_b32 s36, s33, 7
	v_lshlrev_b64 v[90:91], 11, v[90:91]
	v_lshl_add_u64 v[90:91], s[34:35], 0, v[90:91]
	s_ashr_i32 s37, s36, 31
	v_lshl_add_u64 v[90:91], v[90:91], 0, s[36:37]
	s_xor_b32 s33, s24, 1
	s_add_i32 s31, s0, s1
	v_cndmask_b32_e64 v87, v89, v85, s[8:9]
	v_cndmask_b32_e64 v89, v85, v89, s[8:9]
	v_lshl_add_u64 v[90:91], v[90:91], 0, v[70:71]
	s_cmp_ge_i32 s31, s25
	global_store_dwordx4 v[90:91], v[86:89], off nt
	s_cbranch_scc1 .LBB0_220
	v_mul_f32_e32 v72, 0x43800000, v18
	v_mul_f32_e32 v85, 0x43800000, v22
	v_med3_f32 v72, v72, s26, v75
	v_med3_f32 v85, v85, s26, v75
	v_cvt_pk_fp8_f32 v87, v72, v85
	v_mul_f32_e32 v86, 0x43800000, v26
	v_mul_f32_e32 v72, 0x43800000, v30
	v_med3_f32 v85, v86, s26, v75
	v_med3_f32 v72, v72, s26, v75
	v_cvt_pk_fp8_f32 v87, v85, v72 op_sel:[0,0,1]
	s_lshl_b32 s33, s33, 13
	s_add_i32 s33, s33, 0
	v_add3_u32 v72, s33, v74, v76
	ds_write_b32 v72, v87
	v_mul_f32_e32 v72, 0x43800000, v19
	v_mul_f32_e32 v85, 0x43800000, v23
	v_med3_f32 v72, v72, s26, v75
	v_med3_f32 v85, v85, s26, v75
	v_cvt_pk_fp8_f32 v87, v72, v85
	v_mul_f32_e32 v86, 0x43800000, v27
	v_mul_f32_e32 v72, 0x43800000, v31
	v_med3_f32 v85, v86, s26, v75
	v_med3_f32 v72, v72, s26, v75
	v_cvt_pk_fp8_f32 v87, v85, v72 op_sel:[0,0,1]
	v_mul_f32_e32 v72, 0x43800000, v20
	v_mul_f32_e32 v85, 0x43800000, v24
	v_med3_f32 v72, v72, s26, v75
	v_med3_f32 v85, v85, s26, v75
	v_cvt_pk_fp8_f32 v88, v72, v85
	v_mul_f32_e32 v86, 0x43800000, v28
	v_mul_f32_e32 v72, 0x43800000, v32
	v_med3_f32 v85, v86, s26, v75
	v_med3_f32 v72, v72, s26, v75
	v_cvt_pk_fp8_f32 v88, v85, v72 op_sel:[0,0,1]
	v_add3_u32 v72, s33, v79, v77
	ds_write_b32 v72, v87
	v_add3_u32 v72, s33, v80, v82
	ds_write_b32 v72, v88
	v_mul_f32_e32 v72, 0x43800000, v21
	v_mul_f32_e32 v85, 0x43800000, v25
	v_med3_f32 v72, v72, s26, v75
	v_med3_f32 v85, v85, s26, v75
	v_cvt_pk_fp8_f32 v87, v72, v85
	v_mul_f32_e32 v86, 0x43800000, v29
	v_mul_f32_e32 v72, 0x43800000, v33
	v_med3_f32 v85, v86, s26, v75
	v_med3_f32 v72, v72, s26, v75
	v_cvt_pk_fp8_f32 v87, v85, v72 op_sel:[0,0,1]
	s_add_i32 s34, s19, s1
	v_add3_u32 v72, s33, v78, v83
	s_cmp_ge_i32 s34, s25
	ds_write_b32 v72, v87
	s_cbranch_scc1 .LBB0_219
	s_ashr_i32 s35, s34, 31
	s_lshr_b32 s35, s35, 23
	s_add_i32 s35, s34, s35
	s_ashr_i32 s36, s35, 9
	s_and_b32 s35, s35, 0xfe00
	s_ashr_i32 s37, s36, 31
	s_sub_i32 s38, s34, s35
	s_lshl_b64 s[34:35], s[36:37], 24
	v_lshl_add_u64 v[18:19], v[66:67], 0, s[34:35]
	s_sext_i32_i16 s34, s38
	s_bfe_u32 s34, s34, 0x4001b
	s_add_i32 s34, s38, s34
	s_sext_i32_i16 s35, s34
	s_and_b32 s34, s34, 0xfff0
	s_sub_i32 s34, s38, s34
	s_sext_i32_i16 s36, s34
	s_lshl_b32 s34, s35, 2
	s_andn2_b32 s34, s34, 63
	v_lshl_add_u32 v26, s36, 7, v69
	s_ashr_i32 s35, s34, 31
	v_lshl_add_u64 v[18:19], s[34:35], 2, v[18:19]
	v_lshlrev_b32_e32 v72, 2, v68
	v_ashrrev_i32_e32 v27, 31, v26
	v_lshl_add_u64 v[28:29], v[18:19], 0, v[72:73]
	v_lshlrev_b64 v[18:19], 13, v[26:27]
	v_lshl_add_u64 v[30:31], v[28:29], 0, v[18:19]
	v_or_b32_e32 v18, 1, v26
	v_ashrrev_i32_e32 v19, 31, v18
	v_lshlrev_b64 v[18:19], 13, v[18:19]
	v_lshl_add_u64 v[32:33], v[28:29], 0, v[18:19]
	flat_load_dwordx4 v[18:21], v[30:31] nt
	flat_load_dwordx4 v[22:25], v[32:33] nt
	v_or_b32_e32 v30, 2, v26
	v_ashrrev_i32_e32 v31, 31, v30
	v_or_b32_e32 v26, 3, v26
	v_lshlrev_b64 v[30:31], 13, v[30:31]
	v_ashrrev_i32_e32 v27, 31, v26
	v_lshl_add_u64 v[86:87], v[28:29], 0, v[30:31]
	v_lshlrev_b64 v[26:27], 13, v[26:27]
	v_lshl_add_u64 v[88:89], v[28:29], 0, v[26:27]
	flat_load_dwordx4 v[26:29], v[86:87] nt
	flat_load_dwordx4 v[30:33], v[88:89] nt

; #define LAS __attribute__((address_space(3)))
; #define TB_LOAD(R_, t_) do { const int _t = (t_); if (_t < tot) { const int _b = _t / per, _r = _t % per; ttb_load(R_, src + (size_t)_b * K_ * N_, N_, (_r % kt) * 128, (_r / kt) * 64, C.tid); } } while (0)
; __device__ __forceinline__ void ttb_load(TReg& R, const float* src, int ld, int k0, int n0, int tid) {
;     const int kr = tid >> 4, nq = tid & 15;
; #pragma unroll
;     for (int rep = 0; rep < 4; ++rep) R.v[rep] = __builtin_nontemporal_load((const f32x4*)(src + (size_t)(k0 + 4 * kr + rep) * ld + n0 + 4 * nq)); }
; __device__ __forceinline__ void ttb_put(const TReg& R, LAS unsigned* tile, int tid) {
;     const int kr = tid >> 4, nq = tid & 15;
; #pragma unroll
;     for (int c = 0; c < 4; ++c) { const int n = 4 * nq + c;
;         tile[n * 32 + (kr ^ (n & 31))] = pk4_fp8(R.v[0][c] * W_FP8_SCALE, R.v[1][c] * W_FP8_SCALE, R.v[2][c] * W_FP8_SCALE, R.v[3][c] * W_FP8_SCALE); } }
; __device__ __forceinline__ void ttb_finish(LAS const unsigned* tile, unsigned char* dst, int ldd, int k0, int n0, int map, int tid) {
;     const int n = tid >> 3, kq = tid & 7, m = n & 31, ns = n0 + n; int r = ns;
;     if (map == 2) { const int j = ns >> 1, par = ns & 1; r = 256 * (j >> 7) + 128 * par + (j & 127); }
;     const u32x4 g = *(LAS const u32x4*)(tile + n * 32 + 4 * (kq ^ (m >> 2)));
;     const unsigned a0 = (m & 1) ? g.y : g.x, a1 = (m & 1) ? g.x : g.y, a2 = (m & 1) ? g.w : g.z, a3 = (m & 1) ? g.z : g.w;
;     u32x4 w; w.x = (m & 2) ? a2 : a0; w.y = (m & 2) ? a3 : a1; w.z = (m & 2) ? a0 : a2; w.w = (m & 2) ? a1 : a3;
;     __builtin_nontemporal_store(w, (u32x4*)(dst + (size_t)r * ldd + k0 + 16 * kq));
; }
; template <int K_, int N_, int MAP_> __device__ __forceinline__ void tjob_b(const Ctx& C, int bid, int G, const float* src, unsigned char* dstb, int nbatch) {
;     constexpr int kt = K_ / 128, ntile = N_ / 64, per = kt * ntile; const int tot = per * nbatch;
;     TReg R0, R1, R2, R3; int kbuf = 0;
;     ...
;     TB_LOAD(R0, bid); TB_LOAD(R1, bid + G); TB_LOAD(R2, bid + 2 * G); TB_LOAD(R3, bid + 3 * G);
;     for (int t = bid; t < tot; t += 4 * G) { TB_STEP(R0, t); TB_STEP(R1, t + G); TB_STEP(R2, t + 2 * G); TB_STEP(R3, t + 3 * G); }
.LBB0_221:
	v_mul_f32_e32 v72, 0x43800000, v34
	v_mul_f32_e32 v85, 0x43800000, v38
	v_med3_f32 v72, v72, s26, v75
	v_med3_f32 v85, v85, s26, v75
	v_cvt_pk_fp8_f32 v87, v72, v85
	v_mul_f32_e32 v86, 0x43800000, v42
	v_mul_f32_e32 v72, 0x43800000, v46
	v_med3_f32 v85, v86, s26, v75
	v_med3_f32 v72, v72, s26, v75
	v_cvt_pk_fp8_f32 v87, v85, v72 op_sel:[0,0,1]
	s_lshl_b32 s33, s24, 13
	s_add_i32 s33, s33, 0
	v_add3_u32 v72, s33, v74, v76
	ds_write_b32 v72, v87
	v_mul_f32_e32 v72, 0x43800000, v35
	v_mul_f32_e32 v85, 0x43800000, v39
	v_med3_f32 v72, v72, s26, v75
	v_med3_f32 v85, v85, s26, v75
	v_cvt_pk_fp8_f32 v87, v72, v85
	v_mul_f32_e32 v86, 0x43800000, v43
	v_mul_f32_e32 v72, 0x43800000, v47
	v_med3_f32 v85, v86, s26, v75
	v_med3_f32 v72, v72, s26, v75
	v_cvt_pk_fp8_f32 v87, v85, v72 op_sel:[0,0,1]
	v_mul_f32_e32 v72, 0x43800000, v36
	v_mul_f32_e32 v85, 0x43800000, v40
	v_med3_f32 v72, v72, s26, v75
	v_med3_f32 v85, v85, s26, v75
	v_cvt_pk_fp8_f32 v88, v72, v85
	v_mul_f32_e32 v86, 0x43800000, v44
	v_mul_f32_e32 v72, 0x43800000, v48
	v_med3_f32 v85, v86, s26, v75
	v_med3_f32 v72, v72, s26, v75
	v_cvt_pk_fp8_f32 v88, v85, v72 op_sel:[0,0,1]
	v_add3_u32 v72, s33, v79, v77
	ds_write_b32 v72, v87
	v_add3_u32 v72, s33, v80, v82
	ds_write_b32 v72, v88
	v_mul_f32_e32 v72, 0x43800000, v37
	v_mul_f32_e32 v85, 0x43800000, v41
	v_med3_f32 v72, v72, s26, v75
	v_med3_f32 v85, v85, s26, v75
	v_cvt_pk_fp8_f32 v87, v72, v85
	v_mul_f32_e32 v86, 0x43800000, v45
	v_mul_f32_e32 v72, 0x43800000, v49
	v_med3_f32 v85, v86, s26, v75
	v_med3_f32 v72, v72, s26, v75
	v_cvt_pk_fp8_f32 v87, v85, v72 op_sel:[0,0,1]
	s_add_i32 s34, s18, s1
	v_add3_u32 v72, s33, v78, v83
	s_cmp_ge_i32 s34, s25
	ds_write_b32 v72, v87
	s_cbranch_scc1 .LBB0_223
	s_ashr_i32 s35, s34, 31
	s_lshr_b32 s35, s35, 23
	s_add_i32 s35, s34, s35
	s_ashr_i32 s36, s35, 9
	s_and_b32 s35, s35, 0xfe00
	s_ashr_i32 s37, s36, 31
	s_sub_i32 s38, s34, s35
	s_lshl_b64 s[34:35], s[36:37], 24
	v_lshl_add_u64 v[34:35], v[66:67], 0, s[34:35]
	s_sext_i32_i16 s34, s38
	s_bfe_u32 s34, s34, 0x4001b
	s_add_i32 s34, s38, s34
	s_sext_i32_i16 s35, s34
	s_and_b32 s34, s34, 0xfff0
	s_sub_i32 s34, s38, s34
	s_sext_i32_i16 s36, s34
	s_lshl_b32 s34, s35, 2
	s_andn2_b32 s34, s34, 63
	v_lshl_add_u32 v42, s36, 7, v69
	s_ashr_i32 s35, s34, 31
	v_lshl_add_u64 v[34:35], s[34:35], 2, v[34:35]
	v_lshlrev_b32_e32 v72, 2, v68
	v_ashrrev_i32_e32 v43, 31, v42
	v_lshl_add_u64 v[44:45], v[34:35], 0, v[72:73]
	v_lshlrev_b64 v[34:35], 13, v[42:43]
	v_lshl_add_u64 v[46:47], v[44:45], 0, v[34:35]
	v_or_b32_e32 v34, 1, v42
	v_ashrrev_i32_e32 v35, 31, v34
	v_lshlrev_b64 v[34:35], 13, v[34:35]
	v_lshl_add_u64 v[48:49], v[44:45], 0, v[34:35]
	flat_load_dwordx4 v[34:37], v[46:47] nt
	flat_load_dwordx4 v[38:41], v[48:49] nt
	v_or_b32_e32 v46, 2, v42
	v_ashrrev_i32_e32 v47, 31, v46
	v_or_b32_e32 v42, 3, v42
	v_lshlrev_b64 v[46:47], 13, v[46:47]
	v_ashrrev_i32_e32 v43, 31, v42
	v_lshl_add_u64 v[86:87], v[44:45], 0, v[46:47]
	v_lshlrev_b64 v[42:43], 13, v[42:43]
	v_lshl_add_u64 v[88:89], v[44:45], 0, v[42:43]
	flat_load_dwordx4 v[42:45], v[86:87] nt
	flat_load_dwordx4 v[46:49], v[88:89] nt

; #define LAS __attribute__((address_space(3)))
; #define TB_LOAD(R_, t_) do { const int _t = (t_); if (_t < tot) { const int _b = _t / per, _r = _t % per; ttb_load(R_, src + (size_t)_b * K_ * N_, N_, (_r % kt) * 128, (_r / kt) * 64, C.tid); } } while (0)
; __device__ __forceinline__ void ttb_load(TReg& R, const float* src, int ld, int k0, int n0, int tid) {
;     const int kr = tid >> 4, nq = tid & 15;
; #pragma unroll
;     for (int rep = 0; rep < 4; ++rep) R.v[rep] = __builtin_nontemporal_load((const f32x4*)(src + (size_t)(k0 + 4 * kr + rep) * ld + n0 + 4 * nq)); }
; __device__ __forceinline__ void ttb_put(const TReg& R, LAS unsigned* tile, int tid) {
;     const int kr = tid >> 4, nq = tid & 15;
; #pragma unroll
;     for (int c = 0; c < 4; ++c) { const int n = 4 * nq + c;
;         tile[n * 32 + (kr ^ (n & 31))] = pk4_fp8(R.v[0][c] * W_FP8_SCALE, R.v[1][c] * W_FP8_SCALE, R.v[2][c] * W_FP8_SCALE, R.v[3][c] * W_FP8_SCALE); } }
; __device__ __forceinline__ void ttb_finish(LAS const unsigned* tile, unsigned char* dst, int ldd, int k0, int n0, int map, int tid) {
;     const int n = tid >> 3, kq = tid & 7, m = n & 31, ns = n0 + n; int r = ns;
;     if (map == 2) { const int j = ns >> 1, par = ns & 1; r = 256 * (j >> 7) + 128 * par + (j & 127); }
;     const u32x4 g = *(LAS const u32x4*)(tile + n * 32 + 4 * (kq ^ (m >> 2)));
;     const unsigned a0 = (m & 1) ? g.y : g.x, a1 = (m & 1) ? g.x : g.y, a2 = (m & 1) ? g.w : g.z, a3 = (m & 1) ? g.z : g.w;
;     u32x4 w; w.x = (m & 2) ? a2 : a0; w.y = (m & 2) ? a3 : a1; w.z = (m & 2) ? a0 : a2; w.w = (m & 2) ? a1 : a3;
;     __builtin_nontemporal_store(w, (u32x4*)(dst + (size_t)r * ldd + k0 + 16 * kq));
; }
; template <int K_, int N_, int MAP_> __device__ __forceinline__ void tjob_b(const Ctx& C, int bid, int G, const float* src, unsigned char* dstb, int nbatch) {
;     constexpr int kt = K_ / 128, ntile = N_ / 64, per = kt * ntile; const int tot = per * nbatch;
;     TReg R0, R1, R2, R3; int kbuf = 0;
;     ...
;     TB_LOAD(R0, bid); TB_LOAD(R1, bid + G); TB_LOAD(R2, bid + 2 * G); TB_LOAD(R3, bid + 3 * G);
;     for (int t = bid; t < tot; t += 4 * G) { TB_STEP(R0, t); TB_STEP(R1, t + G); TB_STEP(R2, t + 2 * G); TB_STEP(R3, t + 3 * G); }
.LBB0_224:
	s_add_i32 s31, s15, s1
	s_cmp_ge_i32 s31, s25
	s_cbranch_scc1 .LBB0_213
	v_mul_f32_e32 v72, 0x43800000, v50
	v_mul_f32_e32 v85, 0x43800000, v54
	v_med3_f32 v72, v72, s26, v75
	v_med3_f32 v85, v85, s26, v75
	v_cvt_pk_fp8_f32 v87, v72, v85
	v_mul_f32_e32 v86, 0x43800000, v58
	v_mul_f32_e32 v72, 0x43800000, v62
	v_med3_f32 v85, v86, s26, v75
	v_med3_f32 v72, v72, s26, v75
	v_cvt_pk_fp8_f32 v87, v85, v72 op_sel:[0,0,1]
	s_lshl_b32 s33, s24, 13
	s_add_i32 s33, s33, 0
	v_add3_u32 v72, s33, v74, v76
	ds_write_b32 v72, v87
	v_mul_f32_e32 v72, 0x43800000, v51
	v_mul_f32_e32 v85, 0x43800000, v55
	v_med3_f32 v72, v72, s26, v75
	v_med3_f32 v85, v85, s26, v75
	v_cvt_pk_fp8_f32 v87, v72, v85
	v_mul_f32_e32 v86, 0x43800000, v59
	v_mul_f32_e32 v72, 0x43800000, v63
	v_med3_f32 v85, v86, s26, v75
	v_med3_f32 v72, v72, s26, v75
	v_cvt_pk_fp8_f32 v87, v85, v72 op_sel:[0,0,1]
	v_mul_f32_e32 v72, 0x43800000, v52
	v_mul_f32_e32 v85, 0x43800000, v56
	v_med3_f32 v72, v72, s26, v75
	v_med3_f32 v85, v85, s26, v75
	v_cvt_pk_fp8_f32 v88, v72, v85
	v_mul_f32_e32 v86, 0x43800000, v60
	v_mul_f32_e32 v72, 0x43800000, v64
	v_med3_f32 v85, v86, s26, v75
	v_med3_f32 v72, v72, s26, v75
	v_cvt_pk_fp8_f32 v88, v85, v72 op_sel:[0,0,1]
	v_add3_u32 v72, s33, v79, v77
	ds_write_b32 v72, v87
	v_add3_u32 v72, s33, v80, v82
	ds_write_b32 v72, v88
	v_mul_f32_e32 v72, 0x43800000, v53
	v_mul_f32_e32 v85, 0x43800000, v57
	v_med3_f32 v72, v72, s26, v75
	v_med3_f32 v85, v85, s26, v75
	v_cvt_pk_fp8_f32 v87, v72, v85
	v_mul_f32_e32 v86, 0x43800000, v61
	v_mul_f32_e32 v72, 0x43800000, v65
	v_med3_f32 v85, v86, s26, v75
	v_med3_f32 v72, v72, s26, v75
	v_cvt_pk_fp8_f32 v87, v85, v72 op_sel:[0,0,1]
	s_add_i32 s1, s17, s1
	v_add3_u32 v72, s33, v78, v83
	s_cmp_ge_i32 s1, s25
	ds_write_b32 v72, v87
	s_cbranch_scc1 .LBB0_212
	s_ashr_i32 s34, s1, 31
	s_lshr_b32 s34, s34, 23
	s_add_i32 s35, s1, s34
	s_ashr_i32 s34, s35, 9
	s_and_b32 s35, s35, 0xfe00
	s_sub_i32 s1, s1, s35
	s_ashr_i32 s35, s34, 31
	s_lshl_b64 s[34:35], s[34:35], 24
	v_lshl_add_u64 v[50:51], v[66:67], 0, s[34:35]
	s_sext_i32_i16 s34, s1
	s_bfe_u32 s34, s34, 0x4001b
	s_add_i32 s34, s1, s34
	s_sext_i32_i16 s35, s34
	s_and_b32 s34, s34, 0xfff0
	s_sub_i32 s1, s1, s34
	s_lshl_b32 s34, s35, 2
	s_sext_i32_i16 s1, s1
	s_andn2_b32 s34, s34, 63
	v_lshl_add_u32 v58, s1, 7, v69
	s_ashr_i32 s35, s34, 31
	v_lshl_add_u64 v[50:51], s[34:35], 2, v[50:51]
	v_lshlrev_b32_e32 v72, 2, v68
	v_ashrrev_i32_e32 v59, 31, v58
	v_lshl_add_u64 v[60:61], v[50:51], 0, v[72:73]
	v_lshlrev_b64 v[50:51], 13, v[58:59]
	v_lshl_add_u64 v[62:63], v[60:61], 0, v[50:51]
	v_or_b32_e32 v50, 1, v58
	v_ashrrev_i32_e32 v51, 31, v50
	v_lshlrev_b64 v[50:51], 13, v[50:51]
	v_lshl_add_u64 v[64:65], v[60:61], 0, v[50:51]
	flat_load_dwordx4 v[50:53], v[62:63] nt
	flat_load_dwordx4 v[54:57], v[64:65] nt
	v_or_b32_e32 v62, 2, v58
	v_ashrrev_i32_e32 v63, 31, v62
	v_or_b32_e32 v58, 3, v58
	v_lshlrev_b64 v[62:63], 13, v[62:63]
	v_ashrrev_i32_e32 v59, 31, v58
	v_lshl_add_u64 v[86:87], v[60:61], 0, v[62:63]
	v_lshlrev_b64 v[58:59], 13, v[58:59]
	v_lshl_add_u64 v[88:89], v[60:61], 0, v[58:59]
	flat_load_dwordx4 v[58:61], v[86:87] nt
	flat_load_dwordx4 v[62:65], v[88:89] nt
	s_branch .LBB0_212

; #define LAS __attribute__((address_space(3)))
; #define TB_LOAD(R_, t_) do { const int _t = (t_); if (_t < tot) { const int _b = _t / per, _r = _t % per; ttb_load(R_, src + (size_t)_b * K_ * N_, N_, (_r % kt) * 128, (_r / kt) * 64, C.tid); } } while (0)
; __device__ __forceinline__ void ttb_load(TReg& R, const float* src, int ld, int k0, int n0, int tid) {
;     const int kr = tid >> 4, nq = tid & 15;
; #pragma unroll
;     for (int rep = 0; rep < 4; ++rep) R.v[rep] = __builtin_nontemporal_load((const f32x4*)(src + (size_t)(k0 + 4 * kr + rep) * ld + n0 + 4 * nq)); }
; __device__ __forceinline__ void ttb_put(const TReg& R, LAS unsigned* tile, int tid) {
;     const int kr = tid >> 4, nq = tid & 15;
; #pragma unroll
;     for (int c = 0; c < 4; ++c) { const int n = 4 * nq + c;
;         tile[n * 32 + (kr ^ (n & 31))] = pk4_fp8(R.v[0][c] * W_FP8_SCALE, R.v[1][c] * W_FP8_SCALE, R.v[2][c] * W_FP8_SCALE, R.v[3][c] * W_FP8_SCALE); } }
; __device__ __forceinline__ void ttb_finish(LAS const unsigned* tile, unsigned char* dst, int ldd, int k0, int n0, int map, int tid) {
;     const int n = tid >> 3, kq = tid & 7, m = n & 31, ns = n0 + n; int r = ns;
;     if (map == 2) { const int j = ns >> 1, par = ns & 1; r = 256 * (j >> 7) + 128 * par + (j & 127); }
;     const u32x4 g = *(LAS const u32x4*)(tile + n * 32 + 4 * (kq ^ (m >> 2)));
;     const unsigned a0 = (m & 1) ? g.y : g.x, a1 = (m & 1) ? g.x : g.y, a2 = (m & 1) ? g.w : g.z, a3 = (m & 1) ? g.z : g.w;
;     u32x4 w; w.x = (m & 2) ? a2 : a0; w.y = (m & 2) ? a3 : a1; w.z = (m & 2) ? a0 : a2; w.w = (m & 2) ? a1 : a3;
;     __builtin_nontemporal_store(w, (u32x4*)(dst + (size_t)r * ldd + k0 + 16 * kq));
; }
; template <int K_, int N_, int MAP_> __device__ __forceinline__ void tjob_b(const Ctx& C, int bid, int G, const float* src, unsigned char* dstb, int nbatch) {
;     constexpr int kt = K_ / 128, ntile = N_ / 64, per = kt * ntile; const int tot = per * nbatch;
;     TReg R0, R1, R2, R3; int kbuf = 0;
;     ...
;     TB_LOAD(R0, bid); TB_LOAD(R1, bid + G); TB_LOAD(R2, bid + 2 * G); TB_LOAD(R3, bid + 3 * G);
;     for (int t = bid; t < tot; t += 4 * G) { TB_STEP(R0, t); TB_STEP(R1, t + G); TB_STEP(R2, t + 2 * G); TB_STEP(R3, t + 3 * G); }
.LBB0_283:
	s_waitcnt vmcnt(0) lgkmcnt(0)
	v_mul_f32_e32 v72, 0x43800000, v2
	v_mul_f32_e32 v85, 0x43800000, v6
	v_med3_f32 v72, v72, s17, v79
	v_med3_f32 v85, v85, s17, v79
	v_cvt_pk_fp8_f32 v87, v72, v85
	v_mul_f32_e32 v86, 0x43800000, v10
	v_mul_f32_e32 v72, 0x43800000, v14
	v_med3_f32 v85, v86, s17, v79
	v_med3_f32 v72, v72, s17, v79
	v_cvt_pk_fp8_f32 v87, v85, v72 op_sel:[0,0,1]
	v_mul_f32_e32 v72, 0x43800000, v3
	v_mul_f32_e32 v85, 0x43800000, v7
	v_med3_f32 v72, v72, s17, v79
	v_med3_f32 v85, v85, s17, v79
	v_cvt_pk_fp8_f32 v88, v72, v85
	v_mul_f32_e32 v86, 0x43800000, v11
	v_mul_f32_e32 v72, 0x43800000, v15
	v_med3_f32 v85, v86, s17, v79
	v_med3_f32 v72, v72, s17, v79
	s_lshl_b32 s2, s13, 13
	v_cvt_pk_fp8_f32 v88, v85, v72 op_sel:[0,0,1]
	s_add_i32 s20, s2, 0
	v_add3_u32 v72, s20, v1, v80
	ds_write_b32 v72, v87
	v_add3_u32 v72, s20, v69, v81
	ds_write_b32 v72, v88
	v_mul_f32_e32 v72, 0x43800000, v4
	v_mul_f32_e32 v85, 0x43800000, v8
	v_med3_f32 v72, v72, s17, v79
	v_med3_f32 v85, v85, s17, v79
	v_cvt_pk_fp8_f32 v87, v72, v85
	v_mul_f32_e32 v86, 0x43800000, v12
	v_mul_f32_e32 v72, 0x43800000, v16
	v_med3_f32 v85, v86, s17, v79
	v_med3_f32 v72, v72, s17, v79
	v_cvt_pk_fp8_f32 v87, v85, v72 op_sel:[0,0,1]
	v_mul_f32_e32 v72, 0x43800000, v5
	v_mul_f32_e32 v85, 0x43800000, v9
	v_med3_f32 v72, v72, s17, v79
	v_med3_f32 v85, v85, s17, v79
	v_cvt_pk_fp8_f32 v88, v72, v85
	v_mul_f32_e32 v86, 0x43800000, v13
	v_mul_f32_e32 v72, 0x43800000, v17
	v_med3_f32 v85, v86, s17, v79
	v_med3_f32 v72, v72, s17, v79
	v_cvt_pk_fp8_f32 v88, v85, v72 op_sel:[0,0,1]
	s_add_i32 s18, s19, s12
	s_cmpk_gt_i32 s18, 0x15ff
	v_add3_u32 v72, s20, v74, v82
	s_cselect_b64 s[2:3], -1, 0
	ds_write_b32 v72, v87
	v_add3_u32 v72, s20, v75, v83
	s_and_b64 vcc, exec, s[2:3]
	ds_write_b32 v72, v88
	s_cbranch_vccnz .LBB0_285
	s_ashr_i32 s21, s18, 31
	s_lshr_b32 s21, s21, 23
	s_add_i32 s21, s18, s21
	s_ashr_i32 s22, s21, 9
	s_and_b32 s21, s21, 0xfe00
	s_ashr_i32 s23, s22, 31
	s_sub_i32 s21, s18, s21
	s_lshl_b64 s[22:23], s[22:23], 24
	v_lshl_add_u64 v[2:3], v[66:67], 0, s[22:23]
	s_sext_i32_i16 s22, s21
	s_bfe_u32 s22, s22, 0x4001b
	s_add_i32 s22, s21, s22
	s_sext_i32_i16 s23, s22
	s_and_b32 s22, s22, 0xfff0
	s_sub_i32 s21, s21, s22
	s_lshl_b32 s22, s23, 2
	s_sext_i32_i16 s21, s21
	s_andn2_b32 s22, s22, 63
	v_lshl_add_u32 v10, s21, 7, v78
	s_ashr_i32 s23, s22, 31
	v_lshl_add_u64 v[2:3], s[22:23], 2, v[2:3]
	v_lshlrev_b32_e32 v72, 2, v68
	v_ashrrev_i32_e32 v11, 31, v10
	v_lshl_add_u64 v[12:13], v[2:3], 0, v[72:73]
	v_lshlrev_b64 v[2:3], 13, v[10:11]
	v_lshl_add_u64 v[14:15], v[12:13], 0, v[2:3]
	v_or_b32_e32 v2, 1, v10
	v_ashrrev_i32_e32 v3, 31, v2
	v_lshlrev_b64 v[2:3], 13, v[2:3]
	v_lshl_add_u64 v[16:17], v[12:13], 0, v[2:3]
	flat_load_dwordx4 v[2:5], v[14:15] nt
	flat_load_dwordx4 v[6:9], v[16:17] nt
	v_or_b32_e32 v14, 2, v10
	v_ashrrev_i32_e32 v15, 31, v14
	v_or_b32_e32 v10, 3, v10
	v_lshlrev_b64 v[14:15], 13, v[14:15]
	v_ashrrev_i32_e32 v11, 31, v10
	v_lshl_add_u64 v[86:87], v[12:13], 0, v[14:15]
	v_lshlrev_b64 v[10:11], 13, v[10:11]
	v_lshl_add_u64 v[88:89], v[12:13], 0, v[10:11]
	flat_load_dwordx4 v[10:13], v[86:87] nt
	flat_load_dwordx4 v[14:17], v[88:89] nt
; #define LAS __attribute__((address_space(3)))
; #define TB_LOAD(R_, t_) do { const int _t = (t_); if (_t < tot) { const int _b = _t / per, _r = _t % per; ttb_load(R_, src + (size_t)_b * K_ * N_, N_, (_r % kt) * 128, (_r / kt) * 64, C.tid); } } while (0)
; __device__ __forceinline__ void ttb_load(TReg& R, const float* src, int ld, int k0, int n0, int tid) {
;     const int kr = tid >> 4, nq = tid & 15;
; #pragma unroll
;     for (int rep = 0; rep < 4; ++rep) R.v[rep] = __builtin_nontemporal_load((const f32x4*)(src + (size_t)(k0 + 4 * kr + rep) * ld + n0 + 4 * nq)); }
; __device__ __forceinline__ void ttb_put(const TReg& R, LAS unsigned* tile, int tid) {
;     const int kr = tid >> 4, nq = tid & 15;
; #pragma unroll
;     for (int c = 0; c < 4; ++c) { const int n = 4 * nq + c;
;         tile[n * 32 + (kr ^ (n & 31))] = pk4_fp8(R.v[0][c] * W_FP8_SCALE, R.v[1][c] * W_FP8_SCALE, R.v[2][c] * W_FP8_SCALE, R.v[3][c] * W_FP8_SCALE); } }
; __device__ __forceinline__ void ttb_finish(LAS const unsigned* tile, unsigned char* dst, int ldd, int k0, int n0, int map, int tid) {
;     const int n = tid >> 3, kq = tid & 7, m = n & 31, ns = n0 + n; int r = ns;
;     if (map == 2) { const int j = ns >> 1, par = ns & 1; r = 256 * (j >> 7) + 128 * par + (j & 127); }
;     const u32x4 g = *(LAS const u32x4*)(tile + n * 32 + 4 * (kq ^ (m >> 2)));
;     const unsigned a0 = (m & 1) ? g.y : g.x, a1 = (m & 1) ? g.x : g.y, a2 = (m & 1) ? g.w : g.z, a3 = (m & 1) ? g.z : g.w;
;     u32x4 w; w.x = (m & 2) ? a2 : a0; w.y = (m & 2) ? a3 : a1; w.z = (m & 2) ? a0 : a2; w.w = (m & 2) ? a1 : a3;
;     __builtin_nontemporal_store(w, (u32x4*)(dst + (size_t)r * ldd + k0 + 16 * kq));
; }
; template <int K_, int N_, int MAP_> __device__ __forceinline__ void tjob_b(const Ctx& C, int bid, int G, const float* src, unsigned char* dstb, int nbatch) {
;     constexpr int kt = K_ / 128, ntile = N_ / 64, per = kt * ntile; const int tot = per * nbatch;
;     TReg R0, R1, R2, R3; int kbuf = 0;
;     ...
;     TB_LOAD(R0, bid); TB_LOAD(R1, bid + G); TB_LOAD(R2, bid + 2 * G); TB_LOAD(R3, bid + 3 * G);
;     for (int t = bid; t < tot; t += 4 * G) { TB_STEP(R0, t); TB_STEP(R1, t + G); TB_STEP(R2, t + 2 * G); TB_STEP(R3, t + 3 * G); }
.LBB0_285:
	s_ashr_i32 s21, s19, 31
	s_lshr_b32 s21, s21, 23
	s_add_i32 s21, s19, s21
	s_ashr_i32 s22, s21, 9
	s_and_b32 s21, s21, 0xfe00
	s_ashr_i32 s23, s22, 31
	s_sub_i32 s21, s19, s21
	s_lshl_b64 s[22:23], s[22:23], 22
	s_add_u32 s22, s0, s22
	s_sext_i32_i16 s24, s21
	s_addc_u32 s23, s1, s23
	s_bfe_u32 s24, s24, 0x4001b
	s_add_i32 s24, s21, s24
	v_add3_u32 v72, s20, v77, v84
	s_waitcnt lgkmcnt(0)
	s_barrier
	s_sext_i32_i16 s25, s24
	s_and_b32 s24, s24, 0xfff0
	ds_read_b128 v[86:89], v72
	s_sub_i32 s21, s21, s24
	s_sext_i32_i16 s21, s21
	s_lshl_b32 s20, s21, 7
	s_lshl_b32 s21, s25, 2
	s_andn2_b32 s21, s21, 63
	v_add_u32_e32 v90, s21, v76
	s_waitcnt lgkmcnt(0)
	v_cndmask_b32_e64 v72, v87, v86, s[6:7]
	v_cndmask_b32_e64 v91, v89, v88, s[6:7]
	v_cndmask_b32_e64 v85, v86, v87, s[6:7]
	v_cndmask_b32_e64 v89, v88, v89, s[6:7]
	v_cndmask_b32_e64 v86, v91, v72, s[8:9]
	v_cndmask_b32_e64 v88, v72, v91, s[8:9]
	v_ashrrev_i32_e32 v91, 31, v90
	v_lshlrev_b64 v[90:91], 11, v[90:91]
	v_lshl_add_u64 v[90:91], s[22:23], 0, v[90:91]
	s_ashr_i32 s21, s20, 31
	v_lshl_add_u64 v[90:91], v[90:91], 0, s[20:21]
	s_xor_b32 s21, s13, 1
	s_add_i32 s20, s28, s19
	v_cndmask_b32_e64 v87, v89, v85, s[8:9]
	v_cndmask_b32_e64 v89, v85, v89, s[8:9]
	v_lshl_add_u64 v[90:91], v[90:91], 0, v[70:71]
	s_cmpk_gt_i32 s20, 0x15ff
	global_store_dwordx4 v[90:91], v[86:89], off nt
	s_cbranch_scc1 .LBB0_289
	v_mul_f32_e32 v72, 0x43800000, v18
	v_mul_f32_e32 v85, 0x43800000, v22
	v_med3_f32 v72, v72, s17, v79
	v_med3_f32 v85, v85, s17, v79
	v_cvt_pk_fp8_f32 v87, v72, v85
	v_mul_f32_e32 v86, 0x43800000, v26
	v_mul_f32_e32 v72, 0x43800000, v30
	v_med3_f32 v85, v86, s17, v79
	v_med3_f32 v72, v72, s17, v79
	v_cvt_pk_fp8_f32 v87, v85, v72 op_sel:[0,0,1]
	s_lshl_b32 s21, s21, 13
	s_add_i32 s21, s21, 0
	v_add3_u32 v72, s21, v1, v80
	ds_write_b32 v72, v87
	v_mul_f32_e32 v72, 0x43800000, v19
	v_mul_f32_e32 v85, 0x43800000, v23
	v_med3_f32 v72, v72, s17, v79
	v_med3_f32 v85, v85, s17, v79
	v_cvt_pk_fp8_f32 v87, v72, v85
	v_mul_f32_e32 v86, 0x43800000, v27
	v_mul_f32_e32 v72, 0x43800000, v31
	v_med3_f32 v85, v86, s17, v79
	v_med3_f32 v72, v72, s17, v79
	v_cvt_pk_fp8_f32 v87, v85, v72 op_sel:[0,0,1]
	v_mul_f32_e32 v72, 0x43800000, v20
	v_mul_f32_e32 v85, 0x43800000, v24
	v_med3_f32 v72, v72, s17, v79
	v_med3_f32 v85, v85, s17, v79
	v_cvt_pk_fp8_f32 v88, v72, v85
	v_mul_f32_e32 v86, 0x43800000, v28
	v_mul_f32_e32 v72, 0x43800000, v32
	v_med3_f32 v85, v86, s17, v79
	v_med3_f32 v72, v72, s17, v79
	v_cvt_pk_fp8_f32 v88, v85, v72 op_sel:[0,0,1]
	v_add3_u32 v72, s21, v69, v81
	ds_write_b32 v72, v87
	v_add3_u32 v72, s21, v74, v82
	ds_write_b32 v72, v88
	v_mul_f32_e32 v72, 0x43800000, v21
	v_mul_f32_e32 v85, 0x43800000, v25
	v_med3_f32 v72, v72, s17, v79
	v_med3_f32 v85, v85, s17, v79
	v_cvt_pk_fp8_f32 v87, v72, v85
	v_mul_f32_e32 v86, 0x43800000, v29
	v_mul_f32_e32 v72, 0x43800000, v33
	v_med3_f32 v85, v86, s17, v79
	v_med3_f32 v72, v72, s17, v79
	v_cvt_pk_fp8_f32 v87, v85, v72 op_sel:[0,0,1]
	s_add_i32 s22, s16, s19
	v_add3_u32 v72, s21, v75, v83
	s_cmpk_gt_i32 s22, 0x15ff
	ds_write_b32 v72, v87
	s_cbranch_scc1 .LBB0_288
	s_ashr_i32 s23, s22, 31
	s_lshr_b32 s23, s23, 23
	s_add_i32 s23, s22, s23
	s_ashr_i32 s24, s23, 9
	s_and_b32 s23, s23, 0xfe00
	s_ashr_i32 s25, s24, 31
	s_sub_i32 s26, s22, s23
	s_lshl_b64 s[22:23], s[24:25], 24
	v_lshl_add_u64 v[18:19], v[66:67], 0, s[22:23]
	s_sext_i32_i16 s22, s26
	s_bfe_u32 s22, s22, 0x4001b
	s_add_i32 s22, s26, s22
	s_sext_i32_i16 s23, s22
	s_and_b32 s22, s22, 0xfff0
	s_sub_i32 s22, s26, s22
	s_sext_i32_i16 s24, s22
	s_lshl_b32 s22, s23, 2
	s_andn2_b32 s22, s22, 63
	v_lshl_add_u32 v26, s24, 7, v78
	s_ashr_i32 s23, s22, 31
	v_lshl_add_u64 v[18:19], s[22:23], 2, v[18:19]
	v_lshlrev_b32_e32 v72, 2, v68
	v_ashrrev_i32_e32 v27, 31, v26
	v_lshl_add_u64 v[28:29], v[18:19], 0, v[72:73]
	v_lshlrev_b64 v[18:19], 13, v[26:27]
	v_lshl_add_u64 v[30:31], v[28:29], 0, v[18:19]
	v_or_b32_e32 v18, 1, v26
	v_ashrrev_i32_e32 v19, 31, v18
	v_lshlrev_b64 v[18:19], 13, v[18:19]
	v_lshl_add_u64 v[32:33], v[28:29], 0, v[18:19]
	flat_load_dwordx4 v[18:21], v[30:31] nt
	flat_load_dwordx4 v[22:25], v[32:33] nt
	v_or_b32_e32 v30, 2, v26
	v_ashrrev_i32_e32 v31, 31, v30
	v_or_b32_e32 v26, 3, v26
	v_lshlrev_b64 v[30:31], 13, v[30:31]
	v_ashrrev_i32_e32 v27, 31, v26
	v_lshl_add_u64 v[86:87], v[28:29], 0, v[30:31]
	v_lshlrev_b64 v[26:27], 13, v[26:27]
	v_lshl_add_u64 v[88:89], v[28:29], 0, v[26:27]
	flat_load_dwordx4 v[26:29], v[86:87] nt
	flat_load_dwordx4 v[30:33], v[88:89] nt

; #define LAS __attribute__((address_space(3)))
; #define TB_LOAD(R_, t_) do { const int _t = (t_); if (_t < tot) { const int _b = _t / per, _r = _t % per; ttb_load(R_, src + (size_t)_b * K_ * N_, N_, (_r % kt) * 128, (_r / kt) * 64, C.tid); } } while (0)
; __device__ __forceinline__ void ttb_load(TReg& R, const float* src, int ld, int k0, int n0, int tid) {
;     const int kr = tid >> 4, nq = tid & 15;
; #pragma unroll
;     for (int rep = 0; rep < 4; ++rep) R.v[rep] = __builtin_nontemporal_load((const f32x4*)(src + (size_t)(k0 + 4 * kr + rep) * ld + n0 + 4 * nq)); }
; __device__ __forceinline__ void ttb_put(const TReg& R, LAS unsigned* tile, int tid) {
;     const int kr = tid >> 4, nq = tid & 15;
; #pragma unroll
;     for (int c = 0; c < 4; ++c) { const int n = 4 * nq + c;
;         tile[n * 32 + (kr ^ (n & 31))] = pk4_fp8(R.v[0][c] * W_FP8_SCALE, R.v[1][c] * W_FP8_SCALE, R.v[2][c] * W_FP8_SCALE, R.v[3][c] * W_FP8_SCALE); } }
; __device__ __forceinline__ void ttb_finish(LAS const unsigned* tile, unsigned char* dst, int ldd, int k0, int n0, int map, int tid) {
;     const int n = tid >> 3, kq = tid & 7, m = n & 31, ns = n0 + n; int r = ns;
;     if (map == 2) { const int j = ns >> 1, par = ns & 1; r = 256 * (j >> 7) + 128 * par + (j & 127); }
;     const u32x4 g = *(LAS const u32x4*)(tile + n * 32 + 4 * (kq ^ (m >> 2)));
;     const unsigned a0 = (m & 1) ? g.y : g.x, a1 = (m & 1) ? g.x : g.y, a2 = (m & 1) ? g.w : g.z, a3 = (m & 1) ? g.z : g.w;
;     u32x4 w; w.x = (m & 2) ? a2 : a0; w.y = (m & 2) ? a3 : a1; w.z = (m & 2) ? a0 : a2; w.w = (m & 2) ? a1 : a3;
;     __builtin_nontemporal_store(w, (u32x4*)(dst + (size_t)r * ldd + k0 + 16 * kq));
; }
; template <int K_, int N_, int MAP_> __device__ __forceinline__ void tjob_b(const Ctx& C, int bid, int G, const float* src, unsigned char* dstb, int nbatch) {
;     constexpr int kt = K_ / 128, ntile = N_ / 64, per = kt * ntile; const int tot = per * nbatch;
;     TReg R0, R1, R2, R3; int kbuf = 0;
;     ...
;     TB_LOAD(R0, bid); TB_LOAD(R1, bid + G); TB_LOAD(R2, bid + 2 * G); TB_LOAD(R3, bid + 3 * G);
;     for (int t = bid; t < tot; t += 4 * G) { TB_STEP(R0, t); TB_STEP(R1, t + G); TB_STEP(R2, t + 2 * G); TB_STEP(R3, t + 3 * G); }
.LBB0_290:
	v_mul_f32_e32 v72, 0x43800000, v34
	v_mul_f32_e32 v85, 0x43800000, v38
	v_med3_f32 v72, v72, s17, v79
	v_med3_f32 v85, v85, s17, v79
	v_cvt_pk_fp8_f32 v87, v72, v85
	v_mul_f32_e32 v86, 0x43800000, v42
	v_mul_f32_e32 v72, 0x43800000, v46
	v_med3_f32 v85, v86, s17, v79
	v_med3_f32 v72, v72, s17, v79
	v_cvt_pk_fp8_f32 v87, v85, v72 op_sel:[0,0,1]
	s_lshl_b32 s21, s13, 13
	s_add_i32 s21, s21, 0
	v_add3_u32 v72, s21, v1, v80
	ds_write_b32 v72, v87
	v_mul_f32_e32 v72, 0x43800000, v35
	v_mul_f32_e32 v85, 0x43800000, v39
	v_med3_f32 v72, v72, s17, v79
	v_med3_f32 v85, v85, s17, v79
	v_cvt_pk_fp8_f32 v87, v72, v85
	v_mul_f32_e32 v86, 0x43800000, v43
	v_mul_f32_e32 v72, 0x43800000, v47
	v_med3_f32 v85, v86, s17, v79
	v_med3_f32 v72, v72, s17, v79
	v_cvt_pk_fp8_f32 v87, v85, v72 op_sel:[0,0,1]
	v_mul_f32_e32 v72, 0x43800000, v36
	v_mul_f32_e32 v85, 0x43800000, v40
	v_med3_f32 v72, v72, s17, v79
	v_med3_f32 v85, v85, s17, v79
	v_cvt_pk_fp8_f32 v88, v72, v85
	v_mul_f32_e32 v86, 0x43800000, v44
	v_mul_f32_e32 v72, 0x43800000, v48
	v_med3_f32 v85, v86, s17, v79
	v_med3_f32 v72, v72, s17, v79
	v_cvt_pk_fp8_f32 v88, v85, v72 op_sel:[0,0,1]
	v_add3_u32 v72, s21, v69, v81
	ds_write_b32 v72, v87
	v_add3_u32 v72, s21, v74, v82
	ds_write_b32 v72, v88
	v_mul_f32_e32 v72, 0x43800000, v37
	v_mul_f32_e32 v85, 0x43800000, v41
	v_med3_f32 v72, v72, s17, v79
	v_med3_f32 v85, v85, s17, v79
	v_cvt_pk_fp8_f32 v87, v72, v85
	v_mul_f32_e32 v86, 0x43800000, v45
	v_mul_f32_e32 v72, 0x43800000, v49
	v_med3_f32 v85, v86, s17, v79
	v_med3_f32 v72, v72, s17, v79
	v_cvt_pk_fp8_f32 v87, v85, v72 op_sel:[0,0,1]
	s_add_i32 s22, s15, s19
	v_add3_u32 v72, s21, v75, v83
	s_cmpk_gt_i32 s22, 0x15ff
	ds_write_b32 v72, v87
	s_cbranch_scc1 .LBB0_292
	s_ashr_i32 s23, s22, 31
	s_lshr_b32 s23, s23, 23
	s_add_i32 s23, s22, s23
	s_ashr_i32 s24, s23, 9
	s_and_b32 s23, s23, 0xfe00
	s_ashr_i32 s25, s24, 31
	s_sub_i32 s26, s22, s23
	s_lshl_b64 s[22:23], s[24:25], 24
	v_lshl_add_u64 v[34:35], v[66:67], 0, s[22:23]
	s_sext_i32_i16 s22, s26
	s_bfe_u32 s22, s22, 0x4001b
	s_add_i32 s22, s26, s22
	s_sext_i32_i16 s23, s22
	s_and_b32 s22, s22, 0xfff0
	s_sub_i32 s22, s26, s22
	s_sext_i32_i16 s24, s22
	s_lshl_b32 s22, s23, 2
	s_andn2_b32 s22, s22, 63
	v_lshl_add_u32 v42, s24, 7, v78
	s_ashr_i32 s23, s22, 31
	v_lshl_add_u64 v[34:35], s[22:23], 2, v[34:35]
	v_lshlrev_b32_e32 v72, 2, v68
	v_ashrrev_i32_e32 v43, 31, v42
	v_lshl_add_u64 v[44:45], v[34:35], 0, v[72:73]
	v_lshlrev_b64 v[34:35], 13, v[42:43]
	v_lshl_add_u64 v[46:47], v[44:45], 0, v[34:35]
	v_or_b32_e32 v34, 1, v42
	v_ashrrev_i32_e32 v35, 31, v34
	v_lshlrev_b64 v[34:35], 13, v[34:35]
	v_lshl_add_u64 v[48:49], v[44:45], 0, v[34:35]
	flat_load_dwordx4 v[34:37], v[46:47] nt
	flat_load_dwordx4 v[38:41], v[48:49] nt
	v_or_b32_e32 v46, 2, v42
	v_ashrrev_i32_e32 v47, 31, v46
	v_or_b32_e32 v42, 3, v42
	v_lshlrev_b64 v[46:47], 13, v[46:47]
	v_ashrrev_i32_e32 v43, 31, v42
	v_lshl_add_u64 v[86:87], v[44:45], 0, v[46:47]
	v_lshlrev_b64 v[42:43], 13, v[42:43]
	v_lshl_add_u64 v[88:89], v[44:45], 0, v[42:43]
	flat_load_dwordx4 v[42:45], v[86:87] nt
	flat_load_dwordx4 v[46:49], v[88:89] nt

; #define LAS __attribute__((address_space(3)))
; #define TB_LOAD(R_, t_) do { const int _t = (t_); if (_t < tot) { const int _b = _t / per, _r = _t % per; ttb_load(R_, src + (size_t)_b * K_ * N_, N_, (_r % kt) * 128, (_r / kt) * 64, C.tid); } } while (0)
; __device__ __forceinline__ void ttb_load(TReg& R, const float* src, int ld, int k0, int n0, int tid) {
;     const int kr = tid >> 4, nq = tid & 15;
; #pragma unroll
;     for (int rep = 0; rep < 4; ++rep) R.v[rep] = __builtin_nontemporal_load((const f32x4*)(src + (size_t)(k0 + 4 * kr + rep) * ld + n0 + 4 * nq)); }
; __device__ __forceinline__ void ttb_put(const TReg& R, LAS unsigned* tile, int tid) {
;     const int kr = tid >> 4, nq = tid & 15;
; #pragma unroll
;     for (int c = 0; c < 4; ++c) { const int n = 4 * nq + c;
;         tile[n * 32 + (kr ^ (n & 31))] = pk4_fp8(R.v[0][c] * W_FP8_SCALE, R.v[1][c] * W_FP8_SCALE, R.v[2][c] * W_FP8_SCALE, R.v[3][c] * W_FP8_SCALE); } }
; __device__ __forceinline__ void ttb_finish(LAS const unsigned* tile, unsigned char* dst, int ldd, int k0, int n0, int map, int tid) {
;     const int n = tid >> 3, kq = tid & 7, m = n & 31, ns = n0 + n; int r = ns;
;     if (map == 2) { const int j = ns >> 1, par = ns & 1; r = 256 * (j >> 7) + 128 * par + (j & 127); }
;     const u32x4 g = *(LAS const u32x4*)(tile + n * 32 + 4 * (kq ^ (m >> 2)));
;     const unsigned a0 = (m & 1) ? g.y : g.x, a1 = (m & 1) ? g.x : g.y, a2 = (m & 1) ? g.w : g.z, a3 = (m & 1) ? g.z : g.w;
;     u32x4 w; w.x = (m & 2) ? a2 : a0; w.y = (m & 2) ? a3 : a1; w.z = (m & 2) ? a0 : a2; w.w = (m & 2) ? a1 : a3;
;     __builtin_nontemporal_store(w, (u32x4*)(dst + (size_t)r * ldd + k0 + 16 * kq));
; }
; template <int K_, int N_, int MAP_> __device__ __forceinline__ void tjob_b(const Ctx& C, int bid, int G, const float* src, unsigned char* dstb, int nbatch) {
;     constexpr int kt = K_ / 128, ntile = N_ / 64, per = kt * ntile; const int tot = per * nbatch;
;     TReg R0, R1, R2, R3; int kbuf = 0;
;     ...
;     TB_LOAD(R0, bid); TB_LOAD(R1, bid + G); TB_LOAD(R2, bid + 2 * G); TB_LOAD(R3, bid + 3 * G);
;     for (int t = bid; t < tot; t += 4 * G) { TB_STEP(R0, t); TB_STEP(R1, t + G); TB_STEP(R2, t + 2 * G); TB_STEP(R3, t + 3 * G); }
.LBB0_293:
	s_add_i32 s20, s11, s19
	s_cmpk_gt_i32 s20, 0x15ff
	s_cbranch_scc1 .LBB0_282
	v_mul_f32_e32 v72, 0x43800000, v50
	v_mul_f32_e32 v85, 0x43800000, v54
	v_med3_f32 v72, v72, s17, v79
	v_med3_f32 v85, v85, s17, v79
	v_cvt_pk_fp8_f32 v87, v72, v85
	v_mul_f32_e32 v86, 0x43800000, v58
	v_mul_f32_e32 v72, 0x43800000, v62
	v_med3_f32 v85, v86, s17, v79
	v_med3_f32 v72, v72, s17, v79
	v_cvt_pk_fp8_f32 v87, v85, v72 op_sel:[0,0,1]
	s_lshl_b32 s21, s13, 13
	s_add_i32 s21, s21, 0
	v_add3_u32 v72, s21, v1, v80
	ds_write_b32 v72, v87
	v_mul_f32_e32 v72, 0x43800000, v51
	v_mul_f32_e32 v85, 0x43800000, v55
	v_med3_f32 v72, v72, s17, v79
	v_med3_f32 v85, v85, s17, v79
	v_cvt_pk_fp8_f32 v87, v72, v85
	v_mul_f32_e32 v86, 0x43800000, v59
	v_mul_f32_e32 v72, 0x43800000, v63
	v_med3_f32 v85, v86, s17, v79
	v_med3_f32 v72, v72, s17, v79
	v_cvt_pk_fp8_f32 v87, v85, v72 op_sel:[0,0,1]
	v_mul_f32_e32 v72, 0x43800000, v52
	v_mul_f32_e32 v85, 0x43800000, v56
	v_med3_f32 v72, v72, s17, v79
	v_med3_f32 v85, v85, s17, v79
	v_cvt_pk_fp8_f32 v88, v72, v85
	v_mul_f32_e32 v86, 0x43800000, v60
	v_mul_f32_e32 v72, 0x43800000, v64
	v_med3_f32 v85, v86, s17, v79
	v_med3_f32 v72, v72, s17, v79
	v_cvt_pk_fp8_f32 v88, v85, v72 op_sel:[0,0,1]
	v_add3_u32 v72, s21, v69, v81
	ds_write_b32 v72, v87
	v_add3_u32 v72, s21, v74, v82
	ds_write_b32 v72, v88
	v_mul_f32_e32 v72, 0x43800000, v53
	v_mul_f32_e32 v85, 0x43800000, v57
	v_med3_f32 v72, v72, s17, v79
	v_med3_f32 v85, v85, s17, v79
	v_cvt_pk_fp8_f32 v87, v72, v85
	v_mul_f32_e32 v86, 0x43800000, v61
	v_mul_f32_e32 v72, 0x43800000, v65
	v_med3_f32 v85, v86, s17, v79
	v_med3_f32 v72, v72, s17, v79
	v_cvt_pk_fp8_f32 v87, v85, v72 op_sel:[0,0,1]
	s_add_i32 s19, s14, s19
	v_add3_u32 v72, s21, v75, v83
	s_cmpk_gt_i32 s19, 0x15ff
	ds_write_b32 v72, v87
	s_cbranch_scc1 .LBB0_281
	s_ashr_i32 s22, s19, 31
	s_lshr_b32 s22, s22, 23
	s_add_i32 s23, s19, s22
	s_ashr_i32 s22, s23, 9
	s_and_b32 s23, s23, 0xfe00
	s_sub_i32 s19, s19, s23
	s_ashr_i32 s23, s22, 31
	s_lshl_b64 s[22:23], s[22:23], 24
	v_lshl_add_u64 v[50:51], v[66:67], 0, s[22:23]
	s_sext_i32_i16 s22, s19
	s_bfe_u32 s22, s22, 0x4001b
	s_add_i32 s22, s19, s22
	s_sext_i32_i16 s23, s22
	s_and_b32 s22, s22, 0xfff0
	s_sub_i32 s19, s19, s22
	s_lshl_b32 s22, s23, 2
	s_sext_i32_i16 s19, s19
	s_andn2_b32 s22, s22, 63
	v_lshl_add_u32 v58, s19, 7, v78
	s_ashr_i32 s23, s22, 31
	v_lshl_add_u64 v[50:51], s[22:23], 2, v[50:51]
	v_lshlrev_b32_e32 v72, 2, v68
	v_ashrrev_i32_e32 v59, 31, v58
	v_lshl_add_u64 v[60:61], v[50:51], 0, v[72:73]
	v_lshlrev_b64 v[50:51], 13, v[58:59]
	v_lshl_add_u64 v[62:63], v[60:61], 0, v[50:51]
	v_or_b32_e32 v50, 1, v58
	v_ashrrev_i32_e32 v51, 31, v50
	v_lshlrev_b64 v[50:51], 13, v[50:51]
	v_lshl_add_u64 v[64:65], v[60:61], 0, v[50:51]
	flat_load_dwordx4 v[50:53], v[62:63] nt
	flat_load_dwordx4 v[54:57], v[64:65] nt
	v_or_b32_e32 v62, 2, v58
	v_ashrrev_i32_e32 v63, 31, v62
	v_or_b32_e32 v58, 3, v58
	v_lshlrev_b64 v[62:63], 13, v[62:63]
	v_ashrrev_i32_e32 v59, 31, v58
	v_lshl_add_u64 v[86:87], v[60:61], 0, v[62:63]
	v_lshlrev_b64 v[58:59], 13, v[58:59]
	v_lshl_add_u64 v[88:89], v[60:61], 0, v[58:59]
	flat_load_dwordx4 v[58:61], v[86:87] nt
	flat_load_dwordx4 v[62:65], v[88:89] nt
	s_branch .LBB0_281

; #define LAS __attribute__((address_space(3)))
;     __device__ __forceinline__ void operator()(const f32x4 (&acc)[2][2][4][2], const Unit& u, int wr, int wc, int fr, int fq, LAS const unsigned char* tbl, LAS const unsigned char* b2l) const {
;         { int t_ = threadIdx.x; asm volatile("" : "+v"(t_)); fr = t_ & 15; fq = (t_ >> 4) & 3; }
;         const int row0 = u.pm * BM + wr * 64 + fr; const int cl = wc * 32 + 8 * fq; const int col0 = u.pn * HALF + cl;
;         unsigned char* act = ws + WS_ACT;
;         typedef float f32x2_ __attribute__((ext_vector_type(2)));
;         f32x4 gb[2], lb[2]; gb[0] = *(LAS const f32x4*)(tbl + 1024 + cl * 4); gb[1] = *(LAS const f32x4*)(tbl + 1024 + cl * 4 + 16); lb[0] = *(LAS const f32x4*)(tbl + 1536 + cl * 4) + 1.0f; lb[1] = *(LAS const f32x4*)(tbl + 1536 + cl * 4 + 16) + 1.0f;
;         const f32x2_ sc2 = {1.0f / W_FP8_SCALE, 1.0f / W_FP8_SCALE}, ce2 = {-1.702f * 1.4426950409f, -1.702f * 1.4426950409f}, one2 = {1.0f, 1.0f};
; #pragma unroll
;         for (int ai = 0; ai < 2; ++ai)
; #pragma unroll
;             for (int m = 0; m < 4; ++m) { unsigned char* rowp = act + (size_t)(row0 + ai * HALF + m * 16) * FF + col0; f32x2_ o[4];
; #pragma unroll
;                 for (int n = 0; n < 2; ++n)
; #pragma unroll
;                     for (int h = 0; h < 2; ++h) { const f32x4 ag = acc[ai][0][m][n], al = acc[ai][1][m][n];
;                         const f32x2_ a2 = {ag[2 * h], ag[2 * h + 1]}, b2 = {al[2 * h], al[2 * h + 1]}, g2 = {gb[n][2 * h], gb[n][2 * h + 1]}, l2 = {lb[n][2 * h], lb[n][2 * h + 1]};
;                         f32x2_ gv = __builtin_elementwise_fma(a2, sc2, g2), lv = __builtin_elementwise_fma(b2, sc2, l2);
;                         gv[0] = fminf(gv[0], 7.0f); gv[1] = fminf(gv[1], 7.0f); lv[0] = __builtin_amdgcn_fmed3f(lv[0], -6.0f, 8.0f); lv[1] = __builtin_amdgcn_fmed3f(lv[1], -6.0f, 8.0f);
;                         f32x2_ e = gv * ce2; e[0] = __builtin_amdgcn_exp2f(e[0]); e[1] = __builtin_amdgcn_exp2f(e[1]); e = e + one2; e[0] = __builtin_amdgcn_rcpf(e[0]); e[1] = __builtin_amdgcn_rcpf(e[1]);
;                         o[n * 2 + h] = (gv * e) * lv; }
.LBB0_979:
	v_mov_b32_e32 v2, v0
	s_lshl_b32 s18, s66, 8
	s_lshl_b32 s1, s69, 11
	s_add_i32 s18, s18, s43
	s_add_i32 s1, s1, 0
	v_and_or_b32 v146, v2, 15, s18
	v_lshrrev_b32_e32 v2, 1, v2
	s_add_i32 s1, s1, 0x20000
	v_and_or_b32 v2, v2, 24, s44
	v_lshl_add_u32 v3, v2, 2, s1
	ds_read_b128 v[10:13], v3 offset:1536
	v_lshl_or_b32 v152, s67, 7, v2
	ds_read_b128 v[148:151], v3 offset:1552
	ds_read_b128 v[6:9], v3 offset:1024
	ds_read_b128 v[2:5], v3 offset:1040
	v_ashrrev_i32_e32 v153, 31, v152
	v_ashrrev_i32_e32 v147, 31, v146
	s_waitcnt lgkmcnt(3)
	v_pk_add_f32 v[14:15], v[12:13], 1.0 op_sel_hi:[1,0]
	s_waitcnt lgkmcnt(1)
	v_pk_fma_f32 v[142:143], v[142:143], s[26:27], v[6:7] op_sel_hi:[1,0,1]
	v_pk_add_f32 v[12:13], v[148:149], 1.0 op_sel_hi:[1,0]
	v_min_f32_e32 v148, 0x40e00000, v142
	v_min_f32_e32 v149, 0x40e00000, v143
	v_pk_mul_f32 v[142:143], v[148:149], s[28:29] op_sel_hi:[1,0]
	v_pk_add_f32 v[16:17], v[10:11], 1.0 op_sel_hi:[1,0]
	v_pk_add_f32 v[10:11], v[150:151], 1.0 op_sel_hi:[1,0]
	v_exp_f32_e32 v150, v142
	v_exp_f32_e32 v151, v143
	v_pk_fma_f32 v[144:145], v[144:145], s[26:27], v[8:9] op_sel_hi:[1,0,1]
	v_pk_fma_f32 v[138:139], v[138:139], s[26:27], v[16:17] op_sel_hi:[1,0,1]
	v_min_f32_e32 v144, 0x40e00000, v144
	v_pk_add_f32 v[150:151], v[150:151], 1.0 op_sel_hi:[1,0]
	v_min_f32_e32 v145, 0x40e00000, v145
	v_rcp_f32_e32 v150, v150
	v_rcp_f32_e32 v151, v151
	v_med3_f32 v138, v138, s55, v179
	v_med3_f32 v139, v139, s55, v179
	s_waitcnt lgkmcnt(0)
	v_pk_fma_f32 v[134:135], v[134:135], s[26:27], v[2:3] op_sel_hi:[1,0,1]
	v_pk_mul_f32 v[148:149], v[148:149], v[150:151]
	v_pk_mul_f32 v[150:151], v[144:145], s[28:29] op_sel_hi:[1,0]
	v_pk_mul_f32 v[138:139], v[138:139], v[148:149]
	v_exp_f32_e32 v150, v150
	v_exp_f32_e32 v151, v151
	v_min_f32_e32 v134, 0x40e00000, v134
	v_min_f32_e32 v135, 0x40e00000, v135
	v_pk_fma_f32 v[140:141], v[140:141], s[26:27], v[14:15] op_sel_hi:[1,0,1]
	v_pk_add_f32 v[148:149], v[150:151], 1.0 op_sel_hi:[1,0]
	v_pk_mul_f32 v[150:151], v[134:135], s[28:29] op_sel_hi:[1,0]
	v_rcp_f32_e32 v148, v148
	v_rcp_f32_e32 v149, v149
	v_exp_f32_e32 v150, v150
	v_exp_f32_e32 v151, v151
	v_med3_f32 v140, v140, s55, v179
	v_med3_f32 v141, v141, s55, v179
	v_pk_mul_f32 v[144:145], v[144:145], v[148:149]
	v_pk_fma_f32 v[130:131], v[130:131], s[26:27], v[12:13] op_sel_hi:[1,0,1]
	v_pk_mul_f32 v[140:141], v[140:141], v[144:145]
	v_pk_add_f32 v[144:145], v[150:151], 1.0 op_sel_hi:[1,0]
	v_med3_f32 v130, v130, s55, v179
	v_rcp_f32_e32 v144, v144
	v_rcp_f32_e32 v145, v145
	v_med3_f32 v131, v131, s55, v179
	v_pk_fma_f32 v[132:133], v[132:133], s[26:27], v[10:11] op_sel_hi:[1,0,1]
	v_pk_fma_f32 v[126:127], v[126:127], s[26:27], v[6:7] op_sel_hi:[1,0,1]
	v_pk_mul_f32 v[134:135], v[134:135], v[144:145]
	v_pk_mul_f32 v[130:131], v[130:131], v[134:135]
	v_pk_fma_f32 v[134:135], v[136:137], s[26:27], v[4:5] op_sel_hi:[1,0,1]
	v_cvt_pk_fp8_f32 v145, v130, v131
	v_min_f32_e32 v134, 0x40e00000, v134
	v_min_f32_e32 v135, 0x40e00000, v135
	v_pk_mul_f32 v[136:137], v[134:135], s[28:29] op_sel_hi:[1,0]
	v_med3_f32 v132, v132, s55, v179
	v_exp_f32_e32 v136, v136
	v_exp_f32_e32 v137, v137
	v_med3_f32 v133, v133, s55, v179
	v_pk_fma_f32 v[128:129], v[128:129], s[26:27], v[8:9] op_sel_hi:[1,0,1]
	v_pk_fma_f32 v[122:123], v[122:123], s[26:27], v[16:17] op_sel_hi:[1,0,1]
	v_pk_add_f32 v[136:137], v[136:137], 1.0 op_sel_hi:[1,0]
	v_min_f32_e32 v128, 0x40e00000, v128
	v_rcp_f32_e32 v136, v136
	v_rcp_f32_e32 v137, v137
	v_min_f32_e32 v129, 0x40e00000, v129
	v_med3_f32 v122, v122, s55, v179
	v_med3_f32 v123, v123, s55, v179
	v_pk_mul_f32 v[130:131], v[134:135], v[136:137]
	v_pk_fma_f32 v[118:119], v[118:119], s[26:27], v[2:3] op_sel_hi:[1,0,1]
	v_pk_mul_f32 v[130:131], v[132:133], v[130:131]
	v_min_f32_e32 v118, 0x40e00000, v118
	v_cvt_pk_fp8_f32 v145, v130, v131 op_sel:[0,0,1]
	v_min_f32_e32 v130, 0x40e00000, v126
	v_min_f32_e32 v131, 0x40e00000, v127
	v_pk_mul_f32 v[126:127], v[130:131], s[28:29] op_sel_hi:[1,0]
	v_min_f32_e32 v119, 0x40e00000, v119
	v_exp_f32_e32 v132, v126
	v_exp_f32_e32 v133, v127
	v_pk_fma_f32 v[124:125], v[124:125], s[26:27], v[14:15] op_sel_hi:[1,0,1]
	v_pk_fma_f32 v[114:115], v[114:115], s[26:27], v[12:13] op_sel_hi:[1,0,1]
	v_med3_f32 v124, v124, s55, v179
	v_pk_add_f32 v[132:133], v[132:133], 1.0 op_sel_hi:[1,0]
	v_med3_f32 v125, v125, s55, v179
	v_rcp_f32_e32 v132, v132
	v_rcp_f32_e32 v133, v133
	v_med3_f32 v114, v114, s55, v179
	v_med3_f32 v115, v115, s55, v179
	v_pk_fma_f32 v[116:117], v[116:117], s[26:27], v[10:11] op_sel_hi:[1,0,1]
	v_pk_mul_f32 v[130:131], v[130:131], v[132:133]
	v_pk_mul_f32 v[132:133], v[128:129], s[28:29] op_sel_hi:[1,0]
	v_pk_mul_f32 v[122:123], v[122:123], v[130:131]
	v_exp_f32_e32 v132, v132
	v_exp_f32_e32 v133, v133
	v_pk_fma_f32 v[30:31], v[30:31], s[26:27], v[6:7] op_sel_hi:[1,0,1]
	v_med3_f32 v116, v116, s55, v179
	v_med3_f32 v117, v117, s55, v179
	v_pk_add_f32 v[130:131], v[132:133], 1.0 op_sel_hi:[1,0]
	v_pk_mul_f32 v[132:133], v[118:119], s[28:29] op_sel_hi:[1,0]
	v_rcp_f32_e32 v130, v130
	v_rcp_f32_e32 v131, v131
	v_exp_f32_e32 v132, v132
	v_exp_f32_e32 v133, v133
	v_min_f32_e32 v30, 0x40e00000, v30
	v_pk_mul_f32 v[128:129], v[128:129], v[130:131]
	v_min_f32_e32 v31, 0x40e00000, v31
	v_pk_mul_f32 v[124:125], v[124:125], v[128:129]
	v_pk_add_f32 v[128:129], v[132:133], 1.0 op_sel_hi:[1,0]
	v_pk_fma_f32 v[32:33], v[32:33], s[26:27], v[8:9] op_sel_hi:[1,0,1]
	v_rcp_f32_e32 v128, v128
	v_rcp_f32_e32 v129, v129
	v_min_f32_e32 v32, 0x40e00000, v32
	v_min_f32_e32 v33, 0x40e00000, v33
	v_pk_fma_f32 v[110:111], v[110:111], s[26:27], v[16:17] op_sel_hi:[1,0,1]
	v_pk_mul_f32 v[118:119], v[118:119], v[128:129]
;     __device__ __forceinline__ void operator()(const f32x4 (&acc)[2][2][4][2], const Unit& u, int wr, int wc, int fr, int fq, LAS const unsigned char* tbl, LAS const unsigned char* b2l) const {
;     ...
;             for (int m = 0; m < 4; ++m) { unsigned char* rowp = act + (size_t)(row0 + ai * HALF + m * 16) * FF + col0; f32x2_ o[4];
; #pragma unroll
;                 for (int n = 0; n < 2; ++n)
; #pragma unroll
;                     for (int h = 0; h < 2; ++h) { const f32x4 ag = acc[ai][0][m][n], al = acc[ai][1][m][n];
;                         const f32x2_ a2 = {ag[2 * h], ag[2 * h + 1]}, b2 = {al[2 * h], al[2 * h + 1]}, g2 = {gb[n][2 * h], gb[n][2 * h + 1]}, l2 = {lb[n][2 * h], lb[n][2 * h + 1]};
;                         f32x2_ gv = __builtin_elementwise_fma(a2, sc2, g2), lv = __builtin_elementwise_fma(b2, sc2, l2);
;                         gv[0] = fminf(gv[0], 7.0f); gv[1] = fminf(gv[1], 7.0f); lv[0] = __builtin_amdgcn_fmed3f(lv[0], -6.0f, 8.0f); lv[1] = __builtin_amdgcn_fmed3f(lv[1], -6.0f, 8.0f);
;                         f32x2_ e = gv * ce2; e[0] = __builtin_amdgcn_exp2f(e[0]); e[1] = __builtin_amdgcn_exp2f(e[1]); e = e + one2; e[0] = __builtin_amdgcn_rcpf(e[0]); e[1] = __builtin_amdgcn_rcpf(e[1]);
;                         o[n * 2 + h] = (gv * e) * lv; }
;                 u32x2 w; int p0 = __builtin_amdgcn_cvt_pk_fp8_f32(o[0][0], o[0][1], 0, false); p0 = __builtin_amdgcn_cvt_pk_fp8_f32(o[1][0], o[1][1], p0, true);
;                 int p1 = __builtin_amdgcn_cvt_pk_fp8_f32(o[2][0], o[2][1], 0, false); p1 = __builtin_amdgcn_cvt_pk_fp8_f32(o[3][0], o[3][1], p1, true); w.x = (unsigned)p0; w.y = (unsigned)p1;
	v_pk_mul_f32 v[114:115], v[114:115], v[118:119]
	v_pk_fma_f32 v[118:119], v[120:121], s[26:27], v[4:5] op_sel_hi:[1,0,1]
	v_cvt_pk_fp8_f32 v129, v114, v115
	v_min_f32_e32 v118, 0x40e00000, v118
	v_min_f32_e32 v119, 0x40e00000, v119
	v_pk_mul_f32 v[120:121], v[118:119], s[28:29] op_sel_hi:[1,0]
	v_med3_f32 v110, v110, s55, v179
	v_exp_f32_e32 v120, v120
	v_exp_f32_e32 v121, v121
	v_med3_f32 v111, v111, s55, v179
	v_pk_fma_f32 v[26:27], v[26:27], s[26:27], v[2:3] op_sel_hi:[1,0,1]
	v_pk_fma_f32 v[112:113], v[112:113], s[26:27], v[14:15] op_sel_hi:[1,0,1]
	v_pk_add_f32 v[120:121], v[120:121], 1.0 op_sel_hi:[1,0]
	v_min_f32_e32 v26, 0x40e00000, v26
	v_rcp_f32_e32 v120, v120
	v_rcp_f32_e32 v121, v121
	v_min_f32_e32 v27, 0x40e00000, v27
	v_pk_fma_f32 v[28:29], v[28:29], s[26:27], v[4:5] op_sel_hi:[1,0,1]
	v_med3_f32 v112, v112, s55, v179
	v_pk_mul_f32 v[114:115], v[118:119], v[120:121]
	v_pk_mul_f32 v[118:119], v[32:33], s[28:29] op_sel_hi:[1,0]
	v_pk_mul_f32 v[114:115], v[116:117], v[114:115]
	v_pk_mul_f32 v[116:117], v[30:31], s[28:29] op_sel_hi:[1,0]
	v_exp_f32_e32 v118, v118
	v_exp_f32_e32 v116, v116
	v_exp_f32_e32 v117, v117
	v_exp_f32_e32 v119, v119
	v_med3_f32 v113, v113, s55, v179
	v_min_f32_e32 v28, 0x40e00000, v28
	v_pk_add_f32 v[116:117], v[116:117], 1.0 op_sel_hi:[1,0]
	v_min_f32_e32 v29, 0x40e00000, v29
	v_rcp_f32_e32 v116, v116
	v_rcp_f32_e32 v117, v117
	v_pk_fma_f32 v[106:107], v[106:107], s[26:27], v[12:13] op_sel_hi:[1,0,1]
	v_pk_fma_f32 v[108:109], v[108:109], s[26:27], v[10:11] op_sel_hi:[1,0,1]
	v_med3_f32 v106, v106, s55, v179
	v_pk_mul_f32 v[30:31], v[30:31], v[116:117]
	v_med3_f32 v107, v107, s55, v179
	v_pk_mul_f32 v[30:31], v[110:111], v[30:31]
	v_pk_add_f32 v[110:111], v[118:119], 1.0 op_sel_hi:[1,0]
	v_med3_f32 v108, v108, s55, v179
	v_rcp_f32_e32 v110, v110
	v_rcp_f32_e32 v111, v111
	v_med3_f32 v109, v109, s55, v179
	v_pk_fma_f32 v[22:23], v[22:23], s[26:27], v[6:7] op_sel_hi:[1,0,1]
	v_pk_fma_f32 v[24:25], v[24:25], s[26:27], v[8:9] op_sel_hi:[1,0,1]
	v_pk_mul_f32 v[32:33], v[32:33], v[110:111]
	v_pk_mul_f32 v[110:111], v[26:27], s[28:29] op_sel_hi:[1,0]
	v_pk_mul_f32 v[32:33], v[112:113], v[32:33]
	v_exp_f32_e32 v110, v110
	v_exp_f32_e32 v111, v111
	v_pk_mul_f32 v[112:113], v[28:29], s[28:29] op_sel_hi:[1,0]
	v_min_f32_e32 v22, 0x40e00000, v22
	v_exp_f32_e32 v112, v112
	v_pk_add_f32 v[110:111], v[110:111], 1.0 op_sel_hi:[1,0]
	v_exp_f32_e32 v113, v113
	v_rcp_f32_e32 v110, v110
	v_rcp_f32_e32 v111, v111
	v_min_f32_e32 v23, 0x40e00000, v23
	v_min_f32_e32 v24, 0x40e00000, v24
	v_min_f32_e32 v25, 0x40e00000, v25
	v_pk_mul_f32 v[26:27], v[26:27], v[110:111]
	v_pk_fma_f32 v[18:19], v[18:19], s[26:27], v[2:3] op_sel_hi:[1,0,1]
	v_pk_mul_f32 v[26:27], v[106:107], v[26:27]
	v_pk_add_f32 v[106:107], v[112:113], 1.0 op_sel_hi:[1,0]
	v_min_f32_e32 v18, 0x40e00000, v18
	v_rcp_f32_e32 v106, v106
	v_rcp_f32_e32 v107, v107
	v_min_f32_e32 v19, 0x40e00000, v19
	v_pk_fma_f32 v[20:21], v[20:21], s[26:27], v[4:5] op_sel_hi:[1,0,1]
	v_pk_mul_f32 v[28:29], v[28:29], v[106:107]
	v_cvt_pk_fp8_f32 v107, v26, v27
	v_pk_mul_f32 v[26:27], v[108:109], v[28:29]
	v_cvt_pk_fp8_f32 v106, v30, v31
	v_cvt_pk_fp8_f32 v107, v26, v27 op_sel:[0,0,1]
	v_pk_mul_f32 v[26:27], v[22:23], s[28:29] op_sel_hi:[1,0]
	v_min_f32_e32 v20, 0x40e00000, v20
	v_exp_f32_e32 v26, v26
	v_exp_f32_e32 v27, v27
	v_cvt_pk_fp8_f32 v106, v32, v33 op_sel:[0,0,1]
	v_pk_mul_f32 v[32:33], v[18:19], s[28:29] op_sel_hi:[1,0]
	v_min_f32_e32 v21, 0x40e00000, v21
	v_pk_add_f32 v[26:27], v[26:27], 1.0 op_sel_hi:[1,0]
	v_exp_f32_e32 v32, v32
	v_rcp_f32_e32 v26, v26
	v_rcp_f32_e32 v27, v27
	v_exp_f32_e32 v33, v33
	v_pk_fma_f32 v[30:31], v[102:103], s[26:27], v[16:17] op_sel_hi:[1,0,1]
	v_cvt_pk_fp8_f32 v128, v122, v123
	v_pk_mul_f32 v[22:23], v[22:23], v[26:27]
	v_pk_mul_f32 v[26:27], v[24:25], s[28:29] op_sel_hi:[1,0]
	v_med3_f32 v30, v30, s55, v179
	v_exp_f32_e32 v26, v26
	v_exp_f32_e32 v27, v27
	v_med3_f32 v31, v31, s55, v179
	v_pk_mul_f32 v[22:23], v[30:31], v[22:23]
	v_pk_fma_f32 v[30:31], v[104:105], s[26:27], v[14:15] op_sel_hi:[1,0,1]
	v_pk_add_f32 v[26:27], v[26:27], 1.0 op_sel_hi:[1,0]
	v_med3_f32 v30, v30, s55, v179
	v_rcp_f32_e32 v26, v26
	v_rcp_f32_e32 v27, v27
	v_med3_f32 v31, v31, s55, v179
	v_or_b32_e32 v134, 16, v146
	v_cvt_pk_fp8_f32 v128, v124, v125 op_sel:[0,0,1]
	v_pk_mul_f32 v[24:25], v[24:25], v[26:27]
	v_pk_add_f32 v[26:27], v[32:33], 1.0 op_sel_hi:[1,0]
	v_pk_mul_f32 v[24:25], v[30:31], v[24:25]
	v_rcp_f32_e32 v26, v26
	v_rcp_f32_e32 v27, v27
	v_pk_fma_f32 v[30:31], v[98:99], s[26:27], v[12:13] op_sel_hi:[1,0,1]
	v_med3_f32 v30, v30, s55, v179
	v_pk_mul_f32 v[18:19], v[18:19], v[26:27]
	v_pk_mul_f32 v[26:27], v[20:21], s[28:29] op_sel_hi:[1,0]
	v_med3_f32 v31, v31, s55, v179
	v_exp_f32_e32 v26, v26
	v_exp_f32_e32 v27, v27
	v_pk_mul_f32 v[18:19], v[30:31], v[18:19]
	v_pk_fma_f32 v[30:31], v[100:101], s[26:27], v[10:11] op_sel_hi:[1,0,1]
	v_cvt_pk_fp8_f32 v33, v18, v19
	v_pk_add_f32 v[26:27], v[26:27], 1.0 op_sel_hi:[1,0]
	v_med3_f32 v30, v30, s55, v179
	v_rcp_f32_e32 v26, v26
	v_rcp_f32_e32 v27, v27
	v_med3_f32 v31, v31, s55, v179
	v_cvt_pk_fp8_f32 v129, v114, v115 op_sel:[0,0,1]
	v_pk_mul_f32 v[18:19], v[20:21], v[26:27]
	v_ashrrev_i32_e32 v135, 31, v134
	v_pk_mul_f32 v[18:19], v[30:31], v[18:19]
	v_cvt_pk_fp8_f32 v32, v22, v23
	v_cvt_pk_fp8_f32 v33, v18, v19 op_sel:[0,0,1]
	v_pk_fma_f32 v[18:19], v[94:95], s[26:27], v[6:7] op_sel_hi:[1,0,1]
	v_lshl_add_u64 v[142:143], s[6:7], 0, v[152:153]
	v_min_f32_e32 v18, 0x40e00000, v18
	v_min_f32_e32 v19, 0x40e00000, v19
	v_pk_mul_f32 v[20:21], v[18:19], s[28:29] op_sel_hi:[1,0]
	v_lshlrev_b64 v[114:115], 11, v[134:135]
;     __device__ __forceinline__ void operator()(const f32x4 (&acc)[2][2][4][2], const Unit& u, int wr, int wc, int fr, int fq, LAS const unsigned char* tbl, LAS const unsigned char* b2l) const {
;     ...
;             for (int m = 0; m < 4; ++m) { unsigned char* rowp = act + (size_t)(row0 + ai * HALF + m * 16) * FF + col0; f32x2_ o[4];
; #pragma unroll
;                 for (int n = 0; n < 2; ++n)
; #pragma unroll
;                     for (int h = 0; h < 2; ++h) { const f32x4 ag = acc[ai][0][m][n], al = acc[ai][1][m][n];
;                         const f32x2_ a2 = {ag[2 * h], ag[2 * h + 1]}, b2 = {al[2 * h], al[2 * h + 1]}, g2 = {gb[n][2 * h], gb[n][2 * h + 1]}, l2 = {lb[n][2 * h], lb[n][2 * h + 1]};
;                         f32x2_ gv = __builtin_elementwise_fma(a2, sc2, g2), lv = __builtin_elementwise_fma(b2, sc2, l2);
;                         gv[0] = fminf(gv[0], 7.0f); gv[1] = fminf(gv[1], 7.0f); lv[0] = __builtin_amdgcn_fmed3f(lv[0], -6.0f, 8.0f); lv[1] = __builtin_amdgcn_fmed3f(lv[1], -6.0f, 8.0f);
;                         f32x2_ e = gv * ce2; e[0] = __builtin_amdgcn_exp2f(e[0]); e[1] = __builtin_amdgcn_exp2f(e[1]); e = e + one2; e[0] = __builtin_amdgcn_rcpf(e[0]); e[1] = __builtin_amdgcn_rcpf(e[1]);
;                         o[n * 2 + h] = (gv * e) * lv; }
;                 u32x2 w; int p0 = __builtin_amdgcn_cvt_pk_fp8_f32(o[0][0], o[0][1], 0, false); p0 = __builtin_amdgcn_cvt_pk_fp8_f32(o[1][0], o[1][1], p0, true);
;                 int p1 = __builtin_amdgcn_cvt_pk_fp8_f32(o[2][0], o[2][1], 0, false); p1 = __builtin_amdgcn_cvt_pk_fp8_f32(o[3][0], o[3][1], p1, true); w.x = (unsigned)p0; w.y = (unsigned)p1;
;                 *(u32x2*)rowp = w; }
	v_exp_f32_e32 v20, v20
	v_exp_f32_e32 v21, v21
	v_lshl_add_u64 v[114:115], v[142:143], 0, v[114:115]
	global_store_dwordx2 v[114:115], v[128:129], off
	v_or_b32_e32 v114, 32, v146
	v_pk_add_f32 v[20:21], v[20:21], 1.0 op_sel_hi:[1,0]
	v_ashrrev_i32_e32 v115, 31, v114
	v_rcp_f32_e32 v20, v20
	v_rcp_f32_e32 v21, v21
	v_cvt_pk_fp8_f32 v32, v24, v25 op_sel:[0,0,1]
	v_lshlrev_b64 v[114:115], 11, v[114:115]
	v_lshl_add_u64 v[28:29], v[142:143], 0, v[114:115]
	v_pk_mul_f32 v[18:19], v[18:19], v[20:21]
	v_pk_fma_f32 v[20:21], v[96:97], s[26:27], v[8:9] op_sel_hi:[1,0,1]
	global_store_dwordx2 v[28:29], v[106:107], off
	v_min_f32_e32 v20, 0x40e00000, v20
	v_min_f32_e32 v21, 0x40e00000, v21
	v_pk_mul_f32 v[24:25], v[20:21], s[28:29] op_sel_hi:[1,0]
	v_or_b32_e32 v28, 48, v146
	v_exp_f32_e32 v24, v24
	v_exp_f32_e32 v25, v25
	v_ashrrev_i32_e32 v29, 31, v28
	v_pk_fma_f32 v[26:27], v[86:87], s[26:27], v[2:3] op_sel_hi:[1,0,1]
	v_lshlrev_b64 v[22:23], 11, v[28:29]
	v_pk_add_f32 v[24:25], v[24:25], 1.0 op_sel_hi:[1,0]
	v_min_f32_e32 v26, 0x40e00000, v26
	v_min_f32_e32 v27, 0x40e00000, v27
	v_lshl_add_u64 v[22:23], v[142:143], 0, v[22:23]
	v_rcp_f32_e32 v24, v24
	v_rcp_f32_e32 v25, v25
	v_pk_mul_f32 v[28:29], v[26:27], s[28:29] op_sel_hi:[1,0]
	global_store_dwordx2 v[22:23], v[32:33], off
	v_pk_fma_f32 v[22:23], v[90:91], s[26:27], v[16:17] op_sel_hi:[1,0,1]
	v_exp_f32_e32 v28, v28
	v_exp_f32_e32 v29, v29
	v_med3_f32 v22, v22, s55, v179
	v_med3_f32 v23, v23, s55, v179
	v_pk_mul_f32 v[18:19], v[22:23], v[18:19]
	v_pk_fma_f32 v[22:23], v[92:93], s[26:27], v[14:15] op_sel_hi:[1,0,1]
	v_pk_mul_f32 v[20:21], v[20:21], v[24:25]
	v_med3_f32 v22, v22, s55, v179
	v_med3_f32 v23, v23, s55, v179
	v_pk_mul_f32 v[20:21], v[22:23], v[20:21]
	v_pk_add_f32 v[22:23], v[28:29], 1.0 op_sel_hi:[1,0]
	v_pk_fma_f32 v[24:25], v[82:83], s[26:27], v[12:13] op_sel_hi:[1,0,1]
	v_rcp_f32_e32 v22, v22
	v_rcp_f32_e32 v23, v23
	v_med3_f32 v24, v24, s55, v179
	v_med3_f32 v25, v25, s55, v179
	v_pk_mul_f32 v[22:23], v[26:27], v[22:23]
	v_pk_fma_f32 v[28:29], v[84:85], s[26:27], v[10:11] op_sel_hi:[1,0,1]
	v_pk_mul_f32 v[22:23], v[24:25], v[22:23]
	v_pk_fma_f32 v[24:25], v[88:89], s[26:27], v[4:5] op_sel_hi:[1,0,1]
	v_cvt_pk_fp8_f32 v31, v22, v23
	v_min_f32_e32 v24, 0x40e00000, v24
	v_min_f32_e32 v25, 0x40e00000, v25
	v_pk_mul_f32 v[26:27], v[24:25], s[28:29] op_sel_hi:[1,0]
	v_exp_f32_e32 v26, v26
	v_exp_f32_e32 v27, v27
	v_med3_f32 v28, v28, s55, v179
	v_med3_f32 v29, v29, s55, v179
	v_cvt_pk_fp8_f32 v30, v18, v19
	v_pk_add_f32 v[26:27], v[26:27], 1.0 op_sel_hi:[1,0]
	v_lshlrev_b64 v[152:153], 11, v[146:147]
	v_rcp_f32_e32 v26, v26
	v_rcp_f32_e32 v27, v27
	v_cvt_pk_fp8_f32 v30, v20, v21 op_sel:[0,0,1]
	v_lshl_add_u64 v[126:127], v[142:143], 0, v[152:153]
	v_add_co_u32_e32 v22, vcc, s42, v126
	v_pk_mul_f32 v[18:19], v[24:25], v[26:27]
	v_pk_fma_f32 v[26:27], v[70:71], s[26:27], v[2:3] op_sel_hi:[1,0,1]
	v_pk_mul_f32 v[18:19], v[28:29], v[18:19]
	v_min_f32_e32 v26, 0x40e00000, v26
	v_cvt_pk_fp8_f32 v31, v18, v19 op_sel:[0,0,1]
	v_pk_fma_f32 v[18:19], v[78:79], s[26:27], v[6:7] op_sel_hi:[1,0,1]
	v_min_f32_e32 v27, 0x40e00000, v27
	v_min_f32_e32 v18, 0x40e00000, v18
	v_min_f32_e32 v19, 0x40e00000, v19
	v_pk_mul_f32 v[20:21], v[18:19], s[28:29] op_sel_hi:[1,0]
	v_addc_co_u32_e32 v23, vcc, 0, v127, vcc
	v_exp_f32_e32 v20, v20
	v_exp_f32_e32 v21, v21
	v_pk_mul_f32 v[28:29], v[26:27], s[28:29] op_sel_hi:[1,0]
	global_store_dwordx2 v[22:23], v[30:31], off
	v_pk_fma_f32 v[22:23], v[74:75], s[26:27], v[16:17] op_sel_hi:[1,0,1]
	v_pk_add_f32 v[20:21], v[20:21], 1.0 op_sel_hi:[1,0]
	v_exp_f32_e32 v28, v28
	v_rcp_f32_e32 v20, v20
	v_rcp_f32_e32 v21, v21
	v_exp_f32_e32 v29, v29
	v_med3_f32 v22, v22, s55, v179
	v_med3_f32 v23, v23, s55, v179
	v_pk_mul_f32 v[18:19], v[18:19], v[20:21]
	v_pk_fma_f32 v[20:21], v[80:81], s[26:27], v[8:9] op_sel_hi:[1,0,1]
	v_pk_mul_f32 v[18:19], v[22:23], v[18:19]
	v_min_f32_e32 v20, 0x40e00000, v20
	v_min_f32_e32 v21, 0x40e00000, v21
	v_pk_mul_f32 v[24:25], v[20:21], s[28:29] op_sel_hi:[1,0]
	v_pk_fma_f32 v[22:23], v[76:77], s[26:27], v[14:15] op_sel_hi:[1,0,1]
	v_exp_f32_e32 v24, v24
	v_exp_f32_e32 v25, v25
	v_med3_f32 v22, v22, s55, v179
	v_med3_f32 v23, v23, s55, v179
	v_pk_add_f32 v[24:25], v[24:25], 1.0 op_sel_hi:[1,0]
	v_rcp_f32_e32 v24, v24
	v_rcp_f32_e32 v25, v25
	v_cvt_pk_fp8_f32 v30, v18, v19
	v_cvt_pk_fp8_f32 v144, v138, v139
	v_pk_mul_f32 v[20:21], v[20:21], v[24:25]
	v_pk_fma_f32 v[24:25], v[66:67], s[26:27], v[12:13] op_sel_hi:[1,0,1]
	v_pk_mul_f32 v[20:21], v[22:23], v[20:21]
	v_pk_add_f32 v[22:23], v[28:29], 1.0 op_sel_hi:[1,0]
	v_med3_f32 v24, v24, s55, v179
	v_rcp_f32_e32 v22, v22
	v_rcp_f32_e32 v23, v23
	v_med3_f32 v25, v25, s55, v179
	v_pk_fma_f32 v[28:29], v[68:69], s[26:27], v[10:11] op_sel_hi:[1,0,1]
	v_cvt_pk_fp8_f32 v30, v20, v21 op_sel:[0,0,1]
	v_pk_mul_f32 v[22:23], v[26:27], v[22:23]
	v_med3_f32 v28, v28, s55, v179
	v_pk_mul_f32 v[22:23], v[24:25], v[22:23]
	v_pk_fma_f32 v[24:25], v[72:73], s[26:27], v[4:5] op_sel_hi:[1,0,1]
	v_cvt_pk_fp8_f32 v31, v22, v23
	v_min_f32_e32 v24, 0x40e00000, v24
	v_min_f32_e32 v25, 0x40e00000, v25
	v_pk_mul_f32 v[26:27], v[24:25], s[28:29] op_sel_hi:[1,0]
	v_med3_f32 v29, v29, s55, v179
	v_exp_f32_e32 v26, v26
	v_exp_f32_e32 v27, v27
	v_add_co_u32_e32 v22, vcc, s56, v126
	v_cvt_pk_fp8_f32 v144, v140, v141 op_sel:[0,0,1]
	v_pk_add_f32 v[26:27], v[26:27], 1.0 op_sel_hi:[1,0]
	v_addc_co_u32_e32 v23, vcc, 0, v127, vcc
	v_rcp_f32_e32 v26, v26
	v_rcp_f32_e32 v27, v27
;     __device__ __forceinline__ void operator()(const f32x4 (&acc)[2][2][4][2], const Unit& u, int wr, int wc, int fr, int fq, LAS const unsigned char* tbl, LAS const unsigned char* b2l) const {
;     ...
;             for (int m = 0; m < 4; ++m) { unsigned char* rowp = act + (size_t)(row0 + ai * HALF + m * 16) * FF + col0; f32x2_ o[4];
; #pragma unroll
;                 for (int n = 0; n < 2; ++n)
; #pragma unroll
;                     for (int h = 0; h < 2; ++h) { const f32x4 ag = acc[ai][0][m][n], al = acc[ai][1][m][n];
;                         const f32x2_ a2 = {ag[2 * h], ag[2 * h + 1]}, b2 = {al[2 * h], al[2 * h + 1]}, g2 = {gb[n][2 * h], gb[n][2 * h + 1]}, l2 = {lb[n][2 * h], lb[n][2 * h + 1]};
;                         f32x2_ gv = __builtin_elementwise_fma(a2, sc2, g2), lv = __builtin_elementwise_fma(b2, sc2, l2);
;                         gv[0] = fminf(gv[0], 7.0f); gv[1] = fminf(gv[1], 7.0f); lv[0] = __builtin_amdgcn_fmed3f(lv[0], -6.0f, 8.0f); lv[1] = __builtin_amdgcn_fmed3f(lv[1], -6.0f, 8.0f);
;                         f32x2_ e = gv * ce2; e[0] = __builtin_amdgcn_exp2f(e[0]); e[1] = __builtin_amdgcn_exp2f(e[1]); e = e + one2; e[0] = __builtin_amdgcn_rcpf(e[0]); e[1] = __builtin_amdgcn_rcpf(e[1]);
;                         o[n * 2 + h] = (gv * e) * lv; }
;                 u32x2 w; int p0 = __builtin_amdgcn_cvt_pk_fp8_f32(o[0][0], o[0][1], 0, false); p0 = __builtin_amdgcn_cvt_pk_fp8_f32(o[1][0], o[1][1], p0, true);
;                 int p1 = __builtin_amdgcn_cvt_pk_fp8_f32(o[2][0], o[2][1], 0, false); p1 = __builtin_amdgcn_cvt_pk_fp8_f32(o[3][0], o[3][1], p1, true); w.x = (unsigned)p0; w.y = (unsigned)p1;
;                 *(u32x2*)rowp = w; }
	s_mov_b32 s67, s59
	s_mov_b32 s66, s63
	s_mov_b32 s69, s65
	v_pk_mul_f32 v[18:19], v[24:25], v[26:27]
	v_pk_fma_f32 v[26:27], v[54:55], s[26:27], v[2:3] op_sel_hi:[1,0,1]
	v_pk_mul_f32 v[18:19], v[28:29], v[18:19]
	v_min_f32_e32 v26, 0x40e00000, v26
	v_cvt_pk_fp8_f32 v31, v18, v19 op_sel:[0,0,1]
	v_pk_fma_f32 v[18:19], v[62:63], s[26:27], v[6:7] op_sel_hi:[1,0,1]
	v_min_f32_e32 v27, 0x40e00000, v27
	v_min_f32_e32 v18, 0x40e00000, v18
	v_min_f32_e32 v19, 0x40e00000, v19
	v_pk_mul_f32 v[20:21], v[18:19], s[28:29] op_sel_hi:[1,0]
	v_pk_mul_f32 v[28:29], v[26:27], s[28:29] op_sel_hi:[1,0]
	v_exp_f32_e32 v20, v20
	v_exp_f32_e32 v21, v21
	global_store_dwordx2 v[22:23], v[30:31], off
	v_pk_fma_f32 v[22:23], v[58:59], s[26:27], v[16:17] op_sel_hi:[1,0,1]
	v_exp_f32_e32 v28, v28
	v_pk_add_f32 v[20:21], v[20:21], 1.0 op_sel_hi:[1,0]
	v_exp_f32_e32 v29, v29
	v_rcp_f32_e32 v20, v20
	v_rcp_f32_e32 v21, v21
	v_med3_f32 v22, v22, s55, v179
	v_med3_f32 v23, v23, s55, v179
	v_pk_mul_f32 v[18:19], v[18:19], v[20:21]
	v_pk_fma_f32 v[20:21], v[64:65], s[26:27], v[8:9] op_sel_hi:[1,0,1]
	v_pk_mul_f32 v[18:19], v[22:23], v[18:19]
	v_min_f32_e32 v20, 0x40e00000, v20
	v_min_f32_e32 v21, 0x40e00000, v21
	v_pk_mul_f32 v[24:25], v[20:21], s[28:29] op_sel_hi:[1,0]
	v_pk_fma_f32 v[22:23], v[60:61], s[26:27], v[14:15] op_sel_hi:[1,0,1]
	v_exp_f32_e32 v24, v24
	v_exp_f32_e32 v25, v25
	v_med3_f32 v22, v22, s55, v179
	v_med3_f32 v23, v23, s55, v179
	v_pk_add_f32 v[24:25], v[24:25], 1.0 op_sel_hi:[1,0]
	v_cvt_pk_fp8_f32 v30, v18, v19
	v_rcp_f32_e32 v24, v24
	v_rcp_f32_e32 v25, v25
	v_pk_fma_f32 v[6:7], v[46:47], s[26:27], v[6:7] op_sel_hi:[1,0,1]
	v_pk_fma_f32 v[8:9], v[48:49], s[26:27], v[8:9] op_sel_hi:[1,0,1]
	v_min_f32_e32 v6, 0x40e00000, v6
	v_pk_mul_f32 v[20:21], v[20:21], v[24:25]
	v_pk_fma_f32 v[24:25], v[50:51], s[26:27], v[12:13] op_sel_hi:[1,0,1]
	v_pk_mul_f32 v[20:21], v[22:23], v[20:21]
	v_pk_add_f32 v[22:23], v[28:29], 1.0 op_sel_hi:[1,0]
	v_med3_f32 v24, v24, s55, v179
	v_rcp_f32_e32 v22, v22
	v_rcp_f32_e32 v23, v23
	v_med3_f32 v25, v25, s55, v179
	v_pk_fma_f32 v[28:29], v[52:53], s[26:27], v[10:11] op_sel_hi:[1,0,1]
	v_min_f32_e32 v7, 0x40e00000, v7
	v_pk_mul_f32 v[22:23], v[26:27], v[22:23]
	v_med3_f32 v28, v28, s55, v179
	v_pk_mul_f32 v[22:23], v[24:25], v[22:23]
	v_pk_fma_f32 v[24:25], v[56:57], s[26:27], v[4:5] op_sel_hi:[1,0,1]
	v_cvt_pk_fp8_f32 v31, v22, v23
	v_min_f32_e32 v24, 0x40e00000, v24
	v_min_f32_e32 v25, 0x40e00000, v25
	v_pk_mul_f32 v[26:27], v[24:25], s[28:29] op_sel_hi:[1,0]
	v_med3_f32 v29, v29, s55, v179
	v_exp_f32_e32 v26, v26
	v_exp_f32_e32 v27, v27
	v_min_f32_e32 v8, 0x40e00000, v8
	v_min_f32_e32 v9, 0x40e00000, v9
	v_pk_fma_f32 v[16:17], v[42:43], s[26:27], v[16:17] op_sel_hi:[1,0,1]
	v_pk_add_f32 v[26:27], v[26:27], 1.0 op_sel_hi:[1,0]
	v_med3_f32 v16, v16, s55, v179
	v_rcp_f32_e32 v26, v26
	v_rcp_f32_e32 v27, v27
	v_med3_f32 v17, v17, s55, v179
	v_pk_fma_f32 v[2:3], v[38:39], s[26:27], v[2:3] op_sel_hi:[1,0,1]
	v_pk_fma_f32 v[14:15], v[44:45], s[26:27], v[14:15] op_sel_hi:[1,0,1]
	v_pk_mul_f32 v[18:19], v[24:25], v[26:27]
	v_min_f32_e32 v2, 0x40e00000, v2
	v_pk_mul_f32 v[18:19], v[28:29], v[18:19]
	v_min_f32_e32 v3, 0x40e00000, v3
	v_cvt_pk_fp8_f32 v31, v18, v19 op_sel:[0,0,1]
	v_pk_mul_f32 v[18:19], v[6:7], s[28:29] op_sel_hi:[1,0]
	v_med3_f32 v14, v14, s55, v179
	v_exp_f32_e32 v18, v18
	v_exp_f32_e32 v19, v19
	v_med3_f32 v15, v15, s55, v179
	v_pk_fma_f32 v[12:13], v[34:35], s[26:27], v[12:13] op_sel_hi:[1,0,1]
	v_pk_fma_f32 v[4:5], v[40:41], s[26:27], v[4:5] op_sel_hi:[1,0,1]
	v_pk_add_f32 v[18:19], v[18:19], 1.0 op_sel_hi:[1,0]
	v_med3_f32 v12, v12, s55, v179
	v_rcp_f32_e32 v18, v18
	v_rcp_f32_e32 v19, v19
	v_med3_f32 v13, v13, s55, v179
	v_min_f32_e32 v4, 0x40e00000, v4
	v_min_f32_e32 v5, 0x40e00000, v5
	v_pk_mul_f32 v[6:7], v[6:7], v[18:19]
	v_pk_mul_f32 v[18:19], v[8:9], s[28:29] op_sel_hi:[1,0]
	v_pk_mul_f32 v[6:7], v[16:17], v[6:7]
	v_exp_f32_e32 v18, v18
	v_exp_f32_e32 v19, v19
	v_pk_fma_f32 v[10:11], v[36:37], s[26:27], v[10:11] op_sel_hi:[1,0,1]
	v_cvt_pk_fp8_f32 v30, v20, v21 op_sel:[0,0,1]
	v_med3_f32 v10, v10, s55, v179
	v_pk_add_f32 v[16:17], v[18:19], 1.0 op_sel_hi:[1,0]
	v_pk_mul_f32 v[18:19], v[2:3], s[28:29] op_sel_hi:[1,0]
	v_rcp_f32_e32 v16, v16
	v_rcp_f32_e32 v17, v17
	v_exp_f32_e32 v18, v18
	v_exp_f32_e32 v19, v19
	v_med3_f32 v11, v11, s55, v179
	v_pk_mul_f32 v[8:9], v[8:9], v[16:17]
	v_add_co_u32_e32 v20, vcc, s57, v126
	v_pk_mul_f32 v[8:9], v[14:15], v[8:9]
	v_pk_add_f32 v[14:15], v[18:19], 1.0 op_sel_hi:[1,0]
	v_addc_co_u32_e32 v21, vcc, 0, v127, vcc
	v_rcp_f32_e32 v14, v14
	v_rcp_f32_e32 v15, v15
	s_mov_b32 s68, s0
	global_store_dwordx2 v[126:127], v[144:145], off
	global_store_dwordx2 v[20:21], v[30:31], off
	v_pk_mul_f32 v[2:3], v[2:3], v[14:15]
	v_pk_mul_f32 v[2:3], v[12:13], v[2:3]
	v_pk_mul_f32 v[12:13], v[4:5], s[28:29] op_sel_hi:[1,0]
	v_exp_f32_e32 v12, v12
	v_exp_f32_e32 v13, v13
	v_cvt_pk_fp8_f32 v14, v6, v7
	v_cvt_pk_fp8_f32 v15, v2, v3
	v_pk_add_f32 v[12:13], v[12:13], 1.0 op_sel_hi:[1,0]
	s_nop 0
	v_rcp_f32_e32 v12, v12
	v_rcp_f32_e32 v13, v13
	v_cvt_pk_fp8_f32 v14, v8, v9 op_sel:[0,0,1]
	v_pk_mul_f32 v[2:3], v[4:5], v[12:13]
	s_nop 0
	v_pk_mul_f32 v[2:3], v[10:11], v[2:3]
	s_nop 0
	v_cvt_pk_fp8_f32 v15, v2, v3 op_sel:[0,0,1]
	v_add_co_u32_e32 v2, vcc, 0x58000, v126
	s_nop 1
	v_addc_co_u32_e32 v3, vcc, 0, v127, vcc
	s_and_b64 vcc, exec, s[30:31]
	global_store_dwordx2 v[2:3], v[14:15], off
	s_cbranch_vccnz .LBB0_994

; #define LAS __attribute__((address_space(3)))
;     __device__ __forceinline__ void operator()(const f32x4 (&acc)[2][2][4][2], const Unit& u, int wr, int wc, int fr, int fq, LAS const unsigned char* tbl, LAS const unsigned char* b2l) const {
;         { int t_ = threadIdx.x; asm volatile("" : "+v"(t_)); fr = t_ & 15; fq = (t_ >> 4) & 3; }
;         const int r0 = wr * 64 + fr; const int col0 = u.pn * BM + wc * 32 + 8 * fq;
;         unsigned char* Y = ws + WS_Y;
;         f32x4 bv[2][2];
; #pragma unroll
;         for (int bj = 0; bj < 2; ++bj)
; #pragma unroll
;             for (int n = 0; n < 2; ++n) bv[bj][n] = *(LAS const f32x4*)(b2l + (wc * 32 + 8 * fq + bj * HALF + 4 * n) * 4);
; #pragma unroll
;         for (int ai = 0; ai < 2; ++ai)
; #pragma unroll
;             for (int m = 0; m < 4; ++m) { const int row = r0 + ai * HALF + m * 16;
;                 if (u.pos0 + row < u.cnt) { const int pid = *(LAS const int*)(tbl + row * 4); const float gt = *(LAS const float*)(tbl + 1024 + row * 4) * Y_FP8_SCALE; unsigned char* rowp = Y + (size_t)pid * D_ + col0;
.Lmid_g2:
	ds_read_b128 v[2:5], v156
	ds_read_b128 v[6:9], v156 offset:1024
	s_nop 2
	ds_read_b128 v[10:13], v156 offset:2048
	ds_read_b128 v[14:17], v156 offset:3072
	s_add_i32 s69, s69, 0x40000
	s_mov_b32 m0, s41
	ds_read_b128 v[18:21], v154 offset:32768
	ds_read_b128 v[22:25], v154 offset:33792
	ds_read_b128 v[26:29], v154 offset:34816
	ds_read_b128 v[30:33], v154 offset:35840
	ds_read_b128 v[34:37], v154 offset:36864
	ds_read_b128 v[38:41], v154 offset:37888
	ds_read_b128 v[42:45], v154 offset:38912
	ds_read_b128 v[46:49], v154 offset:39936
	buffer_load_dwordx4 v1, s[20:23], s69 offen lds
	s_mov_b32 m0, s42
	s_nop 0
	buffer_load_dwordx4 v252, s[20:23], s69 offen lds
	s_waitcnt lgkmcnt(8)
	s_barrier
	s_waitcnt lgkmcnt(0)
	s_setprio 1
	s_waitcnt lgkmcnt(6)
	v_mfma_f32_16x16x128_f8f6f4 v[134:137], v[2:9], v[18:25], v[134:137]
	v_mfma_f32_16x16x128_f8f6f4 v[122:125], v[10:17], v[18:25], v[122:125]
	s_waitcnt lgkmcnt(4)
	v_mfma_f32_16x16x128_f8f6f4 v[110:113], v[2:9], v[26:33], v[192:195]
	v_mfma_f32_16x16x128_f8f6f4 v[106:109], v[10:17], v[26:33], v[196:199]
	s_waitcnt lgkmcnt(2)
	v_mfma_f32_16x16x128_f8f6f4 v[94:97], v[2:9], v[34:41], v[200:203]
	v_mfma_f32_16x16x128_f8f6f4 v[90:93], v[10:17], v[34:41], v[204:207]
	s_waitcnt lgkmcnt(0)
	v_mfma_f32_16x16x128_f8f6f4 v[78:81], v[2:9], v[42:49], v[208:211]
	v_mfma_f32_16x16x128_f8f6f4 v[74:77], v[10:17], v[42:49], v[212:215]
	s_setprio 0
	s_barrier
	s_add_i32 s69, s67, 0x80
	s_mov_b32 m0, s45
	ds_read_b128 v[126:129], v157
	ds_read_b128 v[130:133], v157 offset:1024
	ds_read_b128 v[138:141], v157 offset:2048
	ds_read_b128 v[142:145], v157 offset:3072
	buffer_load_dwordx4 v253, s[24:27], s69 offen lds
	s_mov_b32 m0, s46
	s_nop 0
	buffer_load_dwordx4 v150, s[24:27], s69 offen lds
	s_barrier
	s_waitcnt lgkmcnt(0)
	s_setprio 1
	s_waitcnt lgkmcnt(2)
	v_mfma_f32_16x16x128_f8f6f4 v[118:121], v[126:133], v[18:25], v[118:121]
	s_waitcnt lgkmcnt(0)
	v_mfma_f32_16x16x128_f8f6f4 v[114:117], v[138:145], v[18:25], v[114:117]
	v_mfma_f32_16x16x128_f8f6f4 v[102:105], v[126:133], v[26:33], v[160:163]
	v_mfma_f32_16x16x128_f8f6f4 v[98:101], v[138:145], v[26:33], v[164:167]
	v_mfma_f32_16x16x128_f8f6f4 v[86:89], v[126:133], v[34:41], v[168:171]
	v_mfma_f32_16x16x128_f8f6f4 v[82:85], v[138:145], v[34:41], v[172:175]
	v_mfma_f32_16x16x128_f8f6f4 v[70:73], v[126:133], v[42:49], v[176:179]
	v_mfma_f32_16x16x128_f8f6f4 v[66:69], v[138:145], v[42:49], v[180:183]
	s_setprio 0
	s_mov_b32 m0, s47
	s_barrier
	ds_read_b128 v[26:29], v154 offset:49152
	ds_read_b128 v[30:33], v154 offset:50176
	ds_read_b128 v[34:37], v154 offset:51200
	ds_read_b128 v[38:41], v154 offset:52224
	ds_read_b128 v[160:163], v154 offset:53248
	ds_read_b128 v[164:167], v154 offset:54272
	ds_read_b128 v[168:171], v154 offset:55296
	ds_read_b128 v[172:175], v154 offset:56320
	buffer_load_dwordx4 v1, s[20:23], s68 offen lds
	s_mov_b32 m0, s48
	s_nop 0
	buffer_load_dwordx4 v252, s[20:23], s68 offen lds
	s_barrier
	s_waitcnt lgkmcnt(0)
	s_setprio 1
	s_waitcnt lgkmcnt(6)
	v_mfma_f32_16x16x128_f8f6f4 v[62:65], v[2:9], v[26:33], v[62:65]
	v_mfma_f32_16x16x128_f8f6f4 v[58:61], v[10:17], v[26:33], v[58:61]
	s_waitcnt lgkmcnt(4)
	v_mfma_f32_16x16x128_f8f6f4 v[46:49], v[2:9], v[34:41], v[184:187]
	v_mfma_f32_16x16x128_f8f6f4 v[42:45], v[10:17], v[34:41], v[188:191]
	s_waitcnt lgkmcnt(2)
	v_mfma_f32_16x16x128_f8f6f4 v[22:25], v[2:9], v[160:167], v[216:219]
	v_mfma_f32_16x16x128_f8f6f4 v[18:21], v[10:17], v[160:167], v[220:223]
	s_waitcnt lgkmcnt(0)
	v_mfma_f32_16x16x128_f8f6f4 v[6:9], v[2:9], v[168:175], v[224:227]
	v_mfma_f32_16x16x128_f8f6f4 v[2:5], v[10:17], v[168:175], v[228:231]
	s_setprio 0
	s_barrier
	s_add_i32 s67, s67, 0x40080
	s_mov_b32 m0, s49
	s_nop 0
	buffer_load_dwordx4 v253, s[24:27], s67 offen lds
	s_mov_b32 m0, s50
	s_nop 0
	buffer_load_dwordx4 v150, s[24:27], s67 offen lds
	s_waitcnt vmcnt(6)
	s_barrier
	s_setprio 1
	v_mfma_f32_16x16x128_f8f6f4 v[54:57], v[126:133], v[26:33], v[54:57]
	v_mfma_f32_16x16x128_f8f6f4 v[50:53], v[138:145], v[26:33], v[50:53]
	v_mfma_f32_16x16x128_f8f6f4 v[30:33], v[126:133], v[34:41], v[232:235]
	v_mfma_f32_16x16x128_f8f6f4 v[26:29], v[138:145], v[34:41], v[236:239]
	v_mfma_f32_16x16x128_f8f6f4 v[38:41], v[126:133], v[160:167], v[240:243]
	v_mfma_f32_16x16x128_f8f6f4 v[34:37], v[138:145], v[160:167], v[244:247]
	v_mfma_f32_16x16x128_f8f6f4 v[14:17], v[126:133], v[168:175], v[248:251]
	v_mfma_f32_16x16x128_f8f6f4 v[10:13], v[138:145], v[168:175], v[146:149]
	s_setprio 0
	s_add_i32 s66, s66, 2
	s_addk_i32 s1, 0x100
	s_addk_i32 s19, 0x100
	s_cmp_gt_u32 s66, 13
	s_barrier
	s_cbranch_scc0 .LBB0_1081
	s_lshl_b32 s0, s65, 11
	s_add_i32 s18, s0, 0
	s_lshl_b32 s0, s65, 10
	s_add_i32 s18, s18, 0x20000
	s_add_i32 s0, s0, 0x21800
	v_mov_b32_e32 v146, v0
	s_cmp_lt_i32 s65, 2
	s_cselect_b32 s0, s0, 0x23800
	v_lshrrev_b32_e32 v126, 1, v146
	v_and_b32_e32 v147, 24, v126
	s_add_i32 s0, s0, 0
	v_or_b32_e32 v126, s44, v147
	v_lshl_add_u32 v126, v126, 2, s0
	ds_read_b128 v[142:145], v126
	ds_read_b128 v[138:141], v126 offset:16
	ds_read_b128 v[130:133], v126 offset:512
	ds_read_b128 v[126:129], v126 offset:528
	s_lshl_b32 s0, s64, 8
	s_or_b32 s0, s0, s44
	v_and_or_b32 v159, v146, 15, s43
	v_or_b32_e32 v146, s0, v147
	v_ashrrev_i32_e32 v147, 31, v146
	v_add_u32_e32 v148, s34, v159
	v_lshl_add_u64 v[146:147], s[6:7], 0, v[146:147]
	v_cmp_gt_i32_e32 vcc, s33, v148
	s_and_saveexec_b64 s[0:1], vcc
	s_cbranch_execz .LBB0_1084
; #define LAS __attribute__((address_space(3)))
; __device__ __forceinline__ unsigned pk4_fp8(float a, float b, float c, float d) {
;     a = fminf(fmaxf(a, -448.f), 448.f); b = fminf(fmaxf(b, -448.f), 448.f); c = fminf(fmaxf(c, -448.f), 448.f); d = fminf(fmaxf(d, -448.f), 448.f);
;     int p = __builtin_amdgcn_cvt_pk_fp8_f32(a, b, 0, false); p = __builtin_amdgcn_cvt_pk_fp8_f32(c, d, p, true); return (unsigned)p; }
;     __device__ __forceinline__ void operator()(const f32x4 (&acc)[2][2][4][2], const Unit& u, int wr, int wc, int fr, int fq, LAS const unsigned char* tbl, LAS const unsigned char* b2l) const {
;     ...
;             for (int m = 0; m < 4; ++m) { const int row = r0 + ai * HALF + m * 16;
;                 if (u.pos0 + row < u.cnt) { const int pid = *(LAS const int*)(tbl + row * 4); const float gt = *(LAS const float*)(tbl + 1024 + row * 4) * Y_FP8_SCALE; unsigned char* rowp = Y + (size_t)pid * D_ + col0;
; #pragma unroll
;                     for (int bj = 0; bj < 2; ++bj) { const f32x4 v0 = (acc[ai][bj][m][0] * (1.0f / W_FP8_SCALE) + bv[bj][0]) * gt, v1 = (acc[ai][bj][m][1] * (1.0f / W_FP8_SCALE) + bv[bj][1]) * gt;
;                         u32x2 w; w.x = pk4_fp8(v0[0], v0[1], v0[2], v0[3]); w.y = pk4_fp8(v1[0], v1[1], v1[2], v1[3]);
;                         *(u32x2*)(rowp + bj * HALF) = w; } } }
	v_lshl_add_u32 v148, v159, 2, s18
	ds_read2st64_b32 v[148:149], v148 offset1:4
	s_waitcnt lgkmcnt(4)
	v_pk_fma_f32 v[134:135], v[134:135], s[28:29], v[142:143] op_sel_hi:[1,0,1]
	v_pk_fma_f32 v[136:137], v[136:137], s[28:29], v[144:145] op_sel_hi:[1,0,1]
	s_waitcnt lgkmcnt(3)
	v_pk_fma_f32 v[124:125], v[124:125], s[28:29], v[140:141] op_sel_hi:[1,0,1]
	v_pk_fma_f32 v[122:123], v[122:123], s[28:29], v[138:139] op_sel_hi:[1,0,1]
	s_waitcnt lgkmcnt(0)
	v_ashrrev_i32_e32 v161, 31, v148
	v_mov_b32_e32 v160, v148
	v_mul_f32_e32 v148, 0x41800000, v149
	v_pk_mul_f32 v[134:135], v[134:135], v[148:149] op_sel_hi:[1,0]
	v_pk_mul_f32 v[136:137], v[136:137], v[148:149] op_sel_hi:[1,0]
	v_pk_mul_f32 v[124:125], v[124:125], v[148:149] op_sel_hi:[1,0]
	v_pk_mul_f32 v[122:123], v[122:123], v[148:149] op_sel_hi:[1,0]
	v_med3_f32 v149, v134, s55, v158
	v_med3_f32 v135, v135, s55, v158
	v_cvt_pk_fp8_f32 v134, v149, v135
	v_med3_f32 v122, v122, s55, v158
	v_med3_f32 v123, v123, s55, v158
	v_cvt_pk_fp8_f32 v135, v122, v123
	v_pk_fma_f32 v[118:119], v[118:119], s[28:29], v[130:131] op_sel_hi:[1,0,1]
	v_med3_f32 v122, v124, s55, v158
	v_med3_f32 v123, v125, s55, v158
	v_pk_mul_f32 v[118:119], v[118:119], v[148:149] op_sel_hi:[1,0]
	v_pk_fma_f32 v[114:115], v[114:115], s[28:29], v[126:127] op_sel_hi:[1,0,1]
	v_cvt_pk_fp8_f32 v135, v122, v123 op_sel:[0,0,1]
	v_pk_mul_f32 v[114:115], v[114:115], v[148:149] op_sel_hi:[1,0]
	v_med3_f32 v122, v118, s55, v158
	v_med3_f32 v119, v119, s55, v158
	v_cvt_pk_fp8_f32 v118, v122, v119
	v_med3_f32 v114, v114, s55, v158
	v_med3_f32 v115, v115, s55, v158
	v_cvt_pk_fp8_f32 v119, v114, v115
	v_pk_fma_f32 v[120:121], v[120:121], s[28:29], v[132:133] op_sel_hi:[1,0,1]
	v_pk_fma_f32 v[116:117], v[116:117], s[28:29], v[128:129] op_sel_hi:[1,0,1]
	v_med3_f32 v136, v136, s55, v158
	v_med3_f32 v137, v137, s55, v158
	v_pk_mul_f32 v[120:121], v[120:121], v[148:149] op_sel_hi:[1,0]
	v_pk_mul_f32 v[116:117], v[116:117], v[148:149] op_sel_hi:[1,0]
	v_cvt_pk_fp8_f32 v134, v136, v137 op_sel:[0,0,1]
	v_med3_f32 v120, v120, s55, v158
	v_med3_f32 v121, v121, s55, v158
	v_med3_f32 v114, v116, s55, v158
	v_med3_f32 v115, v117, s55, v158
	v_cvt_pk_fp8_f32 v118, v120, v121 op_sel:[0,0,1]
	v_cvt_pk_fp8_f32 v119, v114, v115 op_sel:[0,0,1]
	v_lshlrev_b64 v[114:115], 11, v[160:161]
	v_lshl_add_u64 v[114:115], v[146:147], 0, v[114:115]
	global_store_dwordx2 v[114:115], v[134:135], off
	global_store_dwordx2 v[114:115], v[118:119], off offset:128
.LBB0_1084:
	s_or_b64 exec, exec, s[0:1]
	v_or_b32_e32 v114, 16, v159
	v_add_u32_e32 v115, s34, v114
	v_cmp_gt_i32_e32 vcc, s33, v115
	s_and_saveexec_b64 s[0:1], vcc
	s_cbranch_execz .LBB0_1086
	v_lshl_add_u32 v114, v114, 2, s18
	ds_read2st64_b32 v[114:115], v114 offset1:4
	s_waitcnt lgkmcnt(4)
	v_pk_fma_f32 v[110:111], v[110:111], s[28:29], v[142:143] op_sel_hi:[1,0,1]
	v_pk_fma_f32 v[112:113], v[112:113], s[28:29], v[144:145] op_sel_hi:[1,0,1]
	s_waitcnt lgkmcnt(3)
	v_pk_fma_f32 v[108:109], v[108:109], s[28:29], v[140:141] op_sel_hi:[1,0,1]
	v_pk_fma_f32 v[106:107], v[106:107], s[28:29], v[138:139] op_sel_hi:[1,0,1]
	s_waitcnt lgkmcnt(0)
	v_ashrrev_i32_e32 v117, 31, v114
	v_mov_b32_e32 v116, v114
	v_mul_f32_e32 v114, 0x41800000, v115
	v_pk_mul_f32 v[110:111], v[110:111], v[114:115] op_sel_hi:[1,0]
	v_pk_mul_f32 v[112:113], v[112:113], v[114:115] op_sel_hi:[1,0]
	v_pk_mul_f32 v[108:109], v[108:109], v[114:115] op_sel_hi:[1,0]
	v_pk_mul_f32 v[106:107], v[106:107], v[114:115] op_sel_hi:[1,0]
	v_med3_f32 v115, v110, s55, v158
	v_med3_f32 v111, v111, s55, v158
	v_cvt_pk_fp8_f32 v110, v115, v111
	v_med3_f32 v106, v106, s55, v158
	v_med3_f32 v107, v107, s55, v158
	v_cvt_pk_fp8_f32 v111, v106, v107
	v_pk_fma_f32 v[102:103], v[102:103], s[28:29], v[130:131] op_sel_hi:[1,0,1]
	v_med3_f32 v106, v108, s55, v158
	v_med3_f32 v107, v109, s55, v158
	v_pk_mul_f32 v[102:103], v[102:103], v[114:115] op_sel_hi:[1,0]
	v_pk_fma_f32 v[98:99], v[98:99], s[28:29], v[126:127] op_sel_hi:[1,0,1]
	v_cvt_pk_fp8_f32 v111, v106, v107 op_sel:[0,0,1]
	v_pk_mul_f32 v[98:99], v[98:99], v[114:115] op_sel_hi:[1,0]
	v_med3_f32 v106, v102, s55, v158
	v_med3_f32 v103, v103, s55, v158
	v_cvt_pk_fp8_f32 v102, v106, v103
	v_med3_f32 v98, v98, s55, v158
	v_med3_f32 v99, v99, s55, v158
	v_cvt_pk_fp8_f32 v103, v98, v99
	v_pk_fma_f32 v[104:105], v[104:105], s[28:29], v[132:133] op_sel_hi:[1,0,1]
	v_pk_fma_f32 v[100:101], v[100:101], s[28:29], v[128:129] op_sel_hi:[1,0,1]
	v_med3_f32 v112, v112, s55, v158
	v_med3_f32 v113, v113, s55, v158
	v_pk_mul_f32 v[104:105], v[104:105], v[114:115] op_sel_hi:[1,0]
	v_pk_mul_f32 v[100:101], v[100:101], v[114:115] op_sel_hi:[1,0]
	v_cvt_pk_fp8_f32 v110, v112, v113 op_sel:[0,0,1]
	v_med3_f32 v104, v104, s55, v158
	v_med3_f32 v105, v105, s55, v158
	v_med3_f32 v98, v100, s55, v158
	v_med3_f32 v99, v101, s55, v158
	v_cvt_pk_fp8_f32 v102, v104, v105 op_sel:[0,0,1]
	v_cvt_pk_fp8_f32 v103, v98, v99 op_sel:[0,0,1]
	v_lshlrev_b64 v[98:99], 11, v[116:117]
	v_lshl_add_u64 v[98:99], v[146:147], 0, v[98:99]
	global_store_dwordx2 v[98:99], v[110:111], off
	global_store_dwordx2 v[98:99], v[102:103], off offset:128
; #define LAS __attribute__((address_space(3)))
; __device__ __forceinline__ unsigned pk4_fp8(float a, float b, float c, float d) {
;     a = fminf(fmaxf(a, -448.f), 448.f); b = fminf(fmaxf(b, -448.f), 448.f); c = fminf(fmaxf(c, -448.f), 448.f); d = fminf(fmaxf(d, -448.f), 448.f);
;     int p = __builtin_amdgcn_cvt_pk_fp8_f32(a, b, 0, false); p = __builtin_amdgcn_cvt_pk_fp8_f32(c, d, p, true); return (unsigned)p; }
;     __device__ __forceinline__ void operator()(const f32x4 (&acc)[2][2][4][2], const Unit& u, int wr, int wc, int fr, int fq, LAS const unsigned char* tbl, LAS const unsigned char* b2l) const {
;     ...
;             for (int m = 0; m < 4; ++m) { const int row = r0 + ai * HALF + m * 16;
;                 if (u.pos0 + row < u.cnt) { const int pid = *(LAS const int*)(tbl + row * 4); const float gt = *(LAS const float*)(tbl + 1024 + row * 4) * Y_FP8_SCALE; unsigned char* rowp = Y + (size_t)pid * D_ + col0;
; #pragma unroll
;                     for (int bj = 0; bj < 2; ++bj) { const f32x4 v0 = (acc[ai][bj][m][0] * (1.0f / W_FP8_SCALE) + bv[bj][0]) * gt, v1 = (acc[ai][bj][m][1] * (1.0f / W_FP8_SCALE) + bv[bj][1]) * gt;
;                         u32x2 w; w.x = pk4_fp8(v0[0], v0[1], v0[2], v0[3]); w.y = pk4_fp8(v1[0], v1[1], v1[2], v1[3]);
;                         *(u32x2*)(rowp + bj * HALF) = w; } } }
.LBB0_1086:
	s_or_b64 exec, exec, s[0:1]
	v_or_b32_e32 v98, 32, v159
	v_add_u32_e32 v99, s34, v98
	v_cmp_gt_i32_e32 vcc, s33, v99
	s_and_saveexec_b64 s[0:1], vcc
	s_cbranch_execz .LBB0_1088
	v_lshl_add_u32 v98, v98, 2, s18
	ds_read2st64_b32 v[98:99], v98 offset1:4
	s_waitcnt lgkmcnt(4)
	v_pk_fma_f32 v[94:95], v[94:95], s[28:29], v[142:143] op_sel_hi:[1,0,1]
	v_pk_fma_f32 v[96:97], v[96:97], s[28:29], v[144:145] op_sel_hi:[1,0,1]
	s_waitcnt lgkmcnt(3)
	v_pk_fma_f32 v[92:93], v[92:93], s[28:29], v[140:141] op_sel_hi:[1,0,1]
	v_pk_fma_f32 v[90:91], v[90:91], s[28:29], v[138:139] op_sel_hi:[1,0,1]
	s_waitcnt lgkmcnt(0)
	v_ashrrev_i32_e32 v101, 31, v98
	v_mov_b32_e32 v100, v98
	v_mul_f32_e32 v98, 0x41800000, v99
	v_pk_mul_f32 v[94:95], v[94:95], v[98:99] op_sel_hi:[1,0]
	v_pk_mul_f32 v[96:97], v[96:97], v[98:99] op_sel_hi:[1,0]
	v_pk_mul_f32 v[92:93], v[92:93], v[98:99] op_sel_hi:[1,0]
	v_pk_mul_f32 v[90:91], v[90:91], v[98:99] op_sel_hi:[1,0]
	v_med3_f32 v99, v94, s55, v158
	v_med3_f32 v95, v95, s55, v158
	v_cvt_pk_fp8_f32 v94, v99, v95
	v_med3_f32 v90, v90, s55, v158
	v_med3_f32 v91, v91, s55, v158
	v_cvt_pk_fp8_f32 v95, v90, v91
	v_pk_fma_f32 v[86:87], v[86:87], s[28:29], v[130:131] op_sel_hi:[1,0,1]
	v_med3_f32 v90, v92, s55, v158
	v_med3_f32 v91, v93, s55, v158
	v_pk_mul_f32 v[86:87], v[86:87], v[98:99] op_sel_hi:[1,0]
	v_pk_fma_f32 v[82:83], v[82:83], s[28:29], v[126:127] op_sel_hi:[1,0,1]
	v_cvt_pk_fp8_f32 v95, v90, v91 op_sel:[0,0,1]
	v_pk_mul_f32 v[82:83], v[82:83], v[98:99] op_sel_hi:[1,0]
	v_med3_f32 v90, v86, s55, v158
	v_med3_f32 v87, v87, s55, v158
	v_cvt_pk_fp8_f32 v86, v90, v87
	v_med3_f32 v82, v82, s55, v158
	v_med3_f32 v83, v83, s55, v158
	v_cvt_pk_fp8_f32 v87, v82, v83
	v_pk_fma_f32 v[88:89], v[88:89], s[28:29], v[132:133] op_sel_hi:[1,0,1]
	v_pk_fma_f32 v[84:85], v[84:85], s[28:29], v[128:129] op_sel_hi:[1,0,1]
	v_med3_f32 v96, v96, s55, v158
	v_med3_f32 v97, v97, s55, v158
	v_pk_mul_f32 v[88:89], v[88:89], v[98:99] op_sel_hi:[1,0]
	v_pk_mul_f32 v[84:85], v[84:85], v[98:99] op_sel_hi:[1,0]
	v_cvt_pk_fp8_f32 v94, v96, v97 op_sel:[0,0,1]
	v_med3_f32 v88, v88, s55, v158
	v_med3_f32 v89, v89, s55, v158
	v_med3_f32 v82, v84, s55, v158
	v_med3_f32 v83, v85, s55, v158
	v_cvt_pk_fp8_f32 v86, v88, v89 op_sel:[0,0,1]
	v_cvt_pk_fp8_f32 v87, v82, v83 op_sel:[0,0,1]
	v_lshlrev_b64 v[82:83], 11, v[100:101]
	v_lshl_add_u64 v[82:83], v[146:147], 0, v[82:83]
	global_store_dwordx2 v[82:83], v[94:95], off
	global_store_dwordx2 v[82:83], v[86:87], off offset:128
.LBB0_1088:
	s_or_b64 exec, exec, s[0:1]
	v_or_b32_e32 v82, 48, v159
	v_add_u32_e32 v83, s34, v82
	v_cmp_gt_i32_e32 vcc, s33, v83
	s_and_saveexec_b64 s[0:1], vcc
	s_cbranch_execz .LBB0_1090
	v_lshl_add_u32 v82, v82, 2, s18
	ds_read2st64_b32 v[82:83], v82 offset1:4
	s_waitcnt lgkmcnt(4)
	v_pk_fma_f32 v[78:79], v[78:79], s[28:29], v[142:143] op_sel_hi:[1,0,1]
	v_pk_fma_f32 v[80:81], v[80:81], s[28:29], v[144:145] op_sel_hi:[1,0,1]
	s_waitcnt lgkmcnt(3)
	v_pk_fma_f32 v[76:77], v[76:77], s[28:29], v[140:141] op_sel_hi:[1,0,1]
	v_pk_fma_f32 v[74:75], v[74:75], s[28:29], v[138:139] op_sel_hi:[1,0,1]
	s_waitcnt lgkmcnt(0)
	v_ashrrev_i32_e32 v85, 31, v82
	v_mov_b32_e32 v84, v82
	v_mul_f32_e32 v82, 0x41800000, v83
	v_pk_mul_f32 v[78:79], v[78:79], v[82:83] op_sel_hi:[1,0]
	v_pk_mul_f32 v[80:81], v[80:81], v[82:83] op_sel_hi:[1,0]
	v_pk_mul_f32 v[76:77], v[76:77], v[82:83] op_sel_hi:[1,0]
	v_pk_mul_f32 v[74:75], v[74:75], v[82:83] op_sel_hi:[1,0]
	v_med3_f32 v83, v78, s55, v158
	v_med3_f32 v79, v79, s55, v158
	v_cvt_pk_fp8_f32 v78, v83, v79
	v_med3_f32 v74, v74, s55, v158
	v_med3_f32 v75, v75, s55, v158
	v_cvt_pk_fp8_f32 v79, v74, v75
	v_pk_fma_f32 v[70:71], v[70:71], s[28:29], v[130:131] op_sel_hi:[1,0,1]
	v_med3_f32 v74, v76, s55, v158
	v_med3_f32 v75, v77, s55, v158
	v_pk_mul_f32 v[70:71], v[70:71], v[82:83] op_sel_hi:[1,0]
	v_pk_fma_f32 v[66:67], v[66:67], s[28:29], v[126:127] op_sel_hi:[1,0,1]
	v_cvt_pk_fp8_f32 v79, v74, v75 op_sel:[0,0,1]
	v_pk_mul_f32 v[66:67], v[66:67], v[82:83] op_sel_hi:[1,0]
	v_med3_f32 v74, v70, s55, v158
	v_med3_f32 v71, v71, s55, v158
	v_cvt_pk_fp8_f32 v70, v74, v71
	v_med3_f32 v66, v66, s55, v158
	v_med3_f32 v67, v67, s55, v158
	v_cvt_pk_fp8_f32 v71, v66, v67
	v_pk_fma_f32 v[72:73], v[72:73], s[28:29], v[132:133] op_sel_hi:[1,0,1]
	v_pk_fma_f32 v[68:69], v[68:69], s[28:29], v[128:129] op_sel_hi:[1,0,1]
	v_med3_f32 v80, v80, s55, v158
	v_med3_f32 v81, v81, s55, v158
	v_pk_mul_f32 v[72:73], v[72:73], v[82:83] op_sel_hi:[1,0]
	v_pk_mul_f32 v[68:69], v[68:69], v[82:83] op_sel_hi:[1,0]
	v_cvt_pk_fp8_f32 v78, v80, v81 op_sel:[0,0,1]
	v_med3_f32 v72, v72, s55, v158
	v_med3_f32 v73, v73, s55, v158
	v_med3_f32 v66, v68, s55, v158
	v_med3_f32 v67, v69, s55, v158
	v_cvt_pk_fp8_f32 v70, v72, v73 op_sel:[0,0,1]
	v_cvt_pk_fp8_f32 v71, v66, v67 op_sel:[0,0,1]
	v_lshlrev_b64 v[66:67], 11, v[84:85]
	v_lshl_add_u64 v[66:67], v[146:147], 0, v[66:67]
	global_store_dwordx2 v[66:67], v[78:79], off
	global_store_dwordx2 v[66:67], v[70:71], off offset:128
; #define LAS __attribute__((address_space(3)))
; __device__ __forceinline__ unsigned pk4_fp8(float a, float b, float c, float d) {
;     a = fminf(fmaxf(a, -448.f), 448.f); b = fminf(fmaxf(b, -448.f), 448.f); c = fminf(fmaxf(c, -448.f), 448.f); d = fminf(fmaxf(d, -448.f), 448.f);
;     int p = __builtin_amdgcn_cvt_pk_fp8_f32(a, b, 0, false); p = __builtin_amdgcn_cvt_pk_fp8_f32(c, d, p, true); return (unsigned)p; }
;     __device__ __forceinline__ void operator()(const f32x4 (&acc)[2][2][4][2], const Unit& u, int wr, int wc, int fr, int fq, LAS const unsigned char* tbl, LAS const unsigned char* b2l) const {
;     ...
;             for (int m = 0; m < 4; ++m) { const int row = r0 + ai * HALF + m * 16;
;                 if (u.pos0 + row < u.cnt) { const int pid = *(LAS const int*)(tbl + row * 4); const float gt = *(LAS const float*)(tbl + 1024 + row * 4) * Y_FP8_SCALE; unsigned char* rowp = Y + (size_t)pid * D_ + col0;
; #pragma unroll
;                     for (int bj = 0; bj < 2; ++bj) { const f32x4 v0 = (acc[ai][bj][m][0] * (1.0f / W_FP8_SCALE) + bv[bj][0]) * gt, v1 = (acc[ai][bj][m][1] * (1.0f / W_FP8_SCALE) + bv[bj][1]) * gt;
;                         u32x2 w; w.x = pk4_fp8(v0[0], v0[1], v0[2], v0[3]); w.y = pk4_fp8(v1[0], v1[1], v1[2], v1[3]);
;                         *(u32x2*)(rowp + bj * HALF) = w; } } }
.LBB0_1090:
	s_or_b64 exec, exec, s[0:1]
	v_add_u32_e32 v66, 0x80, v159
	v_add_u32_e32 v67, s34, v66
	v_cmp_gt_i32_e32 vcc, s33, v67
	s_and_saveexec_b64 s[0:1], vcc
	s_cbranch_execz .LBB0_1092
	v_lshl_add_u32 v66, v66, 2, s18
	ds_read2st64_b32 v[66:67], v66 offset1:4
	s_waitcnt lgkmcnt(4)
	v_pk_fma_f32 v[62:63], v[62:63], s[28:29], v[142:143] op_sel_hi:[1,0,1]
	v_pk_fma_f32 v[64:65], v[64:65], s[28:29], v[144:145] op_sel_hi:[1,0,1]
	s_waitcnt lgkmcnt(3)
	v_pk_fma_f32 v[60:61], v[60:61], s[28:29], v[140:141] op_sel_hi:[1,0,1]
	v_pk_fma_f32 v[58:59], v[58:59], s[28:29], v[138:139] op_sel_hi:[1,0,1]
	s_waitcnt lgkmcnt(0)
	v_ashrrev_i32_e32 v69, 31, v66
	v_mov_b32_e32 v68, v66
	v_mul_f32_e32 v66, 0x41800000, v67
	v_pk_mul_f32 v[62:63], v[62:63], v[66:67] op_sel_hi:[1,0]
	v_pk_mul_f32 v[64:65], v[64:65], v[66:67] op_sel_hi:[1,0]
	v_pk_mul_f32 v[60:61], v[60:61], v[66:67] op_sel_hi:[1,0]
	v_pk_mul_f32 v[58:59], v[58:59], v[66:67] op_sel_hi:[1,0]
	v_med3_f32 v67, v62, s55, v158
	v_med3_f32 v63, v63, s55, v158
	v_cvt_pk_fp8_f32 v62, v67, v63
	v_med3_f32 v58, v58, s55, v158
	v_med3_f32 v59, v59, s55, v158
	v_cvt_pk_fp8_f32 v63, v58, v59
	v_pk_fma_f32 v[54:55], v[54:55], s[28:29], v[130:131] op_sel_hi:[1,0,1]
	v_med3_f32 v58, v60, s55, v158
	v_med3_f32 v59, v61, s55, v158
	v_pk_mul_f32 v[54:55], v[54:55], v[66:67] op_sel_hi:[1,0]
	v_pk_fma_f32 v[50:51], v[50:51], s[28:29], v[126:127] op_sel_hi:[1,0,1]
	v_cvt_pk_fp8_f32 v63, v58, v59 op_sel:[0,0,1]
	v_pk_mul_f32 v[50:51], v[50:51], v[66:67] op_sel_hi:[1,0]
	v_med3_f32 v58, v54, s55, v158
	v_med3_f32 v55, v55, s55, v158
	v_cvt_pk_fp8_f32 v54, v58, v55
	v_med3_f32 v50, v50, s55, v158
	v_med3_f32 v51, v51, s55, v158
	v_cvt_pk_fp8_f32 v55, v50, v51
	v_pk_fma_f32 v[56:57], v[56:57], s[28:29], v[132:133] op_sel_hi:[1,0,1]
	v_pk_fma_f32 v[52:53], v[52:53], s[28:29], v[128:129] op_sel_hi:[1,0,1]
	v_med3_f32 v64, v64, s55, v158
	v_med3_f32 v65, v65, s55, v158
	v_pk_mul_f32 v[56:57], v[56:57], v[66:67] op_sel_hi:[1,0]
	v_pk_mul_f32 v[52:53], v[52:53], v[66:67] op_sel_hi:[1,0]
	v_cvt_pk_fp8_f32 v62, v64, v65 op_sel:[0,0,1]
	v_med3_f32 v56, v56, s55, v158
	v_med3_f32 v57, v57, s55, v158
	v_med3_f32 v50, v52, s55, v158
	v_med3_f32 v51, v53, s55, v158
	v_cvt_pk_fp8_f32 v54, v56, v57 op_sel:[0,0,1]
	v_cvt_pk_fp8_f32 v55, v50, v51 op_sel:[0,0,1]
	v_lshlrev_b64 v[50:51], 11, v[68:69]
	v_lshl_add_u64 v[50:51], v[146:147], 0, v[50:51]
	global_store_dwordx2 v[50:51], v[62:63], off
	global_store_dwordx2 v[50:51], v[54:55], off offset:128
.LBB0_1092:
	s_or_b64 exec, exec, s[0:1]
	v_add_u32_e32 v50, 0x90, v159
	v_add_u32_e32 v51, s34, v50
	v_cmp_gt_i32_e32 vcc, s33, v51
	s_and_saveexec_b64 s[0:1], vcc
	s_cbranch_execz .LBB0_1094
	v_lshl_add_u32 v50, v50, 2, s18
	ds_read2st64_b32 v[50:51], v50 offset1:4
	s_waitcnt lgkmcnt(4)
	v_pk_fma_f32 v[46:47], v[46:47], s[28:29], v[142:143] op_sel_hi:[1,0,1]
	v_pk_fma_f32 v[48:49], v[48:49], s[28:29], v[144:145] op_sel_hi:[1,0,1]
	s_waitcnt lgkmcnt(3)
	v_pk_fma_f32 v[44:45], v[44:45], s[28:29], v[140:141] op_sel_hi:[1,0,1]
	v_pk_fma_f32 v[42:43], v[42:43], s[28:29], v[138:139] op_sel_hi:[1,0,1]
	s_waitcnt lgkmcnt(0)
	v_ashrrev_i32_e32 v53, 31, v50
	v_mov_b32_e32 v52, v50
	v_mul_f32_e32 v50, 0x41800000, v51
	v_pk_mul_f32 v[46:47], v[46:47], v[50:51] op_sel_hi:[1,0]
	v_pk_mul_f32 v[48:49], v[48:49], v[50:51] op_sel_hi:[1,0]
	v_pk_mul_f32 v[44:45], v[44:45], v[50:51] op_sel_hi:[1,0]
	v_pk_mul_f32 v[42:43], v[42:43], v[50:51] op_sel_hi:[1,0]
	v_med3_f32 v51, v46, s55, v158
	v_med3_f32 v47, v47, s55, v158
	v_cvt_pk_fp8_f32 v46, v51, v47
	v_med3_f32 v42, v42, s55, v158
	v_med3_f32 v43, v43, s55, v158
	v_cvt_pk_fp8_f32 v47, v42, v43
	v_pk_fma_f32 v[30:31], v[30:31], s[28:29], v[130:131] op_sel_hi:[1,0,1]
	v_med3_f32 v42, v44, s55, v158
	v_med3_f32 v43, v45, s55, v158
	v_pk_mul_f32 v[30:31], v[30:31], v[50:51] op_sel_hi:[1,0]
	v_pk_fma_f32 v[26:27], v[26:27], s[28:29], v[126:127] op_sel_hi:[1,0,1]
	v_cvt_pk_fp8_f32 v47, v42, v43 op_sel:[0,0,1]
	v_pk_mul_f32 v[26:27], v[26:27], v[50:51] op_sel_hi:[1,0]
	v_med3_f32 v42, v30, s55, v158
	v_med3_f32 v31, v31, s55, v158
	v_cvt_pk_fp8_f32 v30, v42, v31
	v_med3_f32 v26, v26, s55, v158
	v_med3_f32 v27, v27, s55, v158
	v_cvt_pk_fp8_f32 v31, v26, v27
	v_pk_fma_f32 v[32:33], v[32:33], s[28:29], v[132:133] op_sel_hi:[1,0,1]
	v_pk_fma_f32 v[28:29], v[28:29], s[28:29], v[128:129] op_sel_hi:[1,0,1]
	v_med3_f32 v48, v48, s55, v158
	v_med3_f32 v49, v49, s55, v158
	v_pk_mul_f32 v[32:33], v[32:33], v[50:51] op_sel_hi:[1,0]
	v_pk_mul_f32 v[28:29], v[28:29], v[50:51] op_sel_hi:[1,0]
	v_cvt_pk_fp8_f32 v46, v48, v49 op_sel:[0,0,1]
	v_med3_f32 v32, v32, s55, v158
	v_med3_f32 v33, v33, s55, v158
	v_med3_f32 v26, v28, s55, v158
	v_med3_f32 v27, v29, s55, v158
	v_cvt_pk_fp8_f32 v30, v32, v33 op_sel:[0,0,1]
	v_cvt_pk_fp8_f32 v31, v26, v27 op_sel:[0,0,1]
	v_lshlrev_b64 v[26:27], 11, v[52:53]
	v_lshl_add_u64 v[26:27], v[146:147], 0, v[26:27]
	global_store_dwordx2 v[26:27], v[46:47], off
	global_store_dwordx2 v[26:27], v[30:31], off offset:128
; #define LAS __attribute__((address_space(3)))
; __device__ __forceinline__ unsigned pk4_fp8(float a, float b, float c, float d) {
;     a = fminf(fmaxf(a, -448.f), 448.f); b = fminf(fmaxf(b, -448.f), 448.f); c = fminf(fmaxf(c, -448.f), 448.f); d = fminf(fmaxf(d, -448.f), 448.f);
;     int p = __builtin_amdgcn_cvt_pk_fp8_f32(a, b, 0, false); p = __builtin_amdgcn_cvt_pk_fp8_f32(c, d, p, true); return (unsigned)p; }
;     __device__ __forceinline__ void operator()(const f32x4 (&acc)[2][2][4][2], const Unit& u, int wr, int wc, int fr, int fq, LAS const unsigned char* tbl, LAS const unsigned char* b2l) const {
;     ...
;             for (int m = 0; m < 4; ++m) { const int row = r0 + ai * HALF + m * 16;
;                 if (u.pos0 + row < u.cnt) { const int pid = *(LAS const int*)(tbl + row * 4); const float gt = *(LAS const float*)(tbl + 1024 + row * 4) * Y_FP8_SCALE; unsigned char* rowp = Y + (size_t)pid * D_ + col0;
; #pragma unroll
;                     for (int bj = 0; bj < 2; ++bj) { const f32x4 v0 = (acc[ai][bj][m][0] * (1.0f / W_FP8_SCALE) + bv[bj][0]) * gt, v1 = (acc[ai][bj][m][1] * (1.0f / W_FP8_SCALE) + bv[bj][1]) * gt;
;                         u32x2 w; w.x = pk4_fp8(v0[0], v0[1], v0[2], v0[3]); w.y = pk4_fp8(v1[0], v1[1], v1[2], v1[3]);
;                         *(u32x2*)(rowp + bj * HALF) = w; } } }
.LBB0_1094:
	s_or_b64 exec, exec, s[0:1]
	v_add_u32_e32 v26, 0xa0, v159
	v_add_u32_e32 v27, s34, v26
	v_cmp_gt_i32_e32 vcc, s33, v27
	s_and_saveexec_b64 s[0:1], vcc
	s_cbranch_execz .LBB0_1096
	v_lshl_add_u32 v26, v26, 2, s18
	ds_read2st64_b32 v[26:27], v26 offset1:4
	s_waitcnt lgkmcnt(4)
	v_pk_fma_f32 v[22:23], v[22:23], s[28:29], v[142:143] op_sel_hi:[1,0,1]
	v_pk_fma_f32 v[24:25], v[24:25], s[28:29], v[144:145] op_sel_hi:[1,0,1]
	s_waitcnt lgkmcnt(3)
	v_pk_fma_f32 v[20:21], v[20:21], s[28:29], v[140:141] op_sel_hi:[1,0,1]
	v_pk_fma_f32 v[18:19], v[18:19], s[28:29], v[138:139] op_sel_hi:[1,0,1]
	s_waitcnt lgkmcnt(0)
	v_ashrrev_i32_e32 v29, 31, v26
	v_mov_b32_e32 v28, v26
	v_mul_f32_e32 v26, 0x41800000, v27
	v_pk_mul_f32 v[22:23], v[22:23], v[26:27] op_sel_hi:[1,0]
	v_pk_mul_f32 v[24:25], v[24:25], v[26:27] op_sel_hi:[1,0]
	v_pk_mul_f32 v[20:21], v[20:21], v[26:27] op_sel_hi:[1,0]
	v_pk_mul_f32 v[18:19], v[18:19], v[26:27] op_sel_hi:[1,0]
	v_med3_f32 v27, v22, s55, v158
	v_med3_f32 v23, v23, s55, v158
	v_cvt_pk_fp8_f32 v22, v27, v23
	v_med3_f32 v18, v18, s55, v158
	v_med3_f32 v19, v19, s55, v158
	v_cvt_pk_fp8_f32 v23, v18, v19
	v_med3_f32 v18, v20, s55, v158
	v_med3_f32 v19, v21, s55, v158
	v_med3_f32 v24, v24, s55, v158
	v_med3_f32 v25, v25, s55, v158
	v_cvt_pk_fp8_f32 v23, v18, v19 op_sel:[0,0,1]
	v_pk_fma_f32 v[18:19], v[40:41], s[28:29], v[132:133] op_sel_hi:[1,0,1]
	v_pk_fma_f32 v[20:21], v[38:39], s[28:29], v[130:131] op_sel_hi:[1,0,1]
	v_cvt_pk_fp8_f32 v22, v24, v25 op_sel:[0,0,1]
	v_pk_mul_f32 v[18:19], v[18:19], v[26:27] op_sel_hi:[1,0]
	v_pk_mul_f32 v[20:21], v[20:21], v[26:27] op_sel_hi:[1,0]
	v_pk_fma_f32 v[24:25], v[36:37], s[28:29], v[128:129] op_sel_hi:[1,0,1]
	v_pk_fma_f32 v[30:31], v[34:35], s[28:29], v[126:127] op_sel_hi:[1,0,1]
	v_pk_mul_f32 v[24:25], v[24:25], v[26:27] op_sel_hi:[1,0]
	v_pk_mul_f32 v[26:27], v[30:31], v[26:27] op_sel_hi:[1,0]
	v_med3_f32 v20, v20, s55, v158
	v_med3_f32 v21, v21, s55, v158
	v_med3_f32 v30, v18, s55, v158
	v_med3_f32 v31, v19, s55, v158
	v_cvt_pk_fp8_f32 v18, v20, v21
	v_med3_f32 v20, v26, s55, v158
	v_med3_f32 v21, v27, s55, v158
	v_cvt_pk_fp8_f32 v19, v20, v21
	v_med3_f32 v20, v24, s55, v158
	v_med3_f32 v21, v25, s55, v158
	v_cvt_pk_fp8_f32 v18, v30, v31 op_sel:[0,0,1]
	v_cvt_pk_fp8_f32 v19, v20, v21 op_sel:[0,0,1]
	v_lshlrev_b64 v[20:21], 11, v[28:29]
	v_lshl_add_u64 v[20:21], v[146:147], 0, v[20:21]
	global_store_dwordx2 v[20:21], v[22:23], off
	global_store_dwordx2 v[20:21], v[18:19], off offset:128
.LBB0_1096:
	s_or_b64 exec, exec, s[0:1]
	v_add_u32_e32 v18, 0xb0, v159
	v_add_u32_e32 v19, s34, v18
	v_cmp_gt_i32_e32 vcc, s33, v19
	s_and_saveexec_b64 s[0:1], vcc
	s_cbranch_execz .LBB0_1070
	v_lshl_add_u32 v18, v18, 2, s18
	ds_read2st64_b32 v[18:19], v18 offset1:4
	s_waitcnt lgkmcnt(4)
	v_pk_fma_f32 v[6:7], v[6:7], s[28:29], v[142:143] op_sel_hi:[1,0,1]
	v_pk_fma_f32 v[8:9], v[8:9], s[28:29], v[144:145] op_sel_hi:[1,0,1]
	s_waitcnt lgkmcnt(3)
	v_pk_fma_f32 v[4:5], v[4:5], s[28:29], v[140:141] op_sel_hi:[1,0,1]
	v_pk_fma_f32 v[2:3], v[2:3], s[28:29], v[138:139] op_sel_hi:[1,0,1]
	s_waitcnt lgkmcnt(0)
	v_ashrrev_i32_e32 v21, 31, v18
	v_mov_b32_e32 v20, v18
	v_mul_f32_e32 v18, 0x41800000, v19
	v_pk_mul_f32 v[6:7], v[6:7], v[18:19] op_sel_hi:[1,0]
	v_pk_mul_f32 v[8:9], v[8:9], v[18:19] op_sel_hi:[1,0]
	v_pk_mul_f32 v[4:5], v[4:5], v[18:19] op_sel_hi:[1,0]
	v_pk_mul_f32 v[2:3], v[2:3], v[18:19] op_sel_hi:[1,0]
	v_med3_f32 v19, v6, s55, v158
	v_med3_f32 v7, v7, s55, v158
	v_cvt_pk_fp8_f32 v6, v19, v7
	v_med3_f32 v2, v2, s55, v158
	v_med3_f32 v3, v3, s55, v158
	v_cvt_pk_fp8_f32 v7, v2, v3
	v_med3_f32 v2, v4, s55, v158
	v_med3_f32 v3, v5, s55, v158
	v_pk_fma_f32 v[4:5], v[14:15], s[28:29], v[130:131] op_sel_hi:[1,0,1]
	v_cvt_pk_fp8_f32 v7, v2, v3 op_sel:[0,0,1]
	v_pk_fma_f32 v[2:3], v[16:17], s[28:29], v[132:133] op_sel_hi:[1,0,1]
	v_med3_f32 v8, v8, s55, v158
	v_med3_f32 v9, v9, s55, v158
	v_pk_mul_f32 v[2:3], v[2:3], v[18:19] op_sel_hi:[1,0]
	v_pk_mul_f32 v[4:5], v[4:5], v[18:19] op_sel_hi:[1,0]
	v_pk_fma_f32 v[10:11], v[10:11], s[28:29], v[126:127] op_sel_hi:[1,0,1]
	v_cvt_pk_fp8_f32 v6, v8, v9 op_sel:[0,0,1]
	v_pk_fma_f32 v[8:9], v[12:13], s[28:29], v[128:129] op_sel_hi:[1,0,1]
	v_pk_mul_f32 v[10:11], v[10:11], v[18:19] op_sel_hi:[1,0]
	v_med3_f32 v4, v4, s55, v158
	v_med3_f32 v5, v5, s55, v158
	v_med3_f32 v12, v2, s55, v158
	v_med3_f32 v13, v3, s55, v158
	v_cvt_pk_fp8_f32 v2, v4, v5
	v_med3_f32 v4, v10, s55, v158
	v_med3_f32 v5, v11, s55, v158
	v_cvt_pk_fp8_f32 v3, v4, v5
	v_pk_mul_f32 v[8:9], v[8:9], v[18:19] op_sel_hi:[1,0]
	v_cvt_pk_fp8_f32 v2, v12, v13 op_sel:[0,0,1]
	v_med3_f32 v4, v8, s55, v158
	v_med3_f32 v5, v9, s55, v158
	v_cvt_pk_fp8_f32 v3, v4, v5 op_sel:[0,0,1]
	v_lshlrev_b64 v[4:5], 11, v[20:21]
	v_lshl_add_u64 v[4:5], v[146:147], 0, v[4:5]
	global_store_dwordx2 v[4:5], v[6:7], off
	global_store_dwordx2 v[4:5], v[2:3], off offset:128
	s_branch .LBB0_1070
